# baseline (speedup 1.0000x reference)
_Z4k_k2ILb0EEvPKDF16_S1_PKfS3_S3_S1_S1_PfS3_S3_S1_PDF16_PKiS4_S4_:
	s_load_dwordx2 s[24:25], s[0:1], 0x58
	s_load_dwordx8 s[4:11], s[0:1], 0x38
	s_load_dwordx4 s[20:23], s[0:1], 0x0
	s_load_dwordx8 s[12:19], s[0:1], 0x18
	s_load_dwordx2 s[54:55], s[0:1], 0x10
	s_lshl_b32 s3, s2, 5
	s_and_b32 s3, s3, 0xe0
	s_lshr_b32 s26, s2, 3
	s_or_b32 s3, s3, s26
	s_movk_i32 s26, 0x100
	s_lshl_b32 s28, s3, 5
	v_cmp_gt_u32_e32 vcc, s26, v0
	v_mov_b32_e32 v67, 0
	v_lshlrev_b32_e32 v66, 4, v0
	s_lshl_b32 s0, s3, 1
	s_and_b32 s26, s0, 0xffffffe
	s_mov_b32 s27, 0
	s_waitcnt lgkmcnt(0)
	v_lshl_add_u64 v[2:3], s[16:17], 0, v[66:67]
	s_lshl_b64 s[0:1], s[26:27], 13
	s_or_b32 s26, s26, 1
	v_lshl_add_u64 v[4:5], v[2:3], 0, s[0:1]
	s_lshl_b64 s[0:1], s[26:27], 13
	v_lshl_add_u64 v[2:3], v[2:3], 0, s[0:1]
	global_load_dwordx4 v[68:71], v[4:5], off
	global_load_dwordx4 v[72:75], v[2:3], off
	v_lshl_add_u64 v[2:3], s[12:13], 0, v[66:67]
	s_movk_i32 s29, 0x2000
	v_add_co_u32_e32 v4, vcc, s29, v2
	s_movk_i32 s52, 0x4000
	s_nop 0
	v_addc_co_u32_e32 v5, vcc, 0, v3, vcc
	v_add_co_u32_e32 v18, vcc, s52, v2
	s_movk_i32 s33, 0x6000
	s_nop 0
	v_addc_co_u32_e32 v19, vcc, 0, v3, vcc
	s_lshl_b32 s26, s3, 2
	global_load_dwordx4 v[14:17], v66, s[12:13]
	global_load_dwordx4 v[10:13], v[4:5], off
	global_load_dwordx4 v[6:9], v[18:19], off
	v_add_co_u32_e32 v18, vcc, s33, v2
	s_add_u32 s0, s24, 0x800000
	s_nop 0
	v_addc_co_u32_e32 v19, vcc, 0, v3, vcc
	s_addc_u32 s1, s25, 0
	s_lshl_b64 s[12:13], s[26:27], 13
	v_lshlrev_b32_e32 v20, 2, v0
	global_load_dwordx4 v[2:5], v[18:19], off
	global_load_dword v1, v20, s[14:15]
	v_or_b32_e32 v18, s12, v66
	v_mov_b32_e32 v19, s13
	s_or_b32 s12, s26, 1
	s_mov_b32 s13, s27
	s_lshl_b64 s[12:13], s[12:13], 13
	v_lshl_add_u64 v[76:77], s[22:23], 0, v[18:19]
	v_lshl_add_u64 v[78:79], s[20:21], 0, v[18:19]
	v_lshl_add_u64 v[80:81], s[0:1], 0, v[18:19]
	v_or_b32_e32 v18, s12, v66
	v_mov_b32_e32 v19, s13
	s_or_b32 s12, s26, 2
	s_mov_b32 s13, s27
	s_lshl_b64 s[12:13], s[12:13], 13
	s_or_b32 s26, s26, 3
	v_lshl_add_u64 v[82:83], s[22:23], 0, v[18:19]
	v_lshl_add_u64 v[84:85], s[20:21], 0, v[18:19]
	v_lshl_add_u64 v[86:87], s[0:1], 0, v[18:19]
	v_or_b32_e32 v18, s12, v66
	v_mov_b32_e32 v19, s13
	s_lshl_b64 s[12:13], s[26:27], 13
	v_lshl_add_u64 v[88:89], s[22:23], 0, v[18:19]
	v_lshl_add_u64 v[90:91], s[20:21], 0, v[18:19]
	v_lshl_add_u64 v[92:93], s[0:1], 0, v[18:19]
	v_or_b32_e32 v18, s12, v66
	v_mov_b32_e32 v19, s13
	v_lshl_add_u64 v[94:95], s[22:23], 0, v[18:19]
	v_lshl_add_u64 v[96:97], s[20:21], 0, v[18:19]
	v_lshl_add_u64 v[98:99], s[0:1], 0, v[18:19]
	global_load_dwordx4 v[62:65], v[76:77], off
	global_load_dwordx4 v[54:57], v[78:79], off
	global_load_dwordx4 v[58:61], v[80:81], off
	v_mov_b64_e32 v[212:213], v[82:83]
	v_mov_b64_e32 v[214:215], v[84:85]
	v_mov_b64_e32 v[216:217], v[86:87]
	v_mov_b64_e32 v[218:219], v[88:89]
	v_mov_b64_e32 v[220:221], v[90:91]
	v_mov_b64_e32 v[222:223], v[92:93]
	v_mov_b64_e32 v[224:225], v[94:95]
	v_mov_b64_e32 v[226:227], v[96:97]
	v_mov_b64_e32 v[228:229], v[98:99]
	s_lshl_b32 s30, s28, 7
	s_add_u32 s54, s54, s30
	s_addc_u32 s55, s55, 0
	s_load_dwordx16 s[36:51], s[54:55], 0x0
	s_load_dwordx16 s[72:87], s[54:55], 0x40
	s_load_dwordx16 s[56:71], s[54:55], 0x80
	s_load_dwordx8 s[88:95], s[54:55], 0xc0
	s_load_dwordx4 s[96:99], s[54:55], 0xe0
	s_load_dwordx4 s[20:23], s[54:55], 0xf0
	v_lshrrev_b32_e32 v196, 6, v0
	s_nop 1
	v_readfirstlane_b32 s16, v196
	s_nop 3
	s_lshl_b32 s16, s16, 9
	s_add_u32 s16, s54, s16
	s_addc_u32 s17, s55, 0
	s_load_dword s30, s[16:17], 0x0
	s_load_dword s30, s[16:17], 0x40
	s_load_dword s30, s[16:17], 0x80
	s_load_dword s30, s[16:17], 0xc0
	s_load_dword s30, s[16:17], 0x100
	s_load_dword s30, s[16:17], 0x140
	s_load_dword s30, s[16:17], 0x180
	s_load_dword s30, s[16:17], 0x1c0
	s_waitcnt vmcnt(9)
	v_cvt_f32_f16_e32 v134, v68
	v_cvt_f32_f16_sdwa v135, v68 dst_sel:DWORD dst_unused:UNUSED_PAD src0_sel:WORD_1
	v_cvt_f32_f16_e32 v136, v69
	v_cvt_f32_f16_sdwa v137, v69 dst_sel:DWORD dst_unused:UNUSED_PAD src0_sel:WORD_1
	v_cvt_f32_f16_e32 v138, v70
	v_cvt_f32_f16_sdwa v139, v70 dst_sel:DWORD dst_unused:UNUSED_PAD src0_sel:WORD_1
	v_cvt_f32_f16_e32 v140, v71
	v_cvt_f32_f16_sdwa v141, v71 dst_sel:DWORD dst_unused:UNUSED_PAD src0_sel:WORD_1
	s_waitcnt vmcnt(8)
	v_cvt_f32_f16_e32 v142, v72
	v_cvt_f32_f16_sdwa v143, v72 dst_sel:DWORD dst_unused:UNUSED_PAD src0_sel:WORD_1
	v_cvt_f32_f16_e32 v144, v73
	v_cvt_f32_f16_sdwa v145, v73 dst_sel:DWORD dst_unused:UNUSED_PAD src0_sel:WORD_1
	v_cvt_f32_f16_e32 v146, v74
	v_cvt_f32_f16_sdwa v147, v74 dst_sel:DWORD dst_unused:UNUSED_PAD src0_sel:WORD_1
	v_cvt_f32_f16_e32 v148, v75
	v_cvt_f32_f16_sdwa v149, v75 dst_sel:DWORD dst_unused:UNUSED_PAD src0_sel:WORD_1
	s_waitcnt lgkmcnt(0)
	v_lshlrev_b32_e32 v68, 1, v0
	s_waitcnt vmcnt(2)
	v_cvt_f32_f16_e32 v150, v62
	s_waitcnt vmcnt(1)
	v_cvt_f32_f16_e32 v69, v54
	v_pk_mul_f32 v[154:155], v[150:151], v[14:15] op_sel_hi:[0,1]
	v_exp_f32_e32 v154, v154
	v_exp_f32_e32 v155, v155
	v_pk_mul_f32 v[156:157], v[150:151], v[16:17] op_sel_hi:[0,1]
	v_exp_f32_e32 v156, v156
	v_exp_f32_e32 v157, v157
	v_mul_f32_e32 v152, v150, v69
	v_pk_mul_f32 v[134:135], v[154:155], v[134:135]
	v_pk_fma_f32 v[134:135], v[152:153], s[36:37], v[134:135] op_sel_hi:[0, 1, 1]
	v_pk_fma_f32 v[70:71], s[72:73], v[134:135], 0 op_sel_hi:[1, 1, 0]
	v_pk_mul_f32 v[86:87], v[156:157], v[136:137]
	s_nop 0
	v_pk_fma_f32 v[136:137], v[152:153], s[38:39], v[86:87] op_sel_hi:[0, 1, 1]
	v_pk_mul_f32 v[72:73], v[150:151], v[10:11] op_sel_hi:[0,1]
	v_exp_f32_e32 v72, v72
	v_exp_f32_e32 v73, v73
	v_pk_mul_f32 v[86:87], v[150:151], v[12:13] op_sel_hi:[0,1]
	v_exp_f32_e32 v86, v86
	v_exp_f32_e32 v87, v87
	v_pk_mul_f32 v[72:73], v[72:73], v[138:139]
	v_pk_fma_f32 v[70:71], s[74:75], v[136:137], v[70:71]
	v_pk_fma_f32 v[138:139], v[152:153], s[40:41], v[72:73] op_sel_hi:[0, 1, 1]
	v_pk_mul_f32 v[72:73], v[86:87], v[140:141]
	v_pk_mul_f32 v[74:75], v[150:151], v[8:9] op_sel_hi:[0,1]
	v_pk_fma_f32 v[140:141], v[152:153], s[42:43], v[72:73] op_sel_hi:[0, 1, 1]
	v_pk_mul_f32 v[72:73], v[150:151], v[6:7] op_sel_hi:[0,1]
	v_exp_f32_e32 v72, v72
	v_exp_f32_e32 v73, v73
	v_exp_f32_e32 v74, v74
	v_exp_f32_e32 v75, v75
	v_pk_fma_f32 v[70:71], s[76:77], v[138:139], v[70:71]
	v_pk_mul_f32 v[72:73], v[72:73], v[142:143]
	v_pk_fma_f32 v[70:71], s[78:79], v[140:141], v[70:71]
	v_pk_fma_f32 v[142:143], v[152:153], s[44:45], v[72:73] op_sel_hi:[0, 1, 1]
	v_pk_mul_f32 v[72:73], v[74:75], v[144:145]
	v_pk_mul_f32 v[74:75], v[150:151], v[4:5] op_sel_hi:[0,1]
	v_pk_fma_f32 v[144:145], v[152:153], s[46:47], v[72:73] op_sel_hi:[0, 1, 1]
	v_pk_mul_f32 v[72:73], v[150:151], v[2:3] op_sel_hi:[0,1]
	v_exp_f32_e32 v72, v72
	v_exp_f32_e32 v73, v73
	v_exp_f32_e32 v74, v74
	v_exp_f32_e32 v75, v75
	v_pk_fma_f32 v[70:71], s[80:81], v[142:143], v[70:71]
	v_pk_mul_f32 v[72:73], v[72:73], v[146:147]
	v_pk_fma_f32 v[70:71], s[82:83], v[144:145], v[70:71]
	v_pk_fma_f32 v[146:147], v[152:153], s[48:49], v[72:73] op_sel_hi:[0, 1, 1]
	v_pk_mul_f32 v[72:73], v[74:75], v[148:149]
	v_pk_fma_f32 v[70:71], s[84:85], v[146:147], v[70:71]
	v_pk_fma_f32 v[148:149], v[152:153], s[50:51], v[72:73] op_sel_hi:[0, 1, 1]
	v_pk_fma_f32 v[70:71], s[86:87], v[148:149], v[70:71]
	s_nop 0
	v_add_f32_e32 v69, v70, v71
	v_fma_mix_f32 v69, v1, v54, v69 op_sel_hi:[0,1,0]
	s_waitcnt vmcnt(0)
	v_fma_mixlo_f16 v69, v69, v58, 0 op_sel_hi:[0,1,0]
	ds_write_b16 v68, v69 offset:4096
	global_load_dwordx4 v[50:53], v[212:213], off
	global_load_dwordx4 v[42:45], v[214:215], off
	global_load_dwordx4 v[46:49], v[216:217], off
	global_load_dwordx4 v[38:41], v[218:219], off
	global_load_dwordx4 v[30:33], v[220:221], off
	global_load_dwordx4 v[34:37], v[222:223], off
	global_load_dwordx4 v[26:29], v[224:225], off
	global_load_dwordx4 v[18:21], v[226:227], off
	global_load_dwordx4 v[22:25], v[228:229], off
	s_waitcnt lgkmcnt(0)
	s_load_dwordx16 s[36:51], s[54:55], 0x100
	s_load_dwordx16 s[72:87], s[54:55], 0x140
	v_cvt_f32_f16_sdwa v62, v62 dst_sel:DWORD dst_unused:UNUSED_PAD src0_sel:WORD_1
	v_cvt_f32_f16_sdwa v69, v54 dst_sel:DWORD dst_unused:UNUSED_PAD src0_sel:WORD_1
	v_pk_mul_f32 v[152:153], v[62:63], v[14:15] op_sel_hi:[0,1]
	v_exp_f32_e32 v152, v152
	v_exp_f32_e32 v153, v153
	v_pk_mul_f32 v[154:155], v[62:63], v[16:17] op_sel_hi:[0,1]
	v_exp_f32_e32 v154, v154
	v_exp_f32_e32 v155, v155
	v_mul_f32_e32 v150, v62, v69
	v_pk_mul_f32 v[134:135], v[152:153], v[134:135]
	v_pk_fma_f32 v[134:135], v[150:151], s[56:57], v[134:135] op_sel_hi:[0, 1, 1]
	v_pk_fma_f32 v[102:103], s[88:89], v[134:135], 0 op_sel_hi:[1, 1, 0]
	v_pk_mul_f32 v[118:119], v[154:155], v[136:137]
	s_nop 0
	v_pk_fma_f32 v[136:137], v[150:151], s[58:59], v[118:119] op_sel_hi:[0, 1, 1]
	v_pk_mul_f32 v[104:105], v[62:63], v[10:11] op_sel_hi:[0,1]
	v_exp_f32_e32 v104, v104
	v_exp_f32_e32 v105, v105
	v_pk_mul_f32 v[118:119], v[62:63], v[12:13] op_sel_hi:[0,1]
	v_exp_f32_e32 v118, v118
	v_exp_f32_e32 v119, v119
	v_pk_mul_f32 v[104:105], v[104:105], v[138:139]
	v_pk_fma_f32 v[102:103], s[90:91], v[136:137], v[102:103]
	v_pk_fma_f32 v[138:139], v[150:151], s[60:61], v[104:105] op_sel_hi:[0, 1, 1]
	v_pk_mul_f32 v[104:105], v[118:119], v[140:141]
	v_pk_mul_f32 v[106:107], v[62:63], v[8:9] op_sel_hi:[0,1]
	v_pk_fma_f32 v[140:141], v[150:151], s[62:63], v[104:105] op_sel_hi:[0, 1, 1]
	v_pk_mul_f32 v[104:105], v[62:63], v[6:7] op_sel_hi:[0,1]
	v_exp_f32_e32 v104, v104
	v_exp_f32_e32 v105, v105
	v_exp_f32_e32 v106, v106
	v_exp_f32_e32 v107, v107
	v_pk_fma_f32 v[102:103], s[92:93], v[138:139], v[102:103]
	v_pk_mul_f32 v[104:105], v[104:105], v[142:143]
	v_pk_fma_f32 v[102:103], s[94:95], v[140:141], v[102:103]
	v_pk_fma_f32 v[142:143], v[150:151], s[64:65], v[104:105] op_sel_hi:[0, 1, 1]
	v_pk_mul_f32 v[104:105], v[106:107], v[144:145]
	v_pk_mul_f32 v[106:107], v[62:63], v[4:5] op_sel_hi:[0,1]
	v_pk_fma_f32 v[144:145], v[150:151], s[66:67], v[104:105] op_sel_hi:[0, 1, 1]
	v_pk_mul_f32 v[104:105], v[62:63], v[2:3] op_sel_hi:[0,1]
	v_exp_f32_e32 v104, v104
	v_exp_f32_e32 v105, v105
	v_exp_f32_e32 v106, v106
	v_exp_f32_e32 v107, v107
	v_pk_fma_f32 v[102:103], s[96:97], v[142:143], v[102:103]
	v_pk_mul_f32 v[104:105], v[104:105], v[146:147]
	v_pk_fma_f32 v[102:103], s[98:99], v[144:145], v[102:103]
	v_pk_fma_f32 v[146:147], v[150:151], s[68:69], v[104:105] op_sel_hi:[0, 1, 1]
	v_pk_mul_f32 v[104:105], v[106:107], v[148:149]
	v_pk_fma_f32 v[102:103], s[20:21], v[146:147], v[102:103]
	v_pk_fma_f32 v[148:149], v[150:151], s[70:71], v[104:105] op_sel_hi:[0, 1, 1]
	v_pk_fma_f32 v[102:103], s[22:23], v[148:149], v[102:103]
	s_nop 0
	v_add_f32_e32 v62, v102, v103
	v_fma_mix_f32 v54, v1, v54, v62 op_sel:[0,1,0] op_sel_hi:[0,1,0]
	v_fma_mixlo_f16 v54, v54, v58, 0 op_sel:[0,1,0] op_sel_hi:[0,1,0]
	ds_write_b16 v68, v54 offset:5136
	s_waitcnt lgkmcnt(0)
	s_load_dwordx16 s[56:71], s[54:55], 0x180
	s_load_dwordx8 s[88:95], s[54:55], 0x1c0
	s_load_dwordx4 s[96:99], s[54:55], 0x1e0
	s_load_dwordx4 s[20:23], s[54:55], 0x1f0
	v_cvt_f32_f16_e32 v54, v63
	v_cvt_f32_f16_e32 v58, v55
	v_pk_mul_f32 v[150:151], v[54:55], v[14:15] op_sel_hi:[0,1]
	v_exp_f32_e32 v150, v150
	v_exp_f32_e32 v151, v151
	v_pk_mul_f32 v[152:153], v[54:55], v[16:17] op_sel_hi:[0,1]
	v_exp_f32_e32 v152, v152
	v_exp_f32_e32 v153, v153
	v_mul_f32_e32 v58, v54, v58
	v_pk_mul_f32 v[134:135], v[150:151], v[134:135]
	v_pk_fma_f32 v[134:135], v[58:59], s[36:37], v[134:135] op_sel_hi:[0, 1, 1]
	v_pk_fma_f32 v[70:71], s[72:73], v[134:135], 0 op_sel_hi:[1, 1, 0]
	v_pk_mul_f32 v[86:87], v[152:153], v[136:137]
	s_nop 0
	v_pk_fma_f32 v[136:137], v[58:59], s[38:39], v[86:87] op_sel_hi:[0, 1, 1]
	v_pk_mul_f32 v[72:73], v[54:55], v[10:11] op_sel_hi:[0,1]
	v_exp_f32_e32 v72, v72
	v_exp_f32_e32 v73, v73
	v_pk_mul_f32 v[86:87], v[54:55], v[12:13] op_sel_hi:[0,1]
	v_exp_f32_e32 v86, v86
	v_exp_f32_e32 v87, v87
	v_pk_mul_f32 v[72:73], v[72:73], v[138:139]
	v_pk_fma_f32 v[70:71], s[74:75], v[136:137], v[70:71]
	v_pk_fma_f32 v[138:139], v[58:59], s[40:41], v[72:73] op_sel_hi:[0, 1, 1]
	v_pk_mul_f32 v[72:73], v[86:87], v[140:141]
	v_pk_mul_f32 v[74:75], v[54:55], v[8:9] op_sel_hi:[0,1]
	v_pk_fma_f32 v[140:141], v[58:59], s[42:43], v[72:73] op_sel_hi:[0, 1, 1]
	v_pk_mul_f32 v[72:73], v[54:55], v[6:7] op_sel_hi:[0,1]
	v_exp_f32_e32 v72, v72
	v_exp_f32_e32 v73, v73
	v_exp_f32_e32 v74, v74
	v_exp_f32_e32 v75, v75
	v_pk_fma_f32 v[70:71], s[76:77], v[138:139], v[70:71]
	v_pk_mul_f32 v[72:73], v[72:73], v[142:143]
	v_pk_fma_f32 v[70:71], s[78:79], v[140:141], v[70:71]
	v_pk_fma_f32 v[142:143], v[58:59], s[44:45], v[72:73] op_sel_hi:[0, 1, 1]
	v_pk_mul_f32 v[72:73], v[74:75], v[144:145]
	v_pk_mul_f32 v[74:75], v[54:55], v[4:5] op_sel_hi:[0,1]
	v_pk_fma_f32 v[144:145], v[58:59], s[46:47], v[72:73] op_sel_hi:[0, 1, 1]
	v_pk_mul_f32 v[72:73], v[54:55], v[2:3] op_sel_hi:[0,1]
	v_exp_f32_e32 v72, v72
	v_exp_f32_e32 v73, v73
	v_exp_f32_e32 v74, v74
	v_exp_f32_e32 v75, v75
	v_pk_fma_f32 v[70:71], s[80:81], v[142:143], v[70:71]
	v_pk_mul_f32 v[72:73], v[72:73], v[146:147]
	v_pk_fma_f32 v[70:71], s[82:83], v[144:145], v[70:71]
	v_pk_fma_f32 v[146:147], v[58:59], s[48:49], v[72:73] op_sel_hi:[0, 1, 1]
	v_pk_mul_f32 v[72:73], v[74:75], v[148:149]
	v_pk_fma_f32 v[70:71], s[84:85], v[146:147], v[70:71]
	v_pk_fma_f32 v[148:149], v[58:59], s[50:51], v[72:73] op_sel_hi:[0, 1, 1]
	v_pk_fma_f32 v[70:71], s[86:87], v[148:149], v[70:71]
	s_nop 0
	v_add_f32_e32 v54, v70, v71
	v_fma_mix_f32 v54, v1, v55, v54 op_sel_hi:[0,1,0]
	v_fma_mixlo_f16 v54, v54, v59, 0 op_sel_hi:[0,1,0]
	ds_write_b16 v68, v54 offset:6176
	s_waitcnt lgkmcnt(0)
	s_load_dwordx16 s[36:51], s[54:55], 0x200
	s_load_dwordx16 s[72:87], s[54:55], 0x240
	v_cvt_f32_f16_sdwa v54, v63 dst_sel:DWORD dst_unused:UNUSED_PAD src0_sel:WORD_1
	v_cvt_f32_f16_sdwa v58, v55 dst_sel:DWORD dst_unused:UNUSED_PAD src0_sel:WORD_1
	v_pk_mul_f32 v[62:63], v[54:55], v[14:15] op_sel_hi:[0,1]
	v_exp_f32_e32 v62, v62
	v_exp_f32_e32 v63, v63
	v_pk_mul_f32 v[150:151], v[54:55], v[16:17] op_sel_hi:[0,1]
	v_exp_f32_e32 v150, v150
	v_exp_f32_e32 v151, v151
	v_mul_f32_e32 v58, v54, v58
	v_pk_mul_f32 v[62:63], v[62:63], v[134:135]
	v_pk_fma_f32 v[62:63], v[58:59], s[56:57], v[62:63] op_sel_hi:[0, 1, 1]
	v_pk_fma_f32 v[102:103], s[88:89], v[62:63], 0 op_sel_hi:[1, 1, 0]
	v_pk_mul_f32 v[118:119], v[150:151], v[136:137]
	s_nop 0
	v_pk_fma_f32 v[134:135], v[58:59], s[58:59], v[118:119] op_sel_hi:[0, 1, 1]
	v_pk_mul_f32 v[104:105], v[54:55], v[10:11] op_sel_hi:[0,1]
	v_exp_f32_e32 v104, v104
	v_exp_f32_e32 v105, v105
	v_pk_mul_f32 v[118:119], v[54:55], v[12:13] op_sel_hi:[0,1]
	v_exp_f32_e32 v118, v118
	v_exp_f32_e32 v119, v119
	v_pk_mul_f32 v[104:105], v[104:105], v[138:139]
	v_pk_fma_f32 v[102:103], s[90:91], v[134:135], v[102:103]
	v_pk_fma_f32 v[136:137], v[58:59], s[60:61], v[104:105] op_sel_hi:[0, 1, 1]
	v_pk_mul_f32 v[104:105], v[118:119], v[140:141]
	v_pk_mul_f32 v[106:107], v[54:55], v[8:9] op_sel_hi:[0,1]
	v_pk_fma_f32 v[138:139], v[58:59], s[62:63], v[104:105] op_sel_hi:[0, 1, 1]
	v_pk_mul_f32 v[104:105], v[54:55], v[6:7] op_sel_hi:[0,1]
	v_exp_f32_e32 v104, v104
	v_exp_f32_e32 v105, v105
	v_exp_f32_e32 v106, v106
	v_exp_f32_e32 v107, v107
	v_pk_fma_f32 v[102:103], s[92:93], v[136:137], v[102:103]
	v_pk_mul_f32 v[104:105], v[104:105], v[142:143]
	v_pk_fma_f32 v[102:103], s[94:95], v[138:139], v[102:103]
	v_pk_fma_f32 v[140:141], v[58:59], s[64:65], v[104:105] op_sel_hi:[0, 1, 1]
	v_pk_mul_f32 v[104:105], v[106:107], v[144:145]
	v_pk_mul_f32 v[106:107], v[54:55], v[4:5] op_sel_hi:[0,1]
	v_pk_fma_f32 v[142:143], v[58:59], s[66:67], v[104:105] op_sel_hi:[0, 1, 1]
	v_pk_mul_f32 v[104:105], v[54:55], v[2:3] op_sel_hi:[0,1]
	v_exp_f32_e32 v104, v104
	v_exp_f32_e32 v105, v105
	v_exp_f32_e32 v106, v106
	v_exp_f32_e32 v107, v107
	v_pk_fma_f32 v[102:103], s[96:97], v[140:141], v[102:103]
	v_pk_mul_f32 v[104:105], v[104:105], v[146:147]
	v_pk_fma_f32 v[102:103], s[98:99], v[142:143], v[102:103]
	v_pk_fma_f32 v[144:145], v[58:59], s[68:69], v[104:105] op_sel_hi:[0, 1, 1]
	v_pk_mul_f32 v[104:105], v[106:107], v[148:149]
	v_pk_fma_f32 v[102:103], s[20:21], v[144:145], v[102:103]
	v_pk_fma_f32 v[146:147], v[58:59], s[70:71], v[104:105] op_sel_hi:[0, 1, 1]
	v_pk_fma_f32 v[102:103], s[22:23], v[146:147], v[102:103]
	s_nop 0
	v_add_f32_e32 v54, v102, v103
	v_fma_mix_f32 v54, v1, v55, v54 op_sel:[0,1,0] op_sel_hi:[0,1,0]
	v_fma_mixlo_f16 v54, v54, v59, 0 op_sel:[0,1,0] op_sel_hi:[0,1,0]
	ds_write_b16 v68, v54 offset:7216
	s_waitcnt lgkmcnt(0)
	s_load_dwordx16 s[56:71], s[54:55], 0x280
	s_load_dwordx8 s[88:95], s[54:55], 0x2c0
	s_load_dwordx4 s[96:99], s[54:55], 0x2e0
	s_load_dwordx4 s[20:23], s[54:55], 0x2f0
	v_cvt_f32_f16_e32 v54, v64
	v_cvt_f32_f16_e32 v55, v56
	v_pk_mul_f32 v[148:149], v[54:55], v[14:15] op_sel_hi:[0,1]
	v_exp_f32_e32 v148, v148
	v_exp_f32_e32 v149, v149
	v_pk_mul_f32 v[150:151], v[54:55], v[16:17] op_sel_hi:[0,1]
	v_exp_f32_e32 v150, v150
	v_exp_f32_e32 v151, v151
	v_mul_f32_e32 v58, v54, v55
	v_pk_mul_f32 v[62:63], v[148:149], v[62:63]
	v_pk_fma_f32 v[62:63], v[58:59], s[36:37], v[62:63] op_sel_hi:[0, 1, 1]
	v_pk_fma_f32 v[70:71], s[72:73], v[62:63], 0 op_sel_hi:[1, 1, 0]
	v_pk_mul_f32 v[86:87], v[150:151], v[134:135]
	s_nop 0
	v_pk_fma_f32 v[134:135], v[58:59], s[38:39], v[86:87] op_sel_hi:[0, 1, 1]
	v_pk_mul_f32 v[72:73], v[54:55], v[10:11] op_sel_hi:[0,1]
	v_exp_f32_e32 v72, v72
	v_exp_f32_e32 v73, v73
	v_pk_mul_f32 v[86:87], v[54:55], v[12:13] op_sel_hi:[0,1]
	v_exp_f32_e32 v86, v86
	v_exp_f32_e32 v87, v87
	v_pk_mul_f32 v[72:73], v[72:73], v[136:137]
	v_pk_fma_f32 v[70:71], s[74:75], v[134:135], v[70:71]
	v_pk_fma_f32 v[136:137], v[58:59], s[40:41], v[72:73] op_sel_hi:[0, 1, 1]
	v_pk_mul_f32 v[72:73], v[86:87], v[138:139]
	v_pk_mul_f32 v[74:75], v[54:55], v[8:9] op_sel_hi:[0,1]
	v_pk_fma_f32 v[138:139], v[58:59], s[42:43], v[72:73] op_sel_hi:[0, 1, 1]
	v_pk_mul_f32 v[72:73], v[54:55], v[6:7] op_sel_hi:[0,1]
	v_exp_f32_e32 v72, v72
	v_exp_f32_e32 v73, v73
	v_exp_f32_e32 v74, v74
	v_exp_f32_e32 v75, v75
	v_pk_fma_f32 v[70:71], s[76:77], v[136:137], v[70:71]
	v_pk_mul_f32 v[72:73], v[72:73], v[140:141]
	v_pk_fma_f32 v[70:71], s[78:79], v[138:139], v[70:71]
	v_pk_fma_f32 v[140:141], v[58:59], s[44:45], v[72:73] op_sel_hi:[0, 1, 1]
	v_pk_mul_f32 v[72:73], v[74:75], v[142:143]
	v_pk_fma_f32 v[70:71], s[80:81], v[140:141], v[70:71]
	v_pk_fma_f32 v[142:143], v[58:59], s[46:47], v[72:73] op_sel_hi:[0, 1, 1]
	v_pk_mul_f32 v[72:73], v[54:55], v[2:3] op_sel_hi:[0,1]
	v_exp_f32_e32 v72, v72
	v_exp_f32_e32 v73, v73
	v_pk_mul_f32 v[54:55], v[54:55], v[4:5] op_sel_hi:[0,1]
	v_exp_f32_e32 v54, v54
	v_exp_f32_e32 v55, v55
	v_pk_mul_f32 v[72:73], v[72:73], v[144:145]
	v_pk_fma_f32 v[70:71], s[82:83], v[142:143], v[70:71]
	v_pk_fma_f32 v[144:145], v[58:59], s[48:49], v[72:73] op_sel_hi:[0, 1, 1]
	v_pk_mul_f32 v[54:55], v[54:55], v[146:147]
	v_pk_fma_f32 v[70:71], s[84:85], v[144:145], v[70:71]
	v_pk_fma_f32 v[54:55], v[58:59], s[50:51], v[54:55] op_sel_hi:[0, 1, 1]
	v_pk_fma_f32 v[58:59], s[86:87], v[54:55], v[70:71]
	s_nop 0
	v_add_f32_e32 v58, v58, v59
	v_fma_mix_f32 v58, v1, v56, v58 op_sel_hi:[0,1,0]
	v_fma_mixlo_f16 v58, v58, v60, 0 op_sel_hi:[0,1,0]
	ds_write_b16 v68, v58 offset:8256
	s_waitcnt lgkmcnt(0)
	s_load_dwordx16 s[36:51], s[54:55], 0x300
	s_load_dwordx16 s[72:87], s[54:55], 0x340
	v_cvt_f32_f16_sdwa v58, v64 dst_sel:DWORD dst_unused:UNUSED_PAD src0_sel:WORD_1
	v_cvt_f32_f16_sdwa v59, v56 dst_sel:DWORD dst_unused:UNUSED_PAD src0_sel:WORD_1
	v_pk_mul_f32 v[146:147], v[58:59], v[14:15] op_sel_hi:[0,1]
	v_exp_f32_e32 v146, v146
	v_exp_f32_e32 v147, v147
	v_pk_mul_f32 v[148:149], v[58:59], v[16:17] op_sel_hi:[0,1]
	v_exp_f32_e32 v148, v148
	v_exp_f32_e32 v149, v149
	v_mul_f32_e32 v64, v58, v59
	v_pk_mul_f32 v[62:63], v[146:147], v[62:63]
	v_pk_fma_f32 v[62:63], v[64:65], s[56:57], v[62:63] op_sel_hi:[0, 1, 1]
	v_pk_fma_f32 v[102:103], s[88:89], v[62:63], 0 op_sel_hi:[1, 1, 0]
	v_pk_mul_f32 v[118:119], v[148:149], v[134:135]
	s_nop 0
	v_pk_fma_f32 v[134:135], v[64:65], s[58:59], v[118:119] op_sel_hi:[0, 1, 1]
	v_pk_mul_f32 v[104:105], v[58:59], v[10:11] op_sel_hi:[0,1]
	v_exp_f32_e32 v104, v104
	v_exp_f32_e32 v105, v105
	v_pk_mul_f32 v[118:119], v[58:59], v[12:13] op_sel_hi:[0,1]
	v_exp_f32_e32 v118, v118
	v_exp_f32_e32 v119, v119
	v_pk_mul_f32 v[104:105], v[104:105], v[136:137]
	v_pk_fma_f32 v[102:103], s[90:91], v[134:135], v[102:103]
	v_pk_fma_f32 v[136:137], v[64:65], s[60:61], v[104:105] op_sel_hi:[0, 1, 1]
	v_pk_mul_f32 v[104:105], v[118:119], v[138:139]
	v_pk_mul_f32 v[106:107], v[58:59], v[8:9] op_sel_hi:[0,1]
	v_pk_fma_f32 v[138:139], v[64:65], s[62:63], v[104:105] op_sel_hi:[0, 1, 1]
	v_pk_mul_f32 v[104:105], v[58:59], v[6:7] op_sel_hi:[0,1]
	v_exp_f32_e32 v104, v104
	v_exp_f32_e32 v105, v105
	v_exp_f32_e32 v106, v106
	v_exp_f32_e32 v107, v107
	v_pk_fma_f32 v[102:103], s[92:93], v[136:137], v[102:103]
	v_pk_mul_f32 v[104:105], v[104:105], v[140:141]
	v_pk_fma_f32 v[102:103], s[94:95], v[138:139], v[102:103]
	v_pk_fma_f32 v[140:141], v[64:65], s[64:65], v[104:105] op_sel_hi:[0, 1, 1]
	v_pk_mul_f32 v[104:105], v[106:107], v[142:143]
	v_pk_fma_f32 v[102:103], s[96:97], v[140:141], v[102:103]
	v_pk_fma_f32 v[142:143], v[64:65], s[66:67], v[104:105] op_sel_hi:[0, 1, 1]
	v_pk_mul_f32 v[104:105], v[58:59], v[2:3] op_sel_hi:[0,1]
	v_exp_f32_e32 v104, v104
	v_exp_f32_e32 v105, v105
	v_pk_mul_f32 v[58:59], v[58:59], v[4:5] op_sel_hi:[0,1]
	v_exp_f32_e32 v58, v58
	v_exp_f32_e32 v59, v59
	v_pk_mul_f32 v[104:105], v[104:105], v[144:145]
	v_pk_fma_f32 v[102:103], s[98:99], v[142:143], v[102:103]
	v_pk_fma_f32 v[144:145], v[64:65], s[68:69], v[104:105] op_sel_hi:[0, 1, 1]
	v_pk_mul_f32 v[54:55], v[58:59], v[54:55]
	v_pk_fma_f32 v[102:103], s[20:21], v[144:145], v[102:103]
	v_pk_fma_f32 v[54:55], v[64:65], s[70:71], v[54:55] op_sel_hi:[0, 1, 1]
	v_pk_fma_f32 v[58:59], s[22:23], v[54:55], v[102:103]
	s_nop 0
	v_add_f32_e32 v58, v58, v59
	v_fma_mix_f32 v56, v1, v56, v58 op_sel:[0,1,0] op_sel_hi:[0,1,0]
	v_fma_mixlo_f16 v56, v56, v60, 0 op_sel:[0,1,0] op_sel_hi:[0,1,0]
	ds_write_b16 v68, v56 offset:9296
	s_waitcnt lgkmcnt(0)
	s_load_dwordx16 s[56:71], s[54:55], 0x380
	s_load_dwordx8 s[88:95], s[54:55], 0x3c0
	s_load_dwordx4 s[96:99], s[54:55], 0x3e0
	s_load_dwordx4 s[20:23], s[54:55], 0x3f0
	v_cvt_f32_f16_e32 v56, v65
	v_cvt_f32_f16_e32 v58, v57
	v_pk_mul_f32 v[146:147], v[56:57], v[14:15] op_sel_hi:[0,1]
	v_exp_f32_e32 v146, v146
	v_exp_f32_e32 v147, v147
	v_pk_mul_f32 v[148:149], v[56:57], v[16:17] op_sel_hi:[0,1]
	v_exp_f32_e32 v148, v148
	v_exp_f32_e32 v149, v149
	v_mul_f32_e32 v58, v56, v58
	v_pk_mul_f32 v[62:63], v[146:147], v[62:63]
	v_pk_fma_f32 v[62:63], v[58:59], s[36:37], v[62:63] op_sel_hi:[0, 1, 1]
	v_pk_fma_f32 v[70:71], s[72:73], v[62:63], 0 op_sel_hi:[1, 1, 0]
	v_pk_mul_f32 v[86:87], v[148:149], v[134:135]
	s_nop 0
	v_pk_fma_f32 v[134:135], v[58:59], s[38:39], v[86:87] op_sel_hi:[0, 1, 1]
	v_pk_mul_f32 v[72:73], v[56:57], v[10:11] op_sel_hi:[0,1]
	v_exp_f32_e32 v72, v72
	v_exp_f32_e32 v73, v73
	v_pk_mul_f32 v[86:87], v[56:57], v[12:13] op_sel_hi:[0,1]
	v_exp_f32_e32 v86, v86
	v_exp_f32_e32 v87, v87
	v_pk_mul_f32 v[72:73], v[72:73], v[136:137]
	v_pk_fma_f32 v[70:71], s[74:75], v[134:135], v[70:71]
	v_pk_fma_f32 v[136:137], v[58:59], s[40:41], v[72:73] op_sel_hi:[0, 1, 1]
	v_pk_mul_f32 v[72:73], v[86:87], v[138:139]
	v_pk_mul_f32 v[74:75], v[56:57], v[8:9] op_sel_hi:[0,1]
	v_pk_fma_f32 v[138:139], v[58:59], s[42:43], v[72:73] op_sel_hi:[0, 1, 1]
	v_pk_mul_f32 v[72:73], v[56:57], v[6:7] op_sel_hi:[0,1]
	v_exp_f32_e32 v72, v72
	v_exp_f32_e32 v73, v73
	v_exp_f32_e32 v74, v74
	v_exp_f32_e32 v75, v75
	v_pk_fma_f32 v[70:71], s[76:77], v[136:137], v[70:71]
	v_pk_mul_f32 v[72:73], v[72:73], v[140:141]
	v_pk_fma_f32 v[70:71], s[78:79], v[138:139], v[70:71]
	v_pk_fma_f32 v[140:141], v[58:59], s[44:45], v[72:73] op_sel_hi:[0, 1, 1]
	v_pk_mul_f32 v[72:73], v[74:75], v[142:143]
	v_pk_mul_f32 v[74:75], v[56:57], v[4:5] op_sel_hi:[0,1]
	v_pk_fma_f32 v[142:143], v[58:59], s[46:47], v[72:73] op_sel_hi:[0, 1, 1]
	v_pk_mul_f32 v[72:73], v[56:57], v[2:3] op_sel_hi:[0,1]
	v_exp_f32_e32 v72, v72
	v_exp_f32_e32 v73, v73
	v_exp_f32_e32 v74, v74
	v_exp_f32_e32 v75, v75
	v_pk_fma_f32 v[70:71], s[80:81], v[140:141], v[70:71]
	v_pk_mul_f32 v[72:73], v[72:73], v[144:145]
	v_pk_fma_f32 v[70:71], s[82:83], v[142:143], v[70:71]
	v_pk_fma_f32 v[144:145], v[58:59], s[48:49], v[72:73] op_sel_hi:[0, 1, 1]
	v_pk_mul_f32 v[54:55], v[74:75], v[54:55]
	v_pk_fma_f32 v[70:71], s[84:85], v[144:145], v[70:71]
	v_pk_fma_f32 v[54:55], v[58:59], s[50:51], v[54:55] op_sel_hi:[0, 1, 1]
	v_pk_fma_f32 v[58:59], s[86:87], v[54:55], v[70:71]
	s_nop 0
	v_add_f32_e32 v56, v58, v59
	v_fma_mix_f32 v56, v1, v57, v56 op_sel_hi:[0,1,0]
	v_fma_mixlo_f16 v56, v56, v61, 0 op_sel_hi:[0,1,0]
	ds_write_b16 v68, v56 offset:10336
	s_waitcnt lgkmcnt(0)
	s_load_dwordx16 s[36:51], s[54:55], 0x400
	s_load_dwordx16 s[72:87], s[54:55], 0x440
	v_cvt_f32_f16_sdwa v56, v65 dst_sel:DWORD dst_unused:UNUSED_PAD src0_sel:WORD_1
	v_cvt_f32_f16_sdwa v58, v57 dst_sel:DWORD dst_unused:UNUSED_PAD src0_sel:WORD_1
	v_pk_mul_f32 v[64:65], v[56:57], v[14:15] op_sel_hi:[0,1]
	v_pk_mul_f32 v[146:147], v[56:57], v[16:17] op_sel_hi:[0,1]
	v_exp_f32_e32 v64, v64
	v_exp_f32_e32 v65, v65
	v_exp_f32_e32 v146, v146
	v_exp_f32_e32 v147, v147
	v_mul_f32_e32 v58, v56, v58
	v_pk_mul_f32 v[62:63], v[64:65], v[62:63]
	v_pk_mul_f32 v[64:65], v[146:147], v[134:135]
	v_pk_fma_f32 v[134:135], v[58:59], s[58:59], v[64:65] op_sel_hi:[0, 1, 1]
	v_pk_mul_f32 v[64:65], v[56:57], v[10:11] op_sel_hi:[0,1]
	v_pk_fma_f32 v[148:149], v[58:59], s[56:57], v[62:63] op_sel_hi:[0, 1, 1]
	v_exp_f32_e32 v64, v64
	v_exp_f32_e32 v65, v65
	v_pk_mul_f32 v[102:103], v[56:57], v[12:13] op_sel_hi:[0,1]
	v_exp_f32_e32 v102, v102
	v_exp_f32_e32 v103, v103
	v_pk_fma_f32 v[62:63], s[88:89], v[148:149], 0 op_sel_hi:[1, 1, 0]
	v_pk_mul_f32 v[64:65], v[64:65], v[136:137]
	v_pk_fma_f32 v[62:63], s[90:91], v[134:135], v[62:63]
	v_pk_fma_f32 v[136:137], v[58:59], s[60:61], v[64:65] op_sel_hi:[0, 1, 1]
	v_pk_mul_f32 v[64:65], v[102:103], v[138:139]
	v_pk_fma_f32 v[62:63], s[92:93], v[136:137], v[62:63]
	v_pk_fma_f32 v[122:123], v[58:59], s[62:63], v[64:65] op_sel_hi:[0, 1, 1]
	v_pk_mul_f32 v[64:65], v[56:57], v[6:7] op_sel_hi:[0,1]
	v_exp_f32_e32 v64, v64
	v_exp_f32_e32 v65, v65
	v_pk_mul_f32 v[102:103], v[56:57], v[8:9] op_sel_hi:[0,1]
	v_exp_f32_e32 v102, v102
	v_exp_f32_e32 v103, v103
	v_pk_mul_f32 v[64:65], v[64:65], v[140:141]
	v_pk_fma_f32 v[62:63], s[94:95], v[122:123], v[62:63]
	v_pk_fma_f32 v[124:125], v[58:59], s[64:65], v[64:65] op_sel_hi:[0, 1, 1]
	v_pk_mul_f32 v[64:65], v[102:103], v[142:143]
	v_pk_fma_f32 v[62:63], s[96:97], v[124:125], v[62:63]
	v_pk_fma_f32 v[126:127], v[58:59], s[66:67], v[64:65] op_sel_hi:[0, 1, 1]
	v_pk_mul_f32 v[64:65], v[56:57], v[2:3] op_sel_hi:[0,1]
	v_exp_f32_e32 v64, v64
	v_exp_f32_e32 v65, v65
	v_pk_mul_f32 v[102:103], v[56:57], v[4:5] op_sel_hi:[0,1]
	v_exp_f32_e32 v102, v102
	v_exp_f32_e32 v103, v103
	v_pk_mul_f32 v[64:65], v[64:65], v[144:145]
	v_pk_fma_f32 v[62:63], s[98:99], v[126:127], v[62:63]
	v_pk_fma_f32 v[128:129], v[58:59], s[68:69], v[64:65] op_sel_hi:[0, 1, 1]
	v_pk_mul_f32 v[54:55], v[102:103], v[54:55]
	v_pk_fma_f32 v[62:63], s[20:21], v[128:129], v[62:63]
	v_pk_fma_f32 v[130:131], v[58:59], s[70:71], v[54:55] op_sel_hi:[0, 1, 1]
	v_pk_fma_f32 v[54:55], s[22:23], v[130:131], v[62:63]
	s_nop 0
	v_add_f32_e32 v54, v54, v55
	v_fma_mix_f32 v54, v1, v57, v54 op_sel:[0,1,0] op_sel_hi:[0,1,0]
	v_fma_mixlo_f16 v54, v54, v61, 0 op_sel:[0,1,0] op_sel_hi:[0,1,0]
	ds_write_b16 v68, v54 offset:11376
	s_waitcnt lgkmcnt(0)
	s_load_dwordx16 s[56:71], s[54:55], 0x480
	s_load_dwordx8 s[88:95], s[54:55], 0x4c0
	s_load_dwordx4 s[96:99], s[54:55], 0x4e0
	s_load_dwordx4 s[20:23], s[54:55], 0x4f0
	s_waitcnt vmcnt(8)
	v_cvt_f32_f16_e32 v132, v50
	s_waitcnt vmcnt(7)
	v_cvt_f32_f16_e32 v69, v42
	v_pk_mul_f32 v[140:141], v[132:133], v[14:15] op_sel_hi:[0,1]
	v_exp_f32_e32 v140, v140
	v_exp_f32_e32 v141, v141
	v_pk_mul_f32 v[142:143], v[132:133], v[16:17] op_sel_hi:[0,1]
	v_exp_f32_e32 v142, v142
	v_exp_f32_e32 v143, v143
	v_mul_f32_e32 v138, v132, v69
	v_pk_mul_f32 v[140:141], v[140:141], v[148:149]
	v_pk_fma_f32 v[140:141], v[138:139], s[36:37], v[140:141] op_sel_hi:[0, 1, 1]
	v_pk_fma_f32 v[70:71], s[72:73], v[140:141], 0 op_sel_hi:[1, 1, 0]
	v_pk_mul_f32 v[86:87], v[142:143], v[134:135]
	s_nop 0
	v_pk_fma_f32 v[134:135], v[138:139], s[38:39], v[86:87] op_sel_hi:[0, 1, 1]
	v_pk_mul_f32 v[72:73], v[132:133], v[10:11] op_sel_hi:[0,1]
	v_exp_f32_e32 v72, v72
	v_exp_f32_e32 v73, v73
	v_pk_mul_f32 v[86:87], v[132:133], v[12:13] op_sel_hi:[0,1]
	v_exp_f32_e32 v86, v86
	v_exp_f32_e32 v87, v87
	v_pk_mul_f32 v[72:73], v[72:73], v[136:137]
	v_pk_fma_f32 v[70:71], s[74:75], v[134:135], v[70:71]
	v_pk_fma_f32 v[136:137], v[138:139], s[40:41], v[72:73] op_sel_hi:[0, 1, 1]
	v_pk_mul_f32 v[72:73], v[86:87], v[122:123]
	v_pk_mul_f32 v[74:75], v[132:133], v[8:9] op_sel_hi:[0,1]
	v_pk_fma_f32 v[122:123], v[138:139], s[42:43], v[72:73] op_sel_hi:[0, 1, 1]
	v_pk_mul_f32 v[72:73], v[132:133], v[6:7] op_sel_hi:[0,1]
	v_exp_f32_e32 v72, v72
	v_exp_f32_e32 v73, v73
	v_exp_f32_e32 v74, v74
	v_exp_f32_e32 v75, v75
	v_pk_fma_f32 v[70:71], s[76:77], v[136:137], v[70:71]
	v_pk_mul_f32 v[72:73], v[72:73], v[124:125]
	v_pk_fma_f32 v[70:71], s[78:79], v[122:123], v[70:71]
	v_pk_fma_f32 v[124:125], v[138:139], s[44:45], v[72:73] op_sel_hi:[0, 1, 1]
	v_pk_mul_f32 v[72:73], v[74:75], v[126:127]
	v_pk_mul_f32 v[74:75], v[132:133], v[4:5] op_sel_hi:[0,1]
	v_pk_fma_f32 v[126:127], v[138:139], s[46:47], v[72:73] op_sel_hi:[0, 1, 1]
	v_pk_mul_f32 v[72:73], v[132:133], v[2:3] op_sel_hi:[0,1]
	v_exp_f32_e32 v72, v72
	v_exp_f32_e32 v73, v73
	v_exp_f32_e32 v74, v74
	v_exp_f32_e32 v75, v75
	v_pk_fma_f32 v[70:71], s[80:81], v[124:125], v[70:71]
	v_pk_mul_f32 v[72:73], v[72:73], v[128:129]
	v_pk_fma_f32 v[70:71], s[82:83], v[126:127], v[70:71]
	v_pk_fma_f32 v[128:129], v[138:139], s[48:49], v[72:73] op_sel_hi:[0, 1, 1]
	v_pk_mul_f32 v[72:73], v[74:75], v[130:131]
	v_pk_fma_f32 v[70:71], s[84:85], v[128:129], v[70:71]
	v_pk_fma_f32 v[130:131], v[138:139], s[50:51], v[72:73] op_sel_hi:[0, 1, 1]
	v_pk_fma_f32 v[70:71], s[86:87], v[130:131], v[70:71]
	s_nop 0
	v_add_f32_e32 v69, v70, v71
	v_fma_mix_f32 v69, v1, v42, v69 op_sel_hi:[0,1,0]
	s_waitcnt vmcnt(6)
	v_fma_mixlo_f16 v69, v69, v46, 0 op_sel_hi:[0,1,0]
	ds_write_b16 v68, v69 offset:12416
	s_waitcnt lgkmcnt(0)
	s_load_dwordx16 s[36:51], s[54:55], 0x500
	s_load_dwordx16 s[72:87], s[54:55], 0x540
	v_cvt_f32_f16_sdwa v50, v50 dst_sel:DWORD dst_unused:UNUSED_PAD src0_sel:WORD_1
	v_cvt_f32_f16_sdwa v69, v42 dst_sel:DWORD dst_unused:UNUSED_PAD src0_sel:WORD_1
	v_pk_mul_f32 v[138:139], v[50:51], v[14:15] op_sel_hi:[0,1]
	v_exp_f32_e32 v138, v138
	v_exp_f32_e32 v139, v139
	v_pk_mul_f32 v[142:143], v[50:51], v[16:17] op_sel_hi:[0,1]
	v_exp_f32_e32 v142, v142
	v_exp_f32_e32 v143, v143
	v_mul_f32_e32 v132, v50, v69
	v_pk_mul_f32 v[138:139], v[138:139], v[140:141]
	v_pk_fma_f32 v[138:139], v[132:133], s[56:57], v[138:139] op_sel_hi:[0, 1, 1]
	v_pk_fma_f32 v[54:55], s[88:89], v[138:139], 0 op_sel_hi:[1, 1, 0]
	v_pk_mul_f32 v[106:107], v[142:143], v[134:135]
	s_nop 0
	v_pk_fma_f32 v[134:135], v[132:133], s[58:59], v[106:107] op_sel_hi:[0, 1, 1]
	v_pk_mul_f32 v[56:57], v[50:51], v[10:11] op_sel_hi:[0,1]
	v_exp_f32_e32 v56, v56
	v_exp_f32_e32 v57, v57
	v_pk_mul_f32 v[106:107], v[50:51], v[12:13] op_sel_hi:[0,1]
	v_exp_f32_e32 v106, v106
	v_exp_f32_e32 v107, v107
	v_pk_mul_f32 v[56:57], v[56:57], v[136:137]
	v_pk_fma_f32 v[54:55], s[90:91], v[134:135], v[54:55]
	v_pk_fma_f32 v[136:137], v[132:133], s[60:61], v[56:57] op_sel_hi:[0, 1, 1]
	v_pk_mul_f32 v[56:57], v[106:107], v[122:123]
	v_pk_mul_f32 v[58:59], v[50:51], v[8:9] op_sel_hi:[0,1]
	v_pk_fma_f32 v[122:123], v[132:133], s[62:63], v[56:57] op_sel_hi:[0, 1, 1]
	v_pk_mul_f32 v[56:57], v[50:51], v[6:7] op_sel_hi:[0,1]
	v_exp_f32_e32 v56, v56
	v_exp_f32_e32 v57, v57
	v_exp_f32_e32 v58, v58
	v_exp_f32_e32 v59, v59
	v_pk_fma_f32 v[54:55], s[92:93], v[136:137], v[54:55]
	v_pk_mul_f32 v[56:57], v[56:57], v[124:125]
	v_pk_fma_f32 v[54:55], s[94:95], v[122:123], v[54:55]
	v_pk_fma_f32 v[124:125], v[132:133], s[64:65], v[56:57] op_sel_hi:[0, 1, 1]
	v_pk_mul_f32 v[56:57], v[58:59], v[126:127]
	v_pk_mul_f32 v[58:59], v[50:51], v[4:5] op_sel_hi:[0,1]
	v_pk_fma_f32 v[126:127], v[132:133], s[66:67], v[56:57] op_sel_hi:[0, 1, 1]
	v_pk_mul_f32 v[56:57], v[50:51], v[2:3] op_sel_hi:[0,1]
	v_exp_f32_e32 v56, v56
	v_exp_f32_e32 v57, v57
	v_exp_f32_e32 v58, v58
	v_exp_f32_e32 v59, v59
	v_pk_fma_f32 v[54:55], s[96:97], v[124:125], v[54:55]
	v_pk_mul_f32 v[56:57], v[56:57], v[128:129]
	v_pk_fma_f32 v[54:55], s[98:99], v[126:127], v[54:55]
	v_pk_fma_f32 v[128:129], v[132:133], s[68:69], v[56:57] op_sel_hi:[0, 1, 1]
	v_pk_mul_f32 v[56:57], v[58:59], v[130:131]
	v_pk_fma_f32 v[54:55], s[20:21], v[128:129], v[54:55]
	v_pk_fma_f32 v[130:131], v[132:133], s[70:71], v[56:57] op_sel_hi:[0, 1, 1]
	v_pk_fma_f32 v[54:55], s[22:23], v[130:131], v[54:55]
	s_nop 0
	v_add_f32_e32 v50, v54, v55
	v_fma_mix_f32 v42, v1, v42, v50 op_sel:[0,1,0] op_sel_hi:[0,1,0]
	v_fma_mixlo_f16 v42, v42, v46, 0 op_sel:[0,1,0] op_sel_hi:[0,1,0]
	ds_write_b16 v68, v42 offset:13456
	s_waitcnt lgkmcnt(0)
	s_load_dwordx16 s[56:71], s[54:55], 0x580
	s_load_dwordx8 s[88:95], s[54:55], 0x5c0
	s_load_dwordx4 s[96:99], s[54:55], 0x5e0
	s_load_dwordx4 s[20:23], s[54:55], 0x5f0
	v_cvt_f32_f16_e32 v42, v51
	v_cvt_f32_f16_e32 v46, v43
	v_pk_mul_f32 v[132:133], v[42:43], v[14:15] op_sel_hi:[0,1]
	v_exp_f32_e32 v132, v132
	v_exp_f32_e32 v133, v133
	v_pk_mul_f32 v[140:141], v[42:43], v[16:17] op_sel_hi:[0,1]
	v_exp_f32_e32 v140, v140
	v_exp_f32_e32 v141, v141
	v_mul_f32_e32 v46, v42, v46
	v_pk_mul_f32 v[132:133], v[132:133], v[138:139]
	v_pk_fma_f32 v[132:133], v[46:47], s[36:37], v[132:133] op_sel_hi:[0, 1, 1]
	v_pk_fma_f32 v[70:71], s[72:73], v[132:133], 0 op_sel_hi:[1, 1, 0]
	v_pk_mul_f32 v[86:87], v[140:141], v[134:135]
	s_nop 0
	v_pk_fma_f32 v[134:135], v[46:47], s[38:39], v[86:87] op_sel_hi:[0, 1, 1]
	v_pk_mul_f32 v[72:73], v[42:43], v[10:11] op_sel_hi:[0,1]
	v_exp_f32_e32 v72, v72
	v_exp_f32_e32 v73, v73
	v_pk_mul_f32 v[86:87], v[42:43], v[12:13] op_sel_hi:[0,1]
	v_exp_f32_e32 v86, v86
	v_exp_f32_e32 v87, v87
	v_pk_mul_f32 v[72:73], v[72:73], v[136:137]
	v_pk_fma_f32 v[70:71], s[74:75], v[134:135], v[70:71]
	v_pk_fma_f32 v[136:137], v[46:47], s[40:41], v[72:73] op_sel_hi:[0, 1, 1]
	v_pk_mul_f32 v[72:73], v[86:87], v[122:123]
	v_pk_mul_f32 v[74:75], v[42:43], v[8:9] op_sel_hi:[0,1]
	v_pk_fma_f32 v[122:123], v[46:47], s[42:43], v[72:73] op_sel_hi:[0, 1, 1]
	v_pk_mul_f32 v[72:73], v[42:43], v[6:7] op_sel_hi:[0,1]
	v_exp_f32_e32 v72, v72
	v_exp_f32_e32 v73, v73
	v_exp_f32_e32 v74, v74
	v_exp_f32_e32 v75, v75
	v_pk_fma_f32 v[70:71], s[76:77], v[136:137], v[70:71]
	v_pk_mul_f32 v[72:73], v[72:73], v[124:125]
	v_pk_fma_f32 v[70:71], s[78:79], v[122:123], v[70:71]
	v_pk_fma_f32 v[124:125], v[46:47], s[44:45], v[72:73] op_sel_hi:[0, 1, 1]
	v_pk_mul_f32 v[72:73], v[74:75], v[126:127]
	v_pk_mul_f32 v[74:75], v[42:43], v[4:5] op_sel_hi:[0,1]
	v_pk_fma_f32 v[126:127], v[46:47], s[46:47], v[72:73] op_sel_hi:[0, 1, 1]
	v_pk_mul_f32 v[72:73], v[42:43], v[2:3] op_sel_hi:[0,1]
	v_exp_f32_e32 v72, v72
	v_exp_f32_e32 v73, v73
	v_exp_f32_e32 v74, v74
	v_exp_f32_e32 v75, v75
	v_pk_fma_f32 v[70:71], s[80:81], v[124:125], v[70:71]
	v_pk_mul_f32 v[72:73], v[72:73], v[128:129]
	v_pk_fma_f32 v[70:71], s[82:83], v[126:127], v[70:71]
	v_pk_fma_f32 v[128:129], v[46:47], s[48:49], v[72:73] op_sel_hi:[0, 1, 1]
	v_pk_mul_f32 v[72:73], v[74:75], v[130:131]
	v_pk_fma_f32 v[70:71], s[84:85], v[128:129], v[70:71]
	v_pk_fma_f32 v[130:131], v[46:47], s[50:51], v[72:73] op_sel_hi:[0, 1, 1]
	v_pk_fma_f32 v[70:71], s[86:87], v[130:131], v[70:71]
	s_nop 0
	v_add_f32_e32 v42, v70, v71
	v_fma_mix_f32 v42, v1, v43, v42 op_sel_hi:[0,1,0]
	v_fma_mixlo_f16 v42, v42, v47, 0 op_sel_hi:[0,1,0]
	ds_write_b16 v68, v42 offset:14496
	s_waitcnt lgkmcnt(0)
	s_load_dwordx16 s[36:51], s[54:55], 0x600
	s_load_dwordx16 s[72:87], s[54:55], 0x640
	v_cvt_f32_f16_sdwa v42, v51 dst_sel:DWORD dst_unused:UNUSED_PAD src0_sel:WORD_1
	v_cvt_f32_f16_sdwa v46, v43 dst_sel:DWORD dst_unused:UNUSED_PAD src0_sel:WORD_1
	v_pk_mul_f32 v[50:51], v[42:43], v[14:15] op_sel_hi:[0,1]
	v_exp_f32_e32 v50, v50
	v_exp_f32_e32 v51, v51
	v_pk_mul_f32 v[138:139], v[42:43], v[16:17] op_sel_hi:[0,1]
	v_exp_f32_e32 v138, v138
	v_exp_f32_e32 v139, v139
	v_mul_f32_e32 v46, v42, v46
	v_pk_mul_f32 v[50:51], v[50:51], v[132:133]
	v_pk_fma_f32 v[50:51], v[46:47], s[56:57], v[50:51] op_sel_hi:[0, 1, 1]
	v_pk_fma_f32 v[54:55], s[88:89], v[50:51], 0 op_sel_hi:[1, 1, 0]
	v_pk_mul_f32 v[106:107], v[138:139], v[134:135]
	s_nop 0
	v_pk_fma_f32 v[132:133], v[46:47], s[58:59], v[106:107] op_sel_hi:[0, 1, 1]
	v_pk_mul_f32 v[56:57], v[42:43], v[10:11] op_sel_hi:[0,1]
	v_exp_f32_e32 v56, v56
	v_exp_f32_e32 v57, v57
	v_pk_mul_f32 v[106:107], v[42:43], v[12:13] op_sel_hi:[0,1]
	v_exp_f32_e32 v106, v106
	v_exp_f32_e32 v107, v107
	v_pk_mul_f32 v[56:57], v[56:57], v[136:137]
	v_pk_fma_f32 v[54:55], s[90:91], v[132:133], v[54:55]
	v_pk_fma_f32 v[134:135], v[46:47], s[60:61], v[56:57] op_sel_hi:[0, 1, 1]
	v_pk_mul_f32 v[56:57], v[106:107], v[122:123]
	v_pk_mul_f32 v[58:59], v[42:43], v[8:9] op_sel_hi:[0,1]
	v_pk_fma_f32 v[122:123], v[46:47], s[62:63], v[56:57] op_sel_hi:[0, 1, 1]
	v_pk_mul_f32 v[56:57], v[42:43], v[6:7] op_sel_hi:[0,1]
	v_exp_f32_e32 v56, v56
	v_exp_f32_e32 v57, v57
	v_exp_f32_e32 v58, v58
	v_exp_f32_e32 v59, v59
	v_pk_fma_f32 v[54:55], s[92:93], v[134:135], v[54:55]
	v_pk_mul_f32 v[56:57], v[56:57], v[124:125]
	v_pk_fma_f32 v[54:55], s[94:95], v[122:123], v[54:55]
	v_pk_fma_f32 v[124:125], v[46:47], s[64:65], v[56:57] op_sel_hi:[0, 1, 1]
	v_pk_mul_f32 v[56:57], v[58:59], v[126:127]
	v_pk_mul_f32 v[58:59], v[42:43], v[4:5] op_sel_hi:[0,1]
	v_pk_fma_f32 v[126:127], v[46:47], s[66:67], v[56:57] op_sel_hi:[0, 1, 1]
	v_pk_mul_f32 v[56:57], v[42:43], v[2:3] op_sel_hi:[0,1]
	v_exp_f32_e32 v56, v56
	v_exp_f32_e32 v57, v57
	v_exp_f32_e32 v58, v58
	v_exp_f32_e32 v59, v59
	v_pk_fma_f32 v[54:55], s[96:97], v[124:125], v[54:55]
	v_pk_mul_f32 v[56:57], v[56:57], v[128:129]
	v_pk_fma_f32 v[54:55], s[98:99], v[126:127], v[54:55]
	v_pk_fma_f32 v[128:129], v[46:47], s[68:69], v[56:57] op_sel_hi:[0, 1, 1]
	v_pk_mul_f32 v[56:57], v[58:59], v[130:131]
	v_pk_fma_f32 v[54:55], s[20:21], v[128:129], v[54:55]
	v_pk_fma_f32 v[130:131], v[46:47], s[70:71], v[56:57] op_sel_hi:[0, 1, 1]
	v_pk_fma_f32 v[54:55], s[22:23], v[130:131], v[54:55]
	s_nop 0
	v_add_f32_e32 v42, v54, v55
	v_fma_mix_f32 v42, v1, v43, v42 op_sel:[0,1,0] op_sel_hi:[0,1,0]
	v_fma_mixlo_f16 v42, v42, v47, 0 op_sel:[0,1,0] op_sel_hi:[0,1,0]
	ds_write_b16 v68, v42 offset:15536
	s_waitcnt lgkmcnt(0)
	s_load_dwordx16 s[56:71], s[54:55], 0x680
	s_load_dwordx8 s[88:95], s[54:55], 0x6c0
	s_load_dwordx4 s[96:99], s[54:55], 0x6e0
	s_load_dwordx4 s[20:23], s[54:55], 0x6f0
	v_cvt_f32_f16_e32 v42, v52
	v_cvt_f32_f16_e32 v43, v44
	v_pk_mul_f32 v[136:137], v[42:43], v[14:15] op_sel_hi:[0,1]
	v_exp_f32_e32 v136, v136
	v_exp_f32_e32 v137, v137
	v_pk_mul_f32 v[138:139], v[42:43], v[16:17] op_sel_hi:[0,1]
	v_exp_f32_e32 v138, v138
	v_exp_f32_e32 v139, v139
	v_mul_f32_e32 v46, v42, v43
	v_pk_mul_f32 v[50:51], v[136:137], v[50:51]
	v_pk_fma_f32 v[50:51], v[46:47], s[36:37], v[50:51] op_sel_hi:[0, 1, 1]
	v_pk_fma_f32 v[70:71], s[72:73], v[50:51], 0 op_sel_hi:[1, 1, 0]
	v_pk_mul_f32 v[86:87], v[138:139], v[132:133]
	s_nop 0
	v_pk_fma_f32 v[132:133], v[46:47], s[38:39], v[86:87] op_sel_hi:[0, 1, 1]
	v_pk_mul_f32 v[72:73], v[42:43], v[10:11] op_sel_hi:[0,1]
	v_exp_f32_e32 v72, v72
	v_exp_f32_e32 v73, v73
	v_pk_mul_f32 v[86:87], v[42:43], v[12:13] op_sel_hi:[0,1]
	v_exp_f32_e32 v86, v86
	v_exp_f32_e32 v87, v87
	v_pk_mul_f32 v[72:73], v[72:73], v[134:135]
	v_pk_fma_f32 v[70:71], s[74:75], v[132:133], v[70:71]
	v_pk_fma_f32 v[134:135], v[46:47], s[40:41], v[72:73] op_sel_hi:[0, 1, 1]
	v_pk_mul_f32 v[72:73], v[86:87], v[122:123]
	v_pk_mul_f32 v[74:75], v[42:43], v[8:9] op_sel_hi:[0,1]
	v_pk_fma_f32 v[122:123], v[46:47], s[42:43], v[72:73] op_sel_hi:[0, 1, 1]
	v_pk_mul_f32 v[72:73], v[42:43], v[6:7] op_sel_hi:[0,1]
	v_exp_f32_e32 v72, v72
	v_exp_f32_e32 v73, v73
	v_exp_f32_e32 v74, v74
	v_exp_f32_e32 v75, v75
	v_pk_fma_f32 v[70:71], s[76:77], v[134:135], v[70:71]
	v_pk_mul_f32 v[72:73], v[72:73], v[124:125]
	v_pk_fma_f32 v[70:71], s[78:79], v[122:123], v[70:71]
	v_pk_fma_f32 v[124:125], v[46:47], s[44:45], v[72:73] op_sel_hi:[0, 1, 1]
	v_pk_mul_f32 v[72:73], v[74:75], v[126:127]
	v_pk_fma_f32 v[70:71], s[80:81], v[124:125], v[70:71]
	v_pk_fma_f32 v[126:127], v[46:47], s[46:47], v[72:73] op_sel_hi:[0, 1, 1]
	v_pk_mul_f32 v[72:73], v[42:43], v[2:3] op_sel_hi:[0,1]
	v_exp_f32_e32 v72, v72
	v_exp_f32_e32 v73, v73
	v_pk_mul_f32 v[42:43], v[42:43], v[4:5] op_sel_hi:[0,1]
	v_exp_f32_e32 v42, v42
	v_exp_f32_e32 v43, v43
	v_pk_mul_f32 v[72:73], v[72:73], v[128:129]
	v_pk_fma_f32 v[70:71], s[82:83], v[126:127], v[70:71]
	v_pk_fma_f32 v[128:129], v[46:47], s[48:49], v[72:73] op_sel_hi:[0, 1, 1]
	v_pk_mul_f32 v[42:43], v[42:43], v[130:131]
	v_pk_fma_f32 v[70:71], s[84:85], v[128:129], v[70:71]
	v_pk_fma_f32 v[42:43], v[46:47], s[50:51], v[42:43] op_sel_hi:[0, 1, 1]
	v_pk_fma_f32 v[46:47], s[86:87], v[42:43], v[70:71]
	s_nop 0
	v_add_f32_e32 v46, v46, v47
	v_fma_mix_f32 v46, v1, v44, v46 op_sel_hi:[0,1,0]
	v_fma_mixlo_f16 v46, v46, v48, 0 op_sel_hi:[0,1,0]
	ds_write_b16 v68, v46 offset:16576
	s_waitcnt lgkmcnt(0)
	s_load_dwordx16 s[36:51], s[54:55], 0x700
	s_load_dwordx16 s[72:87], s[54:55], 0x740
	v_cvt_f32_f16_sdwa v46, v52 dst_sel:DWORD dst_unused:UNUSED_PAD src0_sel:WORD_1
	v_cvt_f32_f16_sdwa v47, v44 dst_sel:DWORD dst_unused:UNUSED_PAD src0_sel:WORD_1
	v_pk_mul_f32 v[130:131], v[46:47], v[14:15] op_sel_hi:[0,1]
	v_exp_f32_e32 v130, v130
	v_exp_f32_e32 v131, v131
	v_pk_mul_f32 v[136:137], v[46:47], v[16:17] op_sel_hi:[0,1]
	v_exp_f32_e32 v136, v136
	v_exp_f32_e32 v137, v137
	v_mul_f32_e32 v52, v46, v47
	v_pk_mul_f32 v[50:51], v[130:131], v[50:51]
	v_pk_fma_f32 v[50:51], v[52:53], s[56:57], v[50:51] op_sel_hi:[0, 1, 1]
	v_pk_fma_f32 v[54:55], s[88:89], v[50:51], 0 op_sel_hi:[1, 1, 0]
	v_pk_mul_f32 v[106:107], v[136:137], v[132:133]
	s_nop 0
	v_pk_fma_f32 v[130:131], v[52:53], s[58:59], v[106:107] op_sel_hi:[0, 1, 1]
	v_pk_mul_f32 v[56:57], v[46:47], v[10:11] op_sel_hi:[0,1]
	v_exp_f32_e32 v56, v56
	v_exp_f32_e32 v57, v57
	v_pk_mul_f32 v[106:107], v[46:47], v[12:13] op_sel_hi:[0,1]
	v_exp_f32_e32 v106, v106
	v_exp_f32_e32 v107, v107
	v_pk_mul_f32 v[56:57], v[56:57], v[134:135]
	v_pk_fma_f32 v[54:55], s[90:91], v[130:131], v[54:55]
	v_pk_fma_f32 v[132:133], v[52:53], s[60:61], v[56:57] op_sel_hi:[0, 1, 1]
	v_pk_mul_f32 v[56:57], v[106:107], v[122:123]
	v_pk_mul_f32 v[58:59], v[46:47], v[8:9] op_sel_hi:[0,1]
	v_pk_fma_f32 v[122:123], v[52:53], s[62:63], v[56:57] op_sel_hi:[0, 1, 1]
	v_pk_mul_f32 v[56:57], v[46:47], v[6:7] op_sel_hi:[0,1]
	v_exp_f32_e32 v56, v56
	v_exp_f32_e32 v57, v57
	v_exp_f32_e32 v58, v58
	v_exp_f32_e32 v59, v59
	v_pk_fma_f32 v[54:55], s[92:93], v[132:133], v[54:55]
	v_pk_mul_f32 v[56:57], v[56:57], v[124:125]
	v_pk_fma_f32 v[54:55], s[94:95], v[122:123], v[54:55]
	v_pk_fma_f32 v[124:125], v[52:53], s[64:65], v[56:57] op_sel_hi:[0, 1, 1]
	v_pk_mul_f32 v[56:57], v[58:59], v[126:127]
	v_pk_fma_f32 v[54:55], s[96:97], v[124:125], v[54:55]
	v_pk_fma_f32 v[126:127], v[52:53], s[66:67], v[56:57] op_sel_hi:[0, 1, 1]
	v_pk_mul_f32 v[56:57], v[46:47], v[2:3] op_sel_hi:[0,1]
	v_exp_f32_e32 v56, v56
	v_exp_f32_e32 v57, v57
	v_pk_mul_f32 v[46:47], v[46:47], v[4:5] op_sel_hi:[0,1]
	v_exp_f32_e32 v46, v46
	v_exp_f32_e32 v47, v47
	v_pk_mul_f32 v[56:57], v[56:57], v[128:129]
	v_pk_fma_f32 v[54:55], s[98:99], v[126:127], v[54:55]
	v_pk_fma_f32 v[128:129], v[52:53], s[68:69], v[56:57] op_sel_hi:[0, 1, 1]
	v_pk_mul_f32 v[42:43], v[46:47], v[42:43]
	v_pk_fma_f32 v[54:55], s[20:21], v[128:129], v[54:55]
	v_pk_fma_f32 v[42:43], v[52:53], s[70:71], v[42:43] op_sel_hi:[0, 1, 1]
	v_pk_fma_f32 v[46:47], s[22:23], v[42:43], v[54:55]
	s_nop 0
	v_add_f32_e32 v46, v46, v47
	v_fma_mix_f32 v44, v1, v44, v46 op_sel:[0,1,0] op_sel_hi:[0,1,0]
	v_fma_mixlo_f16 v44, v44, v48, 0 op_sel:[0,1,0] op_sel_hi:[0,1,0]
	ds_write_b16 v68, v44 offset:17616
	s_waitcnt lgkmcnt(0)
	s_load_dwordx16 s[56:71], s[54:55], 0x780
	s_load_dwordx8 s[88:95], s[54:55], 0x7c0
	s_load_dwordx4 s[96:99], s[54:55], 0x7e0
	s_load_dwordx4 s[20:23], s[54:55], 0x7f0
	v_cvt_f32_f16_e32 v44, v53
	v_cvt_f32_f16_e32 v46, v45
	v_pk_mul_f32 v[134:135], v[44:45], v[14:15] op_sel_hi:[0,1]
	v_exp_f32_e32 v134, v134
	v_exp_f32_e32 v135, v135
	v_pk_mul_f32 v[136:137], v[44:45], v[16:17] op_sel_hi:[0,1]
	v_exp_f32_e32 v136, v136
	v_exp_f32_e32 v137, v137
	v_mul_f32_e32 v46, v44, v46
	v_pk_mul_f32 v[50:51], v[134:135], v[50:51]
	v_pk_fma_f32 v[50:51], v[46:47], s[36:37], v[50:51] op_sel_hi:[0, 1, 1]
	v_pk_fma_f32 v[70:71], s[72:73], v[50:51], 0 op_sel_hi:[1, 1, 0]
	v_pk_mul_f32 v[86:87], v[136:137], v[130:131]
	s_nop 0
	v_pk_fma_f32 v[130:131], v[46:47], s[38:39], v[86:87] op_sel_hi:[0, 1, 1]
	v_pk_mul_f32 v[72:73], v[44:45], v[10:11] op_sel_hi:[0,1]
	v_exp_f32_e32 v72, v72
	v_exp_f32_e32 v73, v73
	v_pk_mul_f32 v[86:87], v[44:45], v[12:13] op_sel_hi:[0,1]
	v_exp_f32_e32 v86, v86
	v_exp_f32_e32 v87, v87
	v_pk_mul_f32 v[72:73], v[72:73], v[132:133]
	v_pk_fma_f32 v[70:71], s[74:75], v[130:131], v[70:71]
	v_pk_fma_f32 v[132:133], v[46:47], s[40:41], v[72:73] op_sel_hi:[0, 1, 1]
	v_pk_mul_f32 v[72:73], v[86:87], v[122:123]
	v_pk_mul_f32 v[74:75], v[44:45], v[8:9] op_sel_hi:[0,1]
	v_pk_fma_f32 v[122:123], v[46:47], s[42:43], v[72:73] op_sel_hi:[0, 1, 1]
	v_pk_mul_f32 v[72:73], v[44:45], v[6:7] op_sel_hi:[0,1]
	v_exp_f32_e32 v72, v72
	v_exp_f32_e32 v73, v73
	v_exp_f32_e32 v74, v74
	v_exp_f32_e32 v75, v75
	v_pk_fma_f32 v[70:71], s[76:77], v[132:133], v[70:71]
	v_pk_mul_f32 v[72:73], v[72:73], v[124:125]
	v_pk_fma_f32 v[70:71], s[78:79], v[122:123], v[70:71]
	v_pk_fma_f32 v[124:125], v[46:47], s[44:45], v[72:73] op_sel_hi:[0, 1, 1]
	v_pk_mul_f32 v[72:73], v[74:75], v[126:127]
	v_pk_mul_f32 v[74:75], v[44:45], v[4:5] op_sel_hi:[0,1]
	v_pk_fma_f32 v[126:127], v[46:47], s[46:47], v[72:73] op_sel_hi:[0, 1, 1]
	v_pk_mul_f32 v[72:73], v[44:45], v[2:3] op_sel_hi:[0,1]
	v_exp_f32_e32 v72, v72
	v_exp_f32_e32 v73, v73
	v_exp_f32_e32 v74, v74
	v_exp_f32_e32 v75, v75
	v_pk_fma_f32 v[70:71], s[80:81], v[124:125], v[70:71]
	v_pk_mul_f32 v[72:73], v[72:73], v[128:129]
	v_pk_fma_f32 v[70:71], s[82:83], v[126:127], v[70:71]
	v_pk_fma_f32 v[128:129], v[46:47], s[48:49], v[72:73] op_sel_hi:[0, 1, 1]
	v_pk_mul_f32 v[42:43], v[74:75], v[42:43]
	v_pk_fma_f32 v[70:71], s[84:85], v[128:129], v[70:71]
	v_pk_fma_f32 v[42:43], v[46:47], s[50:51], v[42:43] op_sel_hi:[0, 1, 1]
	v_pk_fma_f32 v[46:47], s[86:87], v[42:43], v[70:71]
	s_nop 0
	v_add_f32_e32 v44, v46, v47
	v_fma_mix_f32 v44, v1, v45, v44 op_sel_hi:[0,1,0]
	v_fma_mixlo_f16 v44, v44, v49, 0 op_sel_hi:[0,1,0]
	ds_write_b16 v68, v44 offset:18656
	s_waitcnt lgkmcnt(0)
	s_load_dwordx16 s[36:51], s[54:55], 0x800
	s_load_dwordx16 s[72:87], s[54:55], 0x840
	v_cvt_f32_f16_sdwa v44, v53 dst_sel:DWORD dst_unused:UNUSED_PAD src0_sel:WORD_1
	v_cvt_f32_f16_sdwa v46, v45 dst_sel:DWORD dst_unused:UNUSED_PAD src0_sel:WORD_1
	v_pk_mul_f32 v[52:53], v[44:45], v[14:15] op_sel_hi:[0,1]
	v_pk_mul_f32 v[134:135], v[44:45], v[16:17] op_sel_hi:[0,1]
	v_exp_f32_e32 v52, v52
	v_exp_f32_e32 v53, v53
	v_exp_f32_e32 v134, v134
	v_exp_f32_e32 v135, v135
	v_mul_f32_e32 v46, v44, v46
	v_pk_mul_f32 v[50:51], v[52:53], v[50:51]
	v_pk_mul_f32 v[52:53], v[134:135], v[130:131]
	v_pk_fma_f32 v[130:131], v[46:47], s[58:59], v[52:53] op_sel_hi:[0, 1, 1]
	v_pk_mul_f32 v[52:53], v[44:45], v[10:11] op_sel_hi:[0,1]
	v_pk_fma_f32 v[136:137], v[46:47], s[56:57], v[50:51] op_sel_hi:[0, 1, 1]
	v_exp_f32_e32 v52, v52
	v_exp_f32_e32 v53, v53
	v_pk_mul_f32 v[54:55], v[44:45], v[12:13] op_sel_hi:[0,1]
	v_exp_f32_e32 v54, v54
	v_exp_f32_e32 v55, v55
	v_pk_fma_f32 v[50:51], s[88:89], v[136:137], 0 op_sel_hi:[1, 1, 0]
	v_pk_mul_f32 v[52:53], v[52:53], v[132:133]
	v_pk_fma_f32 v[50:51], s[90:91], v[130:131], v[50:51]
	v_pk_fma_f32 v[132:133], v[46:47], s[60:61], v[52:53] op_sel_hi:[0, 1, 1]
	v_pk_mul_f32 v[52:53], v[54:55], v[122:123]
	v_pk_fma_f32 v[50:51], s[92:93], v[132:133], v[50:51]
	v_pk_fma_f32 v[110:111], v[46:47], s[62:63], v[52:53] op_sel_hi:[0, 1, 1]
	v_pk_mul_f32 v[52:53], v[44:45], v[6:7] op_sel_hi:[0,1]
	v_exp_f32_e32 v52, v52
	v_exp_f32_e32 v53, v53
	v_pk_mul_f32 v[54:55], v[44:45], v[8:9] op_sel_hi:[0,1]
	v_exp_f32_e32 v54, v54
	v_exp_f32_e32 v55, v55
	v_pk_mul_f32 v[52:53], v[52:53], v[124:125]
	v_pk_fma_f32 v[50:51], s[94:95], v[110:111], v[50:51]
	v_pk_fma_f32 v[112:113], v[46:47], s[64:65], v[52:53] op_sel_hi:[0, 1, 1]
	v_pk_mul_f32 v[52:53], v[54:55], v[126:127]
	v_pk_fma_f32 v[50:51], s[96:97], v[112:113], v[50:51]
	v_pk_fma_f32 v[114:115], v[46:47], s[66:67], v[52:53] op_sel_hi:[0, 1, 1]
	v_pk_mul_f32 v[52:53], v[44:45], v[2:3] op_sel_hi:[0,1]
	v_exp_f32_e32 v52, v52
	v_exp_f32_e32 v53, v53
	v_pk_mul_f32 v[54:55], v[44:45], v[4:5] op_sel_hi:[0,1]
	v_exp_f32_e32 v54, v54
	v_exp_f32_e32 v55, v55
	v_pk_mul_f32 v[52:53], v[52:53], v[128:129]
	v_pk_fma_f32 v[50:51], s[98:99], v[114:115], v[50:51]
	v_pk_fma_f32 v[116:117], v[46:47], s[68:69], v[52:53] op_sel_hi:[0, 1, 1]
	v_pk_mul_f32 v[42:43], v[54:55], v[42:43]
	v_pk_fma_f32 v[50:51], s[20:21], v[116:117], v[50:51]
	v_pk_fma_f32 v[118:119], v[46:47], s[70:71], v[42:43] op_sel_hi:[0, 1, 1]
	v_pk_fma_f32 v[42:43], s[22:23], v[118:119], v[50:51]
	s_nop 0
	v_add_f32_e32 v42, v42, v43
	v_fma_mix_f32 v42, v1, v45, v42 op_sel:[0,1,0] op_sel_hi:[0,1,0]
	v_fma_mixlo_f16 v42, v42, v49, 0 op_sel:[0,1,0] op_sel_hi:[0,1,0]
	ds_write_b16 v68, v42 offset:19696
	s_waitcnt lgkmcnt(0)
	s_load_dwordx16 s[56:71], s[54:55], 0x880
	s_load_dwordx8 s[88:95], s[54:55], 0x8c0
	s_load_dwordx4 s[96:99], s[54:55], 0x8e0
	s_load_dwordx4 s[20:23], s[54:55], 0x8f0
	s_waitcnt vmcnt(5)
	v_cvt_f32_f16_e32 v120, v38
	s_waitcnt vmcnt(4)
	v_cvt_f32_f16_e32 v69, v30
	v_pk_mul_f32 v[124:125], v[120:121], v[14:15] op_sel_hi:[0,1]
	v_exp_f32_e32 v124, v124
	v_exp_f32_e32 v125, v125
	v_pk_mul_f32 v[126:127], v[120:121], v[16:17] op_sel_hi:[0,1]
	v_exp_f32_e32 v126, v126
	v_exp_f32_e32 v127, v127
	v_mul_f32_e32 v122, v120, v69
	v_pk_mul_f32 v[124:125], v[124:125], v[136:137]
	v_pk_fma_f32 v[124:125], v[122:123], s[36:37], v[124:125] op_sel_hi:[0, 1, 1]
	v_pk_fma_f32 v[70:71], s[72:73], v[124:125], 0 op_sel_hi:[1, 1, 0]
	v_pk_mul_f32 v[86:87], v[126:127], v[130:131]
	s_nop 0
	v_pk_fma_f32 v[126:127], v[122:123], s[38:39], v[86:87] op_sel_hi:[0, 1, 1]
	v_pk_mul_f32 v[72:73], v[120:121], v[10:11] op_sel_hi:[0,1]
	v_exp_f32_e32 v72, v72
	v_exp_f32_e32 v73, v73
	v_pk_mul_f32 v[86:87], v[120:121], v[12:13] op_sel_hi:[0,1]
	v_exp_f32_e32 v86, v86
	v_exp_f32_e32 v87, v87
	v_pk_mul_f32 v[72:73], v[72:73], v[132:133]
	v_pk_fma_f32 v[70:71], s[74:75], v[126:127], v[70:71]
	v_pk_fma_f32 v[128:129], v[122:123], s[40:41], v[72:73] op_sel_hi:[0, 1, 1]
	v_pk_mul_f32 v[72:73], v[86:87], v[110:111]
	v_pk_mul_f32 v[74:75], v[120:121], v[8:9] op_sel_hi:[0,1]
	v_pk_fma_f32 v[110:111], v[122:123], s[42:43], v[72:73] op_sel_hi:[0, 1, 1]
	v_pk_mul_f32 v[72:73], v[120:121], v[6:7] op_sel_hi:[0,1]
	v_exp_f32_e32 v72, v72
	v_exp_f32_e32 v73, v73
	v_exp_f32_e32 v74, v74
	v_exp_f32_e32 v75, v75
	v_pk_fma_f32 v[70:71], s[76:77], v[128:129], v[70:71]
	v_pk_mul_f32 v[72:73], v[72:73], v[112:113]
	v_pk_fma_f32 v[70:71], s[78:79], v[110:111], v[70:71]
	v_pk_fma_f32 v[112:113], v[122:123], s[44:45], v[72:73] op_sel_hi:[0, 1, 1]
	v_pk_mul_f32 v[72:73], v[74:75], v[114:115]
	v_pk_mul_f32 v[74:75], v[120:121], v[4:5] op_sel_hi:[0,1]
	v_pk_fma_f32 v[114:115], v[122:123], s[46:47], v[72:73] op_sel_hi:[0, 1, 1]
	v_pk_mul_f32 v[72:73], v[120:121], v[2:3] op_sel_hi:[0,1]
	v_exp_f32_e32 v72, v72
	v_exp_f32_e32 v73, v73
	v_exp_f32_e32 v74, v74
	v_exp_f32_e32 v75, v75
	v_pk_fma_f32 v[70:71], s[80:81], v[112:113], v[70:71]
	v_pk_mul_f32 v[72:73], v[72:73], v[116:117]
	v_pk_fma_f32 v[70:71], s[82:83], v[114:115], v[70:71]
	v_pk_fma_f32 v[116:117], v[122:123], s[48:49], v[72:73] op_sel_hi:[0, 1, 1]
	v_pk_mul_f32 v[72:73], v[74:75], v[118:119]
	v_pk_fma_f32 v[70:71], s[84:85], v[116:117], v[70:71]
	v_pk_fma_f32 v[118:119], v[122:123], s[50:51], v[72:73] op_sel_hi:[0, 1, 1]
	v_pk_fma_f32 v[70:71], s[86:87], v[118:119], v[70:71]
	s_nop 0
	v_add_f32_e32 v69, v70, v71
	v_fma_mix_f32 v69, v1, v30, v69 op_sel_hi:[0,1,0]
	s_waitcnt vmcnt(3)
	v_fma_mixlo_f16 v69, v69, v34, 0 op_sel_hi:[0,1,0]
	ds_write_b16 v68, v69 offset:20736
	s_waitcnt lgkmcnt(0)
	s_load_dwordx16 s[36:51], s[54:55], 0x900
	s_load_dwordx16 s[72:87], s[54:55], 0x940
	v_cvt_f32_f16_sdwa v38, v38 dst_sel:DWORD dst_unused:UNUSED_PAD src0_sel:WORD_1
	v_cvt_f32_f16_sdwa v69, v30 dst_sel:DWORD dst_unused:UNUSED_PAD src0_sel:WORD_1
	v_pk_mul_f32 v[122:123], v[38:39], v[14:15] op_sel_hi:[0,1]
	v_exp_f32_e32 v122, v122
	v_exp_f32_e32 v123, v123
	v_pk_mul_f32 v[130:131], v[38:39], v[16:17] op_sel_hi:[0,1]
	v_exp_f32_e32 v130, v130
	v_exp_f32_e32 v131, v131
	v_mul_f32_e32 v120, v38, v69
	v_pk_mul_f32 v[122:123], v[122:123], v[124:125]
	v_pk_fma_f32 v[122:123], v[120:121], s[56:57], v[122:123] op_sel_hi:[0, 1, 1]
	v_pk_fma_f32 v[42:43], s[88:89], v[122:123], 0 op_sel_hi:[1, 1, 0]
	v_pk_mul_f32 v[58:59], v[130:131], v[126:127]
	s_nop 0
	v_pk_fma_f32 v[124:125], v[120:121], s[58:59], v[58:59] op_sel_hi:[0, 1, 1]
	v_pk_mul_f32 v[44:45], v[38:39], v[10:11] op_sel_hi:[0,1]
	v_exp_f32_e32 v44, v44
	v_exp_f32_e32 v45, v45
	v_pk_mul_f32 v[58:59], v[38:39], v[12:13] op_sel_hi:[0,1]
	v_exp_f32_e32 v58, v58
	v_exp_f32_e32 v59, v59
	v_pk_mul_f32 v[44:45], v[44:45], v[128:129]
	v_pk_fma_f32 v[42:43], s[90:91], v[124:125], v[42:43]
	v_pk_fma_f32 v[126:127], v[120:121], s[60:61], v[44:45] op_sel_hi:[0, 1, 1]
	v_pk_mul_f32 v[44:45], v[58:59], v[110:111]
	v_pk_mul_f32 v[46:47], v[38:39], v[8:9] op_sel_hi:[0,1]
	v_pk_fma_f32 v[110:111], v[120:121], s[62:63], v[44:45] op_sel_hi:[0, 1, 1]
	v_pk_mul_f32 v[44:45], v[38:39], v[6:7] op_sel_hi:[0,1]
	v_exp_f32_e32 v44, v44
	v_exp_f32_e32 v45, v45
	v_exp_f32_e32 v46, v46
	v_exp_f32_e32 v47, v47
	v_pk_fma_f32 v[42:43], s[92:93], v[126:127], v[42:43]
	v_pk_mul_f32 v[44:45], v[44:45], v[112:113]
	v_pk_fma_f32 v[42:43], s[94:95], v[110:111], v[42:43]
	v_pk_fma_f32 v[112:113], v[120:121], s[64:65], v[44:45] op_sel_hi:[0, 1, 1]
	v_pk_mul_f32 v[44:45], v[46:47], v[114:115]
	v_pk_mul_f32 v[46:47], v[38:39], v[4:5] op_sel_hi:[0,1]
	v_pk_fma_f32 v[114:115], v[120:121], s[66:67], v[44:45] op_sel_hi:[0, 1, 1]
	v_pk_mul_f32 v[44:45], v[38:39], v[2:3] op_sel_hi:[0,1]
	v_exp_f32_e32 v44, v44
	v_exp_f32_e32 v45, v45
	v_exp_f32_e32 v46, v46
	v_exp_f32_e32 v47, v47
	v_pk_fma_f32 v[42:43], s[96:97], v[112:113], v[42:43]
	v_pk_mul_f32 v[44:45], v[44:45], v[116:117]
	v_pk_fma_f32 v[42:43], s[98:99], v[114:115], v[42:43]
	v_pk_fma_f32 v[116:117], v[120:121], s[68:69], v[44:45] op_sel_hi:[0, 1, 1]
	v_pk_mul_f32 v[44:45], v[46:47], v[118:119]
	v_pk_fma_f32 v[42:43], s[20:21], v[116:117], v[42:43]
	v_pk_fma_f32 v[118:119], v[120:121], s[70:71], v[44:45] op_sel_hi:[0, 1, 1]
	v_pk_fma_f32 v[42:43], s[22:23], v[118:119], v[42:43]
	s_nop 0
	v_add_f32_e32 v38, v42, v43
	v_fma_mix_f32 v30, v1, v30, v38 op_sel:[0,1,0] op_sel_hi:[0,1,0]
	v_fma_mixlo_f16 v30, v30, v34, 0 op_sel:[0,1,0] op_sel_hi:[0,1,0]
	ds_write_b16 v68, v30 offset:21776
	s_waitcnt lgkmcnt(0)
	s_load_dwordx16 s[56:71], s[54:55], 0x980
	s_load_dwordx8 s[88:95], s[54:55], 0x9c0
	s_load_dwordx4 s[96:99], s[54:55], 0x9e0
	s_load_dwordx4 s[20:23], s[54:55], 0x9f0
	v_cvt_f32_f16_e32 v30, v39
	v_cvt_f32_f16_e32 v34, v31
	v_pk_mul_f32 v[120:121], v[30:31], v[14:15] op_sel_hi:[0,1]
	v_exp_f32_e32 v120, v120
	v_exp_f32_e32 v121, v121
	v_pk_mul_f32 v[128:129], v[30:31], v[16:17] op_sel_hi:[0,1]
	v_exp_f32_e32 v128, v128
	v_exp_f32_e32 v129, v129
	v_mul_f32_e32 v34, v30, v34
	v_pk_mul_f32 v[120:121], v[120:121], v[122:123]
	v_pk_fma_f32 v[120:121], v[34:35], s[36:37], v[120:121] op_sel_hi:[0, 1, 1]
	v_pk_fma_f32 v[70:71], s[72:73], v[120:121], 0 op_sel_hi:[1, 1, 0]
	v_pk_mul_f32 v[86:87], v[128:129], v[124:125]
	s_nop 0
	v_pk_fma_f32 v[122:123], v[34:35], s[38:39], v[86:87] op_sel_hi:[0, 1, 1]
	v_pk_mul_f32 v[72:73], v[30:31], v[10:11] op_sel_hi:[0,1]
	v_exp_f32_e32 v72, v72
	v_exp_f32_e32 v73, v73
	v_pk_mul_f32 v[86:87], v[30:31], v[12:13] op_sel_hi:[0,1]
	v_exp_f32_e32 v86, v86
	v_exp_f32_e32 v87, v87
	v_pk_mul_f32 v[72:73], v[72:73], v[126:127]
	v_pk_fma_f32 v[70:71], s[74:75], v[122:123], v[70:71]
	v_pk_fma_f32 v[124:125], v[34:35], s[40:41], v[72:73] op_sel_hi:[0, 1, 1]
	v_pk_mul_f32 v[72:73], v[86:87], v[110:111]
	v_pk_mul_f32 v[74:75], v[30:31], v[8:9] op_sel_hi:[0,1]
	v_pk_fma_f32 v[110:111], v[34:35], s[42:43], v[72:73] op_sel_hi:[0, 1, 1]
	v_pk_mul_f32 v[72:73], v[30:31], v[6:7] op_sel_hi:[0,1]
	v_exp_f32_e32 v72, v72
	v_exp_f32_e32 v73, v73
	v_exp_f32_e32 v74, v74
	v_exp_f32_e32 v75, v75
	v_pk_fma_f32 v[70:71], s[76:77], v[124:125], v[70:71]
	v_pk_mul_f32 v[72:73], v[72:73], v[112:113]
	v_pk_fma_f32 v[70:71], s[78:79], v[110:111], v[70:71]
	v_pk_fma_f32 v[112:113], v[34:35], s[44:45], v[72:73] op_sel_hi:[0, 1, 1]
	v_pk_mul_f32 v[72:73], v[74:75], v[114:115]
	v_pk_mul_f32 v[74:75], v[30:31], v[4:5] op_sel_hi:[0,1]
	v_pk_fma_f32 v[114:115], v[34:35], s[46:47], v[72:73] op_sel_hi:[0, 1, 1]
	v_pk_mul_f32 v[72:73], v[30:31], v[2:3] op_sel_hi:[0,1]
	v_exp_f32_e32 v72, v72
	v_exp_f32_e32 v73, v73
	v_exp_f32_e32 v74, v74
	v_exp_f32_e32 v75, v75
	v_pk_fma_f32 v[70:71], s[80:81], v[112:113], v[70:71]
	v_pk_mul_f32 v[72:73], v[72:73], v[116:117]
	v_pk_fma_f32 v[70:71], s[82:83], v[114:115], v[70:71]
	v_pk_fma_f32 v[116:117], v[34:35], s[48:49], v[72:73] op_sel_hi:[0, 1, 1]
	v_pk_mul_f32 v[72:73], v[74:75], v[118:119]
	v_pk_fma_f32 v[70:71], s[84:85], v[116:117], v[70:71]
	v_pk_fma_f32 v[118:119], v[34:35], s[50:51], v[72:73] op_sel_hi:[0, 1, 1]
	v_pk_fma_f32 v[70:71], s[86:87], v[118:119], v[70:71]
	s_nop 0
	v_add_f32_e32 v30, v70, v71
	v_fma_mix_f32 v30, v1, v31, v30 op_sel_hi:[0,1,0]
	v_fma_mixlo_f16 v30, v30, v35, 0 op_sel_hi:[0,1,0]
	ds_write_b16 v68, v30 offset:22816
	s_waitcnt lgkmcnt(0)
	s_load_dwordx16 s[36:51], s[54:55], 0xa00
	s_load_dwordx16 s[72:87], s[54:55], 0xa40
	v_cvt_f32_f16_sdwa v30, v39 dst_sel:DWORD dst_unused:UNUSED_PAD src0_sel:WORD_1
	v_cvt_f32_f16_sdwa v34, v31 dst_sel:DWORD dst_unused:UNUSED_PAD src0_sel:WORD_1
	v_pk_mul_f32 v[38:39], v[30:31], v[14:15] op_sel_hi:[0,1]
	v_exp_f32_e32 v38, v38
	v_exp_f32_e32 v39, v39
	v_pk_mul_f32 v[126:127], v[30:31], v[16:17] op_sel_hi:[0,1]
	v_exp_f32_e32 v126, v126
	v_exp_f32_e32 v127, v127
	v_mul_f32_e32 v34, v30, v34
	v_pk_mul_f32 v[38:39], v[38:39], v[120:121]
	v_pk_fma_f32 v[38:39], v[34:35], s[56:57], v[38:39] op_sel_hi:[0, 1, 1]
	v_pk_fma_f32 v[42:43], s[88:89], v[38:39], 0 op_sel_hi:[1, 1, 0]
	v_pk_mul_f32 v[58:59], v[126:127], v[122:123]
	s_nop 0
	v_pk_fma_f32 v[120:121], v[34:35], s[58:59], v[58:59] op_sel_hi:[0, 1, 1]
	v_pk_mul_f32 v[44:45], v[30:31], v[10:11] op_sel_hi:[0,1]
	v_exp_f32_e32 v44, v44
	v_exp_f32_e32 v45, v45
	v_pk_mul_f32 v[58:59], v[30:31], v[12:13] op_sel_hi:[0,1]
	v_exp_f32_e32 v58, v58
	v_exp_f32_e32 v59, v59
	v_pk_mul_f32 v[44:45], v[44:45], v[124:125]
	v_pk_fma_f32 v[42:43], s[90:91], v[120:121], v[42:43]
	v_pk_fma_f32 v[122:123], v[34:35], s[60:61], v[44:45] op_sel_hi:[0, 1, 1]
	v_pk_mul_f32 v[44:45], v[58:59], v[110:111]
	v_pk_mul_f32 v[46:47], v[30:31], v[8:9] op_sel_hi:[0,1]
	v_pk_fma_f32 v[110:111], v[34:35], s[62:63], v[44:45] op_sel_hi:[0, 1, 1]
	v_pk_mul_f32 v[44:45], v[30:31], v[6:7] op_sel_hi:[0,1]
	v_exp_f32_e32 v44, v44
	v_exp_f32_e32 v45, v45
	v_exp_f32_e32 v46, v46
	v_exp_f32_e32 v47, v47
	v_pk_fma_f32 v[42:43], s[92:93], v[122:123], v[42:43]
	v_pk_mul_f32 v[44:45], v[44:45], v[112:113]
	v_pk_fma_f32 v[42:43], s[94:95], v[110:111], v[42:43]
	v_pk_fma_f32 v[112:113], v[34:35], s[64:65], v[44:45] op_sel_hi:[0, 1, 1]
	v_pk_mul_f32 v[44:45], v[46:47], v[114:115]
	v_pk_mul_f32 v[46:47], v[30:31], v[4:5] op_sel_hi:[0,1]
	v_pk_fma_f32 v[114:115], v[34:35], s[66:67], v[44:45] op_sel_hi:[0, 1, 1]
	v_pk_mul_f32 v[44:45], v[30:31], v[2:3] op_sel_hi:[0,1]
	v_exp_f32_e32 v44, v44
	v_exp_f32_e32 v45, v45
	v_exp_f32_e32 v46, v46
	v_exp_f32_e32 v47, v47
	v_pk_fma_f32 v[42:43], s[96:97], v[112:113], v[42:43]
	v_pk_mul_f32 v[44:45], v[44:45], v[116:117]
	v_pk_fma_f32 v[42:43], s[98:99], v[114:115], v[42:43]
	v_pk_fma_f32 v[116:117], v[34:35], s[68:69], v[44:45] op_sel_hi:[0, 1, 1]
	v_pk_mul_f32 v[44:45], v[46:47], v[118:119]
	v_pk_fma_f32 v[42:43], s[20:21], v[116:117], v[42:43]
	v_pk_fma_f32 v[118:119], v[34:35], s[70:71], v[44:45] op_sel_hi:[0, 1, 1]
	v_pk_fma_f32 v[42:43], s[22:23], v[118:119], v[42:43]
	s_nop 0
	v_add_f32_e32 v30, v42, v43
	v_fma_mix_f32 v30, v1, v31, v30 op_sel:[0,1,0] op_sel_hi:[0,1,0]
	v_fma_mixlo_f16 v30, v30, v35, 0 op_sel:[0,1,0] op_sel_hi:[0,1,0]
	ds_write_b16 v68, v30 offset:23856
	s_waitcnt lgkmcnt(0)
	s_load_dwordx16 s[56:71], s[54:55], 0xa80
	s_load_dwordx8 s[88:95], s[54:55], 0xac0
	s_load_dwordx4 s[96:99], s[54:55], 0xae0
	s_load_dwordx4 s[20:23], s[54:55], 0xaf0
	v_cvt_f32_f16_e32 v30, v40
	v_cvt_f32_f16_e32 v31, v32
	v_pk_mul_f32 v[124:125], v[30:31], v[14:15] op_sel_hi:[0,1]
	v_exp_f32_e32 v124, v124
	v_exp_f32_e32 v125, v125
	v_pk_mul_f32 v[126:127], v[30:31], v[16:17] op_sel_hi:[0,1]
	v_exp_f32_e32 v126, v126
	v_exp_f32_e32 v127, v127
	v_mul_f32_e32 v34, v30, v31
	v_pk_mul_f32 v[38:39], v[124:125], v[38:39]
	v_pk_fma_f32 v[38:39], v[34:35], s[36:37], v[38:39] op_sel_hi:[0, 1, 1]
	v_pk_fma_f32 v[70:71], s[72:73], v[38:39], 0 op_sel_hi:[1, 1, 0]
	v_pk_mul_f32 v[86:87], v[126:127], v[120:121]
	s_nop 0
	v_pk_fma_f32 v[120:121], v[34:35], s[38:39], v[86:87] op_sel_hi:[0, 1, 1]
	v_pk_mul_f32 v[72:73], v[30:31], v[10:11] op_sel_hi:[0,1]
	v_exp_f32_e32 v72, v72
	v_exp_f32_e32 v73, v73
	v_pk_mul_f32 v[86:87], v[30:31], v[12:13] op_sel_hi:[0,1]
	v_exp_f32_e32 v86, v86
	v_exp_f32_e32 v87, v87
	v_pk_mul_f32 v[72:73], v[72:73], v[122:123]
	v_pk_fma_f32 v[70:71], s[74:75], v[120:121], v[70:71]
	v_pk_fma_f32 v[122:123], v[34:35], s[40:41], v[72:73] op_sel_hi:[0, 1, 1]
	v_pk_mul_f32 v[72:73], v[86:87], v[110:111]
	v_pk_mul_f32 v[74:75], v[30:31], v[8:9] op_sel_hi:[0,1]
	v_pk_fma_f32 v[110:111], v[34:35], s[42:43], v[72:73] op_sel_hi:[0, 1, 1]
	v_pk_mul_f32 v[72:73], v[30:31], v[6:7] op_sel_hi:[0,1]
	v_exp_f32_e32 v72, v72
	v_exp_f32_e32 v73, v73
	v_exp_f32_e32 v74, v74
	v_exp_f32_e32 v75, v75
	v_pk_fma_f32 v[70:71], s[76:77], v[122:123], v[70:71]
	v_pk_mul_f32 v[72:73], v[72:73], v[112:113]
	v_pk_fma_f32 v[70:71], s[78:79], v[110:111], v[70:71]
	v_pk_fma_f32 v[112:113], v[34:35], s[44:45], v[72:73] op_sel_hi:[0, 1, 1]
	v_pk_mul_f32 v[72:73], v[74:75], v[114:115]
	v_pk_fma_f32 v[70:71], s[80:81], v[112:113], v[70:71]
	v_pk_fma_f32 v[114:115], v[34:35], s[46:47], v[72:73] op_sel_hi:[0, 1, 1]
	v_pk_mul_f32 v[72:73], v[30:31], v[2:3] op_sel_hi:[0,1]
	v_exp_f32_e32 v72, v72
	v_exp_f32_e32 v73, v73
	v_pk_mul_f32 v[30:31], v[30:31], v[4:5] op_sel_hi:[0,1]
	v_exp_f32_e32 v30, v30
	v_exp_f32_e32 v31, v31
	v_pk_mul_f32 v[72:73], v[72:73], v[116:117]
	v_pk_fma_f32 v[70:71], s[82:83], v[114:115], v[70:71]
	v_pk_fma_f32 v[116:117], v[34:35], s[48:49], v[72:73] op_sel_hi:[0, 1, 1]
	v_pk_mul_f32 v[30:31], v[30:31], v[118:119]
	v_pk_fma_f32 v[70:71], s[84:85], v[116:117], v[70:71]
	v_pk_fma_f32 v[30:31], v[34:35], s[50:51], v[30:31] op_sel_hi:[0, 1, 1]
	v_pk_fma_f32 v[34:35], s[86:87], v[30:31], v[70:71]
	s_nop 0
	v_add_f32_e32 v34, v34, v35
	v_fma_mix_f32 v34, v1, v32, v34 op_sel_hi:[0,1,0]
	v_fma_mixlo_f16 v34, v34, v36, 0 op_sel_hi:[0,1,0]
	ds_write_b16 v68, v34 offset:24896
	s_waitcnt lgkmcnt(0)
	s_load_dwordx16 s[36:51], s[54:55], 0xb00
	s_load_dwordx16 s[72:87], s[54:55], 0xb40
	v_cvt_f32_f16_sdwa v34, v40 dst_sel:DWORD dst_unused:UNUSED_PAD src0_sel:WORD_1
	v_cvt_f32_f16_sdwa v35, v32 dst_sel:DWORD dst_unused:UNUSED_PAD src0_sel:WORD_1
	v_pk_mul_f32 v[118:119], v[34:35], v[14:15] op_sel_hi:[0,1]
	v_exp_f32_e32 v118, v118
	v_exp_f32_e32 v119, v119
	v_pk_mul_f32 v[124:125], v[34:35], v[16:17] op_sel_hi:[0,1]
	v_exp_f32_e32 v124, v124
	v_exp_f32_e32 v125, v125
	v_mul_f32_e32 v40, v34, v35
	v_pk_mul_f32 v[38:39], v[118:119], v[38:39]
	v_pk_fma_f32 v[38:39], v[40:41], s[56:57], v[38:39] op_sel_hi:[0, 1, 1]
	v_pk_fma_f32 v[42:43], s[88:89], v[38:39], 0 op_sel_hi:[1, 1, 0]
	v_pk_mul_f32 v[58:59], v[124:125], v[120:121]
	s_nop 0
	v_pk_fma_f32 v[118:119], v[40:41], s[58:59], v[58:59] op_sel_hi:[0, 1, 1]
	v_pk_mul_f32 v[44:45], v[34:35], v[10:11] op_sel_hi:[0,1]
	v_exp_f32_e32 v44, v44
	v_exp_f32_e32 v45, v45
	v_pk_mul_f32 v[58:59], v[34:35], v[12:13] op_sel_hi:[0,1]
	v_exp_f32_e32 v58, v58
	v_exp_f32_e32 v59, v59
	v_pk_mul_f32 v[44:45], v[44:45], v[122:123]
	v_pk_fma_f32 v[42:43], s[90:91], v[118:119], v[42:43]
	v_pk_fma_f32 v[120:121], v[40:41], s[60:61], v[44:45] op_sel_hi:[0, 1, 1]
	v_pk_mul_f32 v[44:45], v[58:59], v[110:111]
	v_pk_mul_f32 v[46:47], v[34:35], v[8:9] op_sel_hi:[0,1]
	v_pk_fma_f32 v[110:111], v[40:41], s[62:63], v[44:45] op_sel_hi:[0, 1, 1]
	v_pk_mul_f32 v[44:45], v[34:35], v[6:7] op_sel_hi:[0,1]
	v_exp_f32_e32 v44, v44
	v_exp_f32_e32 v45, v45
	v_exp_f32_e32 v46, v46
	v_exp_f32_e32 v47, v47
	v_pk_fma_f32 v[42:43], s[92:93], v[120:121], v[42:43]
	v_pk_mul_f32 v[44:45], v[44:45], v[112:113]
	v_pk_fma_f32 v[42:43], s[94:95], v[110:111], v[42:43]
	v_pk_fma_f32 v[112:113], v[40:41], s[64:65], v[44:45] op_sel_hi:[0, 1, 1]
	v_pk_mul_f32 v[44:45], v[46:47], v[114:115]
	v_pk_fma_f32 v[42:43], s[96:97], v[112:113], v[42:43]
	v_pk_fma_f32 v[114:115], v[40:41], s[66:67], v[44:45] op_sel_hi:[0, 1, 1]
	v_pk_mul_f32 v[44:45], v[34:35], v[2:3] op_sel_hi:[0,1]
	v_exp_f32_e32 v44, v44
	v_exp_f32_e32 v45, v45
	v_pk_mul_f32 v[34:35], v[34:35], v[4:5] op_sel_hi:[0,1]
	v_exp_f32_e32 v34, v34
	v_exp_f32_e32 v35, v35
	v_pk_mul_f32 v[44:45], v[44:45], v[116:117]
	v_pk_fma_f32 v[42:43], s[98:99], v[114:115], v[42:43]
	v_pk_fma_f32 v[116:117], v[40:41], s[68:69], v[44:45] op_sel_hi:[0, 1, 1]
	v_pk_mul_f32 v[30:31], v[34:35], v[30:31]
	v_pk_fma_f32 v[42:43], s[20:21], v[116:117], v[42:43]
	v_pk_fma_f32 v[30:31], v[40:41], s[70:71], v[30:31] op_sel_hi:[0, 1, 1]
	v_pk_fma_f32 v[34:35], s[22:23], v[30:31], v[42:43]
	s_nop 0
	v_add_f32_e32 v34, v34, v35
	v_fma_mix_f32 v32, v1, v32, v34 op_sel:[0,1,0] op_sel_hi:[0,1,0]
	v_fma_mixlo_f16 v32, v32, v36, 0 op_sel:[0,1,0] op_sel_hi:[0,1,0]
	ds_write_b16 v68, v32 offset:25936
	s_waitcnt lgkmcnt(0)
	s_load_dwordx16 s[56:71], s[54:55], 0xb80
	s_load_dwordx8 s[88:95], s[54:55], 0xbc0
	s_load_dwordx4 s[96:99], s[54:55], 0xbe0
	s_load_dwordx4 s[20:23], s[54:55], 0xbf0
	v_cvt_f32_f16_e32 v32, v41
	v_cvt_f32_f16_e32 v34, v33
	v_pk_mul_f32 v[122:123], v[32:33], v[14:15] op_sel_hi:[0,1]
	v_exp_f32_e32 v122, v122
	v_exp_f32_e32 v123, v123
	v_pk_mul_f32 v[124:125], v[32:33], v[16:17] op_sel_hi:[0,1]
	v_exp_f32_e32 v124, v124
	v_exp_f32_e32 v125, v125
	v_mul_f32_e32 v34, v32, v34
	v_pk_mul_f32 v[38:39], v[122:123], v[38:39]
	v_pk_fma_f32 v[38:39], v[34:35], s[36:37], v[38:39] op_sel_hi:[0, 1, 1]
	v_pk_fma_f32 v[70:71], s[72:73], v[38:39], 0 op_sel_hi:[1, 1, 0]
	v_pk_mul_f32 v[86:87], v[124:125], v[118:119]
	s_nop 0
	v_pk_fma_f32 v[118:119], v[34:35], s[38:39], v[86:87] op_sel_hi:[0, 1, 1]
	v_pk_mul_f32 v[72:73], v[32:33], v[10:11] op_sel_hi:[0,1]
	v_exp_f32_e32 v72, v72
	v_exp_f32_e32 v73, v73
	v_pk_mul_f32 v[86:87], v[32:33], v[12:13] op_sel_hi:[0,1]
	v_exp_f32_e32 v86, v86
	v_exp_f32_e32 v87, v87
	v_pk_mul_f32 v[72:73], v[72:73], v[120:121]
	v_pk_fma_f32 v[70:71], s[74:75], v[118:119], v[70:71]
	v_pk_fma_f32 v[120:121], v[34:35], s[40:41], v[72:73] op_sel_hi:[0, 1, 1]
	v_pk_mul_f32 v[72:73], v[86:87], v[110:111]
	v_pk_mul_f32 v[74:75], v[32:33], v[8:9] op_sel_hi:[0,1]
	v_pk_fma_f32 v[110:111], v[34:35], s[42:43], v[72:73] op_sel_hi:[0, 1, 1]
	v_pk_mul_f32 v[72:73], v[32:33], v[6:7] op_sel_hi:[0,1]
	v_exp_f32_e32 v72, v72
	v_exp_f32_e32 v73, v73
	v_exp_f32_e32 v74, v74
	v_exp_f32_e32 v75, v75
	v_pk_fma_f32 v[70:71], s[76:77], v[120:121], v[70:71]
	v_pk_mul_f32 v[72:73], v[72:73], v[112:113]
	v_pk_fma_f32 v[70:71], s[78:79], v[110:111], v[70:71]
	v_pk_fma_f32 v[112:113], v[34:35], s[44:45], v[72:73] op_sel_hi:[0, 1, 1]
	v_pk_mul_f32 v[72:73], v[74:75], v[114:115]
	v_pk_mul_f32 v[74:75], v[32:33], v[4:5] op_sel_hi:[0,1]
	v_pk_fma_f32 v[114:115], v[34:35], s[46:47], v[72:73] op_sel_hi:[0, 1, 1]
	v_pk_mul_f32 v[72:73], v[32:33], v[2:3] op_sel_hi:[0,1]
	v_exp_f32_e32 v72, v72
	v_exp_f32_e32 v73, v73
	v_exp_f32_e32 v74, v74
	v_exp_f32_e32 v75, v75
	v_pk_fma_f32 v[70:71], s[80:81], v[112:113], v[70:71]
	v_pk_mul_f32 v[72:73], v[72:73], v[116:117]
	v_pk_fma_f32 v[70:71], s[82:83], v[114:115], v[70:71]
	v_pk_fma_f32 v[116:117], v[34:35], s[48:49], v[72:73] op_sel_hi:[0, 1, 1]
	v_pk_mul_f32 v[30:31], v[74:75], v[30:31]
	v_pk_fma_f32 v[70:71], s[84:85], v[116:117], v[70:71]
	v_pk_fma_f32 v[30:31], v[34:35], s[50:51], v[30:31] op_sel_hi:[0, 1, 1]
	v_pk_fma_f32 v[34:35], s[86:87], v[30:31], v[70:71]
	s_nop 0
	v_add_f32_e32 v32, v34, v35
	v_fma_mix_f32 v32, v1, v33, v32 op_sel_hi:[0,1,0]
	v_fma_mixlo_f16 v32, v32, v37, 0 op_sel_hi:[0,1,0]
	ds_write_b16 v68, v32 offset:26976
	s_waitcnt lgkmcnt(0)
	s_load_dwordx16 s[36:51], s[54:55], 0xc00
	s_load_dwordx16 s[72:87], s[54:55], 0xc40
	v_cvt_f32_f16_sdwa v32, v41 dst_sel:DWORD dst_unused:UNUSED_PAD src0_sel:WORD_1
	v_cvt_f32_f16_sdwa v34, v33 dst_sel:DWORD dst_unused:UNUSED_PAD src0_sel:WORD_1
	v_pk_mul_f32 v[40:41], v[32:33], v[14:15] op_sel_hi:[0,1]
	v_pk_mul_f32 v[122:123], v[32:33], v[16:17] op_sel_hi:[0,1]
	v_exp_f32_e32 v40, v40
	v_exp_f32_e32 v41, v41
	v_exp_f32_e32 v122, v122
	v_exp_f32_e32 v123, v123
	v_mul_f32_e32 v34, v32, v34
	v_pk_mul_f32 v[38:39], v[40:41], v[38:39]
	v_pk_mul_f32 v[40:41], v[122:123], v[118:119]
	v_pk_fma_f32 v[118:119], v[34:35], s[58:59], v[40:41] op_sel_hi:[0, 1, 1]
	v_pk_mul_f32 v[40:41], v[32:33], v[10:11] op_sel_hi:[0,1]
	v_pk_fma_f32 v[124:125], v[34:35], s[56:57], v[38:39] op_sel_hi:[0, 1, 1]
	v_exp_f32_e32 v40, v40
	v_exp_f32_e32 v41, v41
	v_pk_mul_f32 v[42:43], v[32:33], v[12:13] op_sel_hi:[0,1]
	v_exp_f32_e32 v42, v42
	v_exp_f32_e32 v43, v43
	v_pk_fma_f32 v[38:39], s[88:89], v[124:125], 0 op_sel_hi:[1, 1, 0]
	v_pk_mul_f32 v[40:41], v[40:41], v[120:121]
	v_pk_fma_f32 v[38:39], s[90:91], v[118:119], v[38:39]
	v_pk_fma_f32 v[120:121], v[34:35], s[60:61], v[40:41] op_sel_hi:[0, 1, 1]
	v_pk_mul_f32 v[40:41], v[42:43], v[110:111]
	v_pk_fma_f32 v[38:39], s[92:93], v[120:121], v[38:39]
	v_pk_fma_f32 v[62:63], v[34:35], s[62:63], v[40:41] op_sel_hi:[0, 1, 1]
	v_pk_mul_f32 v[40:41], v[32:33], v[6:7] op_sel_hi:[0,1]
	v_exp_f32_e32 v40, v40
	v_exp_f32_e32 v41, v41
	v_pk_mul_f32 v[42:43], v[32:33], v[8:9] op_sel_hi:[0,1]
	v_exp_f32_e32 v42, v42
	v_exp_f32_e32 v43, v43
	v_pk_mul_f32 v[40:41], v[40:41], v[112:113]
	v_pk_fma_f32 v[38:39], s[94:95], v[62:63], v[38:39]
	v_pk_fma_f32 v[64:65], v[34:35], s[64:65], v[40:41] op_sel_hi:[0, 1, 1]
	v_pk_mul_f32 v[40:41], v[42:43], v[114:115]
	v_pk_fma_f32 v[38:39], s[96:97], v[64:65], v[38:39]
	v_pk_fma_f32 v[102:103], v[34:35], s[66:67], v[40:41] op_sel_hi:[0, 1, 1]
	v_pk_mul_f32 v[40:41], v[32:33], v[2:3] op_sel_hi:[0,1]
	v_exp_f32_e32 v40, v40
	v_exp_f32_e32 v41, v41
	v_pk_mul_f32 v[42:43], v[32:33], v[4:5] op_sel_hi:[0,1]
	v_exp_f32_e32 v42, v42
	v_exp_f32_e32 v43, v43
	v_pk_mul_f32 v[40:41], v[40:41], v[116:117]
	v_pk_fma_f32 v[38:39], s[98:99], v[102:103], v[38:39]
	v_pk_fma_f32 v[104:105], v[34:35], s[68:69], v[40:41] op_sel_hi:[0, 1, 1]
	v_pk_mul_f32 v[30:31], v[42:43], v[30:31]
	v_pk_fma_f32 v[38:39], s[20:21], v[104:105], v[38:39]
	v_pk_fma_f32 v[106:107], v[34:35], s[70:71], v[30:31] op_sel_hi:[0, 1, 1]
	v_pk_fma_f32 v[30:31], s[22:23], v[106:107], v[38:39]
	s_nop 0
	v_add_f32_e32 v30, v30, v31
	v_fma_mix_f32 v30, v1, v33, v30 op_sel:[0,1,0] op_sel_hi:[0,1,0]
	v_fma_mixlo_f16 v30, v30, v37, 0 op_sel:[0,1,0] op_sel_hi:[0,1,0]
	ds_write_b16 v68, v30 offset:28016
	s_waitcnt lgkmcnt(0)
	s_load_dwordx16 s[56:71], s[54:55], 0xc80
	s_load_dwordx8 s[88:95], s[54:55], 0xcc0
	s_load_dwordx4 s[96:99], s[54:55], 0xce0
	s_load_dwordx4 s[20:23], s[54:55], 0xcf0
	s_waitcnt vmcnt(2)
	v_cvt_f32_f16_e32 v108, v26
	s_waitcnt vmcnt(1)
	v_cvt_f32_f16_e32 v69, v18
	v_pk_mul_f32 v[112:113], v[108:109], v[14:15] op_sel_hi:[0,1]
	v_exp_f32_e32 v112, v112
	v_exp_f32_e32 v113, v113
	v_pk_mul_f32 v[114:115], v[108:109], v[16:17] op_sel_hi:[0,1]
	v_exp_f32_e32 v114, v114
	v_exp_f32_e32 v115, v115
	v_mul_f32_e32 v110, v108, v69
	v_pk_mul_f32 v[112:113], v[112:113], v[124:125]
	v_pk_fma_f32 v[112:113], v[110:111], s[36:37], v[112:113] op_sel_hi:[0, 1, 1]
	v_pk_fma_f32 v[70:71], s[72:73], v[112:113], 0 op_sel_hi:[1, 1, 0]
	v_pk_mul_f32 v[86:87], v[114:115], v[118:119]
	s_nop 0
	v_pk_fma_f32 v[114:115], v[110:111], s[38:39], v[86:87] op_sel_hi:[0, 1, 1]
	v_pk_mul_f32 v[72:73], v[108:109], v[10:11] op_sel_hi:[0,1]
	v_exp_f32_e32 v72, v72
	v_exp_f32_e32 v73, v73
	v_pk_mul_f32 v[86:87], v[108:109], v[12:13] op_sel_hi:[0,1]
	v_exp_f32_e32 v86, v86
	v_exp_f32_e32 v87, v87
	v_pk_mul_f32 v[72:73], v[72:73], v[120:121]
	v_pk_fma_f32 v[70:71], s[74:75], v[114:115], v[70:71]
	v_pk_fma_f32 v[116:117], v[110:111], s[40:41], v[72:73] op_sel_hi:[0, 1, 1]
	v_pk_mul_f32 v[62:63], v[86:87], v[62:63]
	v_pk_fma_f32 v[70:71], s[76:77], v[116:117], v[70:71]
	v_pk_fma_f32 v[118:119], v[110:111], s[42:43], v[62:63] op_sel_hi:[0, 1, 1]
	v_pk_fma_f32 v[62:63], s[78:79], v[118:119], v[70:71]
	v_pk_mul_f32 v[70:71], v[108:109], v[6:7] op_sel_hi:[0,1]
	v_exp_f32_e32 v70, v70
	v_exp_f32_e32 v71, v71
	v_pk_mul_f32 v[72:73], v[108:109], v[8:9] op_sel_hi:[0,1]
	v_exp_f32_e32 v72, v72
	v_exp_f32_e32 v73, v73
	v_pk_mul_f32 v[64:65], v[70:71], v[64:65]
	v_pk_mul_f32 v[70:71], v[108:109], v[4:5] op_sel_hi:[0,1]
	v_pk_fma_f32 v[120:121], v[110:111], s[44:45], v[64:65] op_sel_hi:[0, 1, 1]
	v_pk_mul_f32 v[64:65], v[72:73], v[102:103]
	v_exp_f32_e32 v70, v70
	v_pk_fma_f32 v[102:103], v[110:111], s[46:47], v[64:65] op_sel_hi:[0, 1, 1]
	v_pk_mul_f32 v[64:65], v[108:109], v[2:3] op_sel_hi:[0,1]
	v_exp_f32_e32 v64, v64
	v_exp_f32_e32 v65, v65
	v_exp_f32_e32 v71, v71
	v_pk_fma_f32 v[62:63], s[80:81], v[120:121], v[62:63]
	v_pk_mul_f32 v[64:65], v[64:65], v[104:105]
	v_pk_fma_f32 v[62:63], s[82:83], v[102:103], v[62:63]
	v_pk_fma_f32 v[104:105], v[110:111], s[48:49], v[64:65] op_sel_hi:[0, 1, 1]
	v_pk_mul_f32 v[64:65], v[70:71], v[106:107]
	v_pk_fma_f32 v[62:63], s[84:85], v[104:105], v[62:63]
	v_pk_fma_f32 v[98:99], v[110:111], s[50:51], v[64:65] op_sel_hi:[0, 1, 1]
	v_pk_fma_f32 v[62:63], s[86:87], v[98:99], v[62:63]
	s_nop 0
	v_add_f32_e32 v62, v62, v63
	v_fma_mix_f32 v62, v1, v18, v62 op_sel_hi:[0,1,0]
	s_waitcnt vmcnt(0)
	v_fma_mixlo_f16 v62, v62, v22, 0 op_sel_hi:[0,1,0]
	ds_write_b16 v68, v62 offset:29056
	v_lshrrev_b32_e32 v196, 6, v0
	v_and_b32_e32 v197, 48, v0
	v_lshl_or_b32 v196, v196, 7, v197
	v_and_b32_e32 v197, 15, v0
	v_or_b32_e32 v197, s28, v197
	v_lshl_or_b32 v196, v197, 10, v196
	v_add_u32_e32 v197, 0x4000, v196
	global_load_dwordx4 v[180:183], v196, s[4:5]
	global_load_dwordx4 v[184:187], v196, s[4:5] offset:64
	global_load_dwordx4 v[188:191], v197, s[4:5]
	global_load_dwordx4 v[192:195], v197, s[4:5] offset:64
	v_and_b32_e32 v196, 63, v0
	v_lshlrev_b32_e32 v196, 4, v196
	global_load_dwordx4 v[204:207], v196, s[6:7]
	global_load_dwordx4 v[208:211], v196, s[8:9]
	s_waitcnt lgkmcnt(0)
	s_load_dwordx16 s[36:51], s[54:55], 0xd00
	s_load_dwordx16 s[72:87], s[54:55], 0xd40
	v_cvt_f32_f16_sdwa v26, v26 dst_sel:DWORD dst_unused:UNUSED_PAD src0_sel:WORD_1
	v_cvt_f32_f16_sdwa v69, v18 dst_sel:DWORD dst_unused:UNUSED_PAD src0_sel:WORD_1
	v_pk_mul_f32 v[106:107], v[26:27], v[14:15] op_sel_hi:[0,1]
	v_exp_f32_e32 v106, v106
	v_exp_f32_e32 v107, v107
	v_pk_mul_f32 v[108:109], v[26:27], v[16:17] op_sel_hi:[0,1]
	v_exp_f32_e32 v108, v108
	v_exp_f32_e32 v109, v109
	v_mul_f32_e32 v100, v26, v69
	v_pk_mul_f32 v[106:107], v[106:107], v[112:113]
	v_pk_fma_f32 v[106:107], v[100:101], s[56:57], v[106:107] op_sel_hi:[0, 1, 1]
	v_pk_fma_f32 v[30:31], s[88:89], v[106:107], 0 op_sel_hi:[1, 1, 0]
	v_pk_mul_f32 v[46:47], v[108:109], v[114:115]
	s_nop 0
	v_pk_fma_f32 v[108:109], v[100:101], s[58:59], v[46:47] op_sel_hi:[0, 1, 1]
	v_pk_mul_f32 v[32:33], v[26:27], v[10:11] op_sel_hi:[0,1]
	v_exp_f32_e32 v32, v32
	v_exp_f32_e32 v33, v33
	v_pk_mul_f32 v[46:47], v[26:27], v[12:13] op_sel_hi:[0,1]
	v_exp_f32_e32 v46, v46
	v_exp_f32_e32 v47, v47
	v_pk_mul_f32 v[32:33], v[32:33], v[116:117]
	v_pk_fma_f32 v[30:31], s[90:91], v[108:109], v[30:31]
	v_pk_fma_f32 v[110:111], v[100:101], s[60:61], v[32:33] op_sel_hi:[0, 1, 1]
	v_pk_mul_f32 v[32:33], v[46:47], v[118:119]
	v_pk_mul_f32 v[34:35], v[26:27], v[8:9] op_sel_hi:[0,1]
	v_pk_fma_f32 v[112:113], v[100:101], s[62:63], v[32:33] op_sel_hi:[0, 1, 1]
	v_pk_mul_f32 v[32:33], v[26:27], v[6:7] op_sel_hi:[0,1]
	v_exp_f32_e32 v32, v32
	v_exp_f32_e32 v33, v33
	v_exp_f32_e32 v34, v34
	v_exp_f32_e32 v35, v35
	v_pk_fma_f32 v[30:31], s[92:93], v[110:111], v[30:31]
	v_pk_mul_f32 v[32:33], v[32:33], v[120:121]
	v_pk_fma_f32 v[30:31], s[94:95], v[112:113], v[30:31]
	v_pk_fma_f32 v[114:115], v[100:101], s[64:65], v[32:33] op_sel_hi:[0, 1, 1]
	v_pk_mul_f32 v[32:33], v[34:35], v[102:103]
	v_pk_mul_f32 v[34:35], v[26:27], v[4:5] op_sel_hi:[0,1]
	v_pk_fma_f32 v[102:103], v[100:101], s[66:67], v[32:33] op_sel_hi:[0, 1, 1]
	v_pk_mul_f32 v[32:33], v[26:27], v[2:3] op_sel_hi:[0,1]
	v_exp_f32_e32 v32, v32
	v_exp_f32_e32 v33, v33
	v_exp_f32_e32 v34, v34
	v_exp_f32_e32 v35, v35
	v_pk_fma_f32 v[30:31], s[96:97], v[114:115], v[30:31]
	v_pk_mul_f32 v[32:33], v[32:33], v[104:105]
	v_pk_fma_f32 v[30:31], s[98:99], v[102:103], v[30:31]
	v_pk_fma_f32 v[104:105], v[100:101], s[68:69], v[32:33] op_sel_hi:[0, 1, 1]
	v_pk_mul_f32 v[32:33], v[34:35], v[98:99]
	v_pk_fma_f32 v[30:31], s[20:21], v[104:105], v[30:31]
	v_pk_fma_f32 v[98:99], v[100:101], s[70:71], v[32:33] op_sel_hi:[0, 1, 1]
	v_pk_fma_f32 v[30:31], s[22:23], v[98:99], v[30:31]
	s_nop 0
	v_add_f32_e32 v26, v30, v31
	v_fma_mix_f32 v18, v1, v18, v26 op_sel:[0,1,0] op_sel_hi:[0,1,0]
	v_fma_mixlo_f16 v18, v18, v22, 0 op_sel:[0,1,0] op_sel_hi:[0,1,0]
	ds_write_b16 v68, v18 offset:30096
	s_waitcnt lgkmcnt(0)
	s_load_dwordx16 s[56:71], s[54:55], 0xd80
	s_load_dwordx8 s[88:95], s[54:55], 0xdc0
	s_load_dwordx4 s[96:99], s[54:55], 0xde0
	s_load_dwordx4 s[20:23], s[54:55], 0xdf0
	v_cvt_f32_f16_e32 v18, v27
	v_cvt_f32_f16_e32 v22, v19
	v_pk_mul_f32 v[100:101], v[18:19], v[14:15] op_sel_hi:[0,1]
	v_exp_f32_e32 v100, v100
	v_exp_f32_e32 v101, v101
	v_pk_mul_f32 v[116:117], v[18:19], v[16:17] op_sel_hi:[0,1]
	v_exp_f32_e32 v116, v116
	v_exp_f32_e32 v117, v117
	v_mul_f32_e32 v22, v18, v22
	v_pk_mul_f32 v[100:101], v[100:101], v[106:107]
	v_pk_fma_f32 v[100:101], v[22:23], s[36:37], v[100:101] op_sel_hi:[0, 1, 1]
	v_pk_fma_f32 v[62:63], s[72:73], v[100:101], 0 op_sel_hi:[1, 1, 0]
	v_pk_mul_f32 v[82:83], v[116:117], v[108:109]
	s_nop 0
	v_pk_fma_f32 v[106:107], v[22:23], s[38:39], v[82:83] op_sel_hi:[0, 1, 1]
	v_pk_mul_f32 v[64:65], v[18:19], v[10:11] op_sel_hi:[0,1]
	v_exp_f32_e32 v64, v64
	v_exp_f32_e32 v65, v65
	v_pk_mul_f32 v[82:83], v[18:19], v[12:13] op_sel_hi:[0,1]
	v_exp_f32_e32 v82, v82
	v_exp_f32_e32 v83, v83
	v_pk_mul_f32 v[64:65], v[64:65], v[110:111]
	v_pk_fma_f32 v[62:63], s[74:75], v[106:107], v[62:63]
	v_pk_fma_f32 v[108:109], v[22:23], s[40:41], v[64:65] op_sel_hi:[0, 1, 1]
	v_pk_mul_f32 v[64:65], v[82:83], v[112:113]
	v_pk_mul_f32 v[70:71], v[18:19], v[8:9] op_sel_hi:[0,1]
	v_pk_fma_f32 v[110:111], v[22:23], s[42:43], v[64:65] op_sel_hi:[0, 1, 1]
	v_pk_mul_f32 v[64:65], v[18:19], v[6:7] op_sel_hi:[0,1]
	v_exp_f32_e32 v64, v64
	v_exp_f32_e32 v65, v65
	v_exp_f32_e32 v70, v70
	v_exp_f32_e32 v71, v71
	v_pk_fma_f32 v[62:63], s[76:77], v[108:109], v[62:63]
	v_pk_mul_f32 v[64:65], v[64:65], v[114:115]
	v_pk_fma_f32 v[62:63], s[78:79], v[110:111], v[62:63]
	v_pk_fma_f32 v[112:113], v[22:23], s[44:45], v[64:65] op_sel_hi:[0, 1, 1]
	v_pk_mul_f32 v[64:65], v[70:71], v[102:103]
	v_pk_mul_f32 v[70:71], v[18:19], v[4:5] op_sel_hi:[0,1]
	v_pk_fma_f32 v[102:103], v[22:23], s[46:47], v[64:65] op_sel_hi:[0, 1, 1]
	v_pk_mul_f32 v[64:65], v[18:19], v[2:3] op_sel_hi:[0,1]
	v_exp_f32_e32 v64, v64
	v_exp_f32_e32 v65, v65
	v_exp_f32_e32 v70, v70
	v_exp_f32_e32 v71, v71
	v_pk_fma_f32 v[62:63], s[80:81], v[112:113], v[62:63]
	v_pk_mul_f32 v[64:65], v[64:65], v[104:105]
	v_pk_fma_f32 v[62:63], s[82:83], v[102:103], v[62:63]
	v_pk_fma_f32 v[104:105], v[22:23], s[48:49], v[64:65] op_sel_hi:[0, 1, 1]
	v_pk_mul_f32 v[64:65], v[70:71], v[98:99]
	v_pk_fma_f32 v[62:63], s[84:85], v[104:105], v[62:63]
	v_pk_fma_f32 v[98:99], v[22:23], s[50:51], v[64:65] op_sel_hi:[0, 1, 1]
	v_pk_fma_f32 v[62:63], s[86:87], v[98:99], v[62:63]
	s_nop 0
	v_add_f32_e32 v18, v62, v63
	v_fma_mix_f32 v18, v1, v19, v18 op_sel_hi:[0,1,0]
	v_fma_mixlo_f16 v18, v18, v23, 0 op_sel_hi:[0,1,0]
	ds_write_b16 v68, v18 offset:31136
	s_waitcnt lgkmcnt(0)
	s_load_dwordx16 s[36:51], s[54:55], 0xe00
	s_load_dwordx16 s[72:87], s[54:55], 0xe40
	v_cvt_f32_f16_sdwa v18, v27 dst_sel:DWORD dst_unused:UNUSED_PAD src0_sel:WORD_1
	v_cvt_f32_f16_sdwa v22, v19 dst_sel:DWORD dst_unused:UNUSED_PAD src0_sel:WORD_1
	v_pk_mul_f32 v[26:27], v[18:19], v[14:15] op_sel_hi:[0,1]
	v_exp_f32_e32 v26, v26
	v_exp_f32_e32 v27, v27
	v_pk_mul_f32 v[114:115], v[18:19], v[16:17] op_sel_hi:[0,1]
	v_exp_f32_e32 v114, v114
	v_exp_f32_e32 v115, v115
	v_mul_f32_e32 v22, v18, v22
	v_pk_mul_f32 v[26:27], v[26:27], v[100:101]
	v_pk_fma_f32 v[26:27], v[22:23], s[56:57], v[26:27] op_sel_hi:[0, 1, 1]
	v_pk_fma_f32 v[30:31], s[88:89], v[26:27], 0 op_sel_hi:[1, 1, 0]
	v_pk_mul_f32 v[46:47], v[114:115], v[106:107]
	s_nop 0
	v_pk_fma_f32 v[100:101], v[22:23], s[58:59], v[46:47] op_sel_hi:[0, 1, 1]
	v_pk_mul_f32 v[32:33], v[18:19], v[10:11] op_sel_hi:[0,1]
	v_exp_f32_e32 v32, v32
	v_exp_f32_e32 v33, v33
	v_pk_mul_f32 v[46:47], v[18:19], v[12:13] op_sel_hi:[0,1]
	v_exp_f32_e32 v46, v46
	v_exp_f32_e32 v47, v47
	v_pk_mul_f32 v[32:33], v[32:33], v[108:109]
	v_pk_fma_f32 v[30:31], s[90:91], v[100:101], v[30:31]
	v_pk_fma_f32 v[106:107], v[22:23], s[60:61], v[32:33] op_sel_hi:[0, 1, 1]
	v_pk_mul_f32 v[32:33], v[46:47], v[110:111]
	v_pk_mul_f32 v[34:35], v[18:19], v[8:9] op_sel_hi:[0,1]
	v_pk_fma_f32 v[108:109], v[22:23], s[62:63], v[32:33] op_sel_hi:[0, 1, 1]
	v_pk_mul_f32 v[32:33], v[18:19], v[6:7] op_sel_hi:[0,1]
	v_exp_f32_e32 v32, v32
	v_exp_f32_e32 v33, v33
	v_exp_f32_e32 v34, v34
	v_exp_f32_e32 v35, v35
	v_pk_fma_f32 v[30:31], s[92:93], v[106:107], v[30:31]
	v_pk_mul_f32 v[32:33], v[32:33], v[112:113]
	v_pk_fma_f32 v[30:31], s[94:95], v[108:109], v[30:31]
	v_pk_fma_f32 v[110:111], v[22:23], s[64:65], v[32:33] op_sel_hi:[0, 1, 1]
	v_pk_mul_f32 v[32:33], v[34:35], v[102:103]
	v_pk_mul_f32 v[34:35], v[18:19], v[4:5] op_sel_hi:[0,1]
	v_pk_fma_f32 v[102:103], v[22:23], s[66:67], v[32:33] op_sel_hi:[0, 1, 1]
	v_pk_mul_f32 v[32:33], v[18:19], v[2:3] op_sel_hi:[0,1]
	v_exp_f32_e32 v32, v32
	v_exp_f32_e32 v33, v33
	v_exp_f32_e32 v34, v34
	v_exp_f32_e32 v35, v35
	v_pk_fma_f32 v[30:31], s[96:97], v[110:111], v[30:31]
	v_pk_mul_f32 v[32:33], v[32:33], v[104:105]
	v_pk_fma_f32 v[30:31], s[98:99], v[102:103], v[30:31]
	v_pk_fma_f32 v[104:105], v[22:23], s[68:69], v[32:33] op_sel_hi:[0, 1, 1]
	v_pk_mul_f32 v[32:33], v[34:35], v[98:99]
	v_pk_fma_f32 v[30:31], s[20:21], v[104:105], v[30:31]
	v_pk_fma_f32 v[98:99], v[22:23], s[70:71], v[32:33] op_sel_hi:[0, 1, 1]
	v_pk_fma_f32 v[30:31], s[22:23], v[98:99], v[30:31]
	s_nop 0
	v_add_f32_e32 v18, v30, v31
	v_fma_mix_f32 v18, v1, v19, v18 op_sel:[0,1,0] op_sel_hi:[0,1,0]
	v_fma_mixlo_f16 v18, v18, v23, 0 op_sel:[0,1,0] op_sel_hi:[0,1,0]
	ds_write_b16 v68, v18 offset:32176
	s_waitcnt lgkmcnt(0)
	s_load_dwordx16 s[56:71], s[54:55], 0xe80
	s_load_dwordx8 s[88:95], s[54:55], 0xec0
	s_load_dwordx4 s[96:99], s[54:55], 0xee0
	s_load_dwordx4 s[20:23], s[54:55], 0xef0
	v_cvt_f32_f16_e32 v18, v28
	v_cvt_f32_f16_e32 v19, v20
	v_pk_mul_f32 v[112:113], v[18:19], v[14:15] op_sel_hi:[0,1]
	v_exp_f32_e32 v112, v112
	v_exp_f32_e32 v113, v113
	v_pk_mul_f32 v[114:115], v[18:19], v[16:17] op_sel_hi:[0,1]
	v_exp_f32_e32 v114, v114
	v_exp_f32_e32 v115, v115
	v_mul_f32_e32 v22, v18, v19
	v_pk_mul_f32 v[26:27], v[112:113], v[26:27]
	v_pk_fma_f32 v[26:27], v[22:23], s[36:37], v[26:27] op_sel_hi:[0, 1, 1]
	v_pk_fma_f32 v[62:63], s[72:73], v[26:27], 0 op_sel_hi:[1, 1, 0]
	v_pk_mul_f32 v[82:83], v[114:115], v[100:101]
	s_nop 0
	v_pk_fma_f32 v[100:101], v[22:23], s[38:39], v[82:83] op_sel_hi:[0, 1, 1]
	v_pk_mul_f32 v[64:65], v[18:19], v[10:11] op_sel_hi:[0,1]
	v_exp_f32_e32 v64, v64
	v_exp_f32_e32 v65, v65
	v_pk_mul_f32 v[82:83], v[18:19], v[12:13] op_sel_hi:[0,1]
	v_exp_f32_e32 v82, v82
	v_exp_f32_e32 v83, v83
	v_pk_mul_f32 v[64:65], v[64:65], v[106:107]
	v_pk_fma_f32 v[62:63], s[74:75], v[100:101], v[62:63]
	v_pk_fma_f32 v[106:107], v[22:23], s[40:41], v[64:65] op_sel_hi:[0, 1, 1]
	v_pk_mul_f32 v[64:65], v[82:83], v[108:109]
	v_pk_mul_f32 v[70:71], v[18:19], v[8:9] op_sel_hi:[0,1]
	v_pk_fma_f32 v[108:109], v[22:23], s[42:43], v[64:65] op_sel_hi:[0, 1, 1]
	v_pk_mul_f32 v[64:65], v[18:19], v[6:7] op_sel_hi:[0,1]
	v_exp_f32_e32 v64, v64
	v_exp_f32_e32 v65, v65
	v_exp_f32_e32 v70, v70
	v_exp_f32_e32 v71, v71
	v_pk_fma_f32 v[62:63], s[76:77], v[106:107], v[62:63]
	v_pk_mul_f32 v[64:65], v[64:65], v[110:111]
	v_pk_fma_f32 v[62:63], s[78:79], v[108:109], v[62:63]
	v_pk_fma_f32 v[110:111], v[22:23], s[44:45], v[64:65] op_sel_hi:[0, 1, 1]
	v_pk_mul_f32 v[64:65], v[70:71], v[102:103]
	v_pk_fma_f32 v[62:63], s[80:81], v[110:111], v[62:63]
	v_pk_fma_f32 v[102:103], v[22:23], s[46:47], v[64:65] op_sel_hi:[0, 1, 1]
	v_pk_mul_f32 v[64:65], v[18:19], v[2:3] op_sel_hi:[0,1]
	v_exp_f32_e32 v64, v64
	v_exp_f32_e32 v65, v65
	v_pk_mul_f32 v[18:19], v[18:19], v[4:5] op_sel_hi:[0,1]
	v_exp_f32_e32 v18, v18
	v_exp_f32_e32 v19, v19
	v_pk_mul_f32 v[64:65], v[64:65], v[104:105]
	v_pk_fma_f32 v[62:63], s[82:83], v[102:103], v[62:63]
	v_pk_fma_f32 v[104:105], v[22:23], s[48:49], v[64:65] op_sel_hi:[0, 1, 1]
	v_pk_mul_f32 v[18:19], v[18:19], v[98:99]
	v_pk_fma_f32 v[62:63], s[84:85], v[104:105], v[62:63]
	v_pk_fma_f32 v[18:19], v[22:23], s[50:51], v[18:19] op_sel_hi:[0, 1, 1]
	v_pk_fma_f32 v[22:23], s[86:87], v[18:19], v[62:63]
	s_nop 0
	v_add_f32_e32 v22, v22, v23
	v_fma_mix_f32 v22, v1, v20, v22 op_sel_hi:[0,1,0]
	v_fma_mixlo_f16 v22, v22, v24, 0 op_sel_hi:[0,1,0]
	ds_write_b16 v68, v22 offset:33216
	s_waitcnt lgkmcnt(0)
	s_load_dwordx16 s[36:51], s[54:55], 0xf00
	s_load_dwordx16 s[72:87], s[54:55], 0xf40
	v_cvt_f32_f16_sdwa v22, v28 dst_sel:DWORD dst_unused:UNUSED_PAD src0_sel:WORD_1
	v_cvt_f32_f16_sdwa v23, v20 dst_sel:DWORD dst_unused:UNUSED_PAD src0_sel:WORD_1
	v_pk_mul_f32 v[98:99], v[22:23], v[14:15] op_sel_hi:[0,1]
	v_exp_f32_e32 v98, v98
	v_exp_f32_e32 v99, v99
	v_pk_mul_f32 v[112:113], v[22:23], v[16:17] op_sel_hi:[0,1]
	v_exp_f32_e32 v112, v112
	v_exp_f32_e32 v113, v113
	v_mul_f32_e32 v28, v22, v23
	v_pk_mul_f32 v[26:27], v[98:99], v[26:27]
	v_pk_fma_f32 v[26:27], v[28:29], s[56:57], v[26:27] op_sel_hi:[0, 1, 1]
	v_pk_fma_f32 v[30:31], s[88:89], v[26:27], 0 op_sel_hi:[1, 1, 0]
	v_pk_mul_f32 v[46:47], v[112:113], v[100:101]
	s_nop 0
	v_pk_fma_f32 v[98:99], v[28:29], s[58:59], v[46:47] op_sel_hi:[0, 1, 1]
	v_pk_mul_f32 v[32:33], v[22:23], v[10:11] op_sel_hi:[0,1]
	v_exp_f32_e32 v32, v32
	v_exp_f32_e32 v33, v33
	v_pk_mul_f32 v[46:47], v[22:23], v[12:13] op_sel_hi:[0,1]
	v_exp_f32_e32 v46, v46
	v_exp_f32_e32 v47, v47
	v_pk_mul_f32 v[32:33], v[32:33], v[106:107]
	v_pk_fma_f32 v[30:31], s[90:91], v[98:99], v[30:31]
	v_pk_fma_f32 v[100:101], v[28:29], s[60:61], v[32:33] op_sel_hi:[0, 1, 1]
	v_pk_mul_f32 v[32:33], v[46:47], v[108:109]
	v_pk_mul_f32 v[34:35], v[22:23], v[8:9] op_sel_hi:[0,1]
	v_pk_fma_f32 v[106:107], v[28:29], s[62:63], v[32:33] op_sel_hi:[0, 1, 1]
	v_pk_mul_f32 v[32:33], v[22:23], v[6:7] op_sel_hi:[0,1]
	v_exp_f32_e32 v32, v32
	v_exp_f32_e32 v33, v33
	v_exp_f32_e32 v34, v34
	v_exp_f32_e32 v35, v35
	v_pk_fma_f32 v[30:31], s[92:93], v[100:101], v[30:31]
	v_pk_mul_f32 v[32:33], v[32:33], v[110:111]
	v_pk_fma_f32 v[30:31], s[94:95], v[106:107], v[30:31]
	v_pk_fma_f32 v[108:109], v[28:29], s[64:65], v[32:33] op_sel_hi:[0, 1, 1]
	v_pk_mul_f32 v[32:33], v[34:35], v[102:103]
	v_pk_fma_f32 v[30:31], s[96:97], v[108:109], v[30:31]
	v_pk_fma_f32 v[102:103], v[28:29], s[66:67], v[32:33] op_sel_hi:[0, 1, 1]
	v_pk_mul_f32 v[32:33], v[22:23], v[2:3] op_sel_hi:[0,1]
	v_exp_f32_e32 v32, v32
	v_exp_f32_e32 v33, v33
	v_pk_mul_f32 v[22:23], v[22:23], v[4:5] op_sel_hi:[0,1]
	v_exp_f32_e32 v22, v22
	v_exp_f32_e32 v23, v23
	v_pk_mul_f32 v[32:33], v[32:33], v[104:105]
	v_pk_fma_f32 v[30:31], s[98:99], v[102:103], v[30:31]
	v_pk_fma_f32 v[104:105], v[28:29], s[68:69], v[32:33] op_sel_hi:[0, 1, 1]
	v_pk_mul_f32 v[18:19], v[22:23], v[18:19]
	v_pk_fma_f32 v[30:31], s[20:21], v[104:105], v[30:31]
	v_pk_fma_f32 v[18:19], v[28:29], s[70:71], v[18:19] op_sel_hi:[0, 1, 1]
	v_pk_fma_f32 v[22:23], s[22:23], v[18:19], v[30:31]
	s_nop 0
	v_add_f32_e32 v22, v22, v23
	v_fma_mix_f32 v20, v1, v20, v22 op_sel:[0,1,0] op_sel_hi:[0,1,0]
	v_fma_mixlo_f16 v20, v20, v24, 0 op_sel:[0,1,0] op_sel_hi:[0,1,0]
	ds_write_b16 v68, v20 offset:34256
	s_waitcnt lgkmcnt(0)
	s_load_dwordx16 s[56:71], s[54:55], 0xf80
	s_load_dwordx8 s[88:95], s[54:55], 0xfc0
	s_load_dwordx4 s[96:99], s[54:55], 0xfe0
	s_load_dwordx4 s[20:23], s[54:55], 0xff0
	v_cvt_f32_f16_e32 v20, v29
	v_cvt_f32_f16_e32 v22, v21
	v_pk_mul_f32 v[110:111], v[20:21], v[14:15] op_sel_hi:[0,1]
	v_exp_f32_e32 v110, v110
	v_exp_f32_e32 v111, v111
	v_pk_mul_f32 v[112:113], v[20:21], v[16:17] op_sel_hi:[0,1]
	v_exp_f32_e32 v112, v112
	v_exp_f32_e32 v113, v113
	v_mul_f32_e32 v22, v20, v22
	v_pk_mul_f32 v[26:27], v[110:111], v[26:27]
	v_pk_fma_f32 v[26:27], v[22:23], s[36:37], v[26:27] op_sel_hi:[0, 1, 1]
	v_pk_fma_f32 v[62:63], s[72:73], v[26:27], 0 op_sel_hi:[1, 1, 0]
	v_pk_mul_f32 v[82:83], v[112:113], v[98:99]
	s_nop 0
	v_pk_fma_f32 v[64:65], v[22:23], s[38:39], v[82:83] op_sel_hi:[0, 1, 1]
	v_pk_mul_f32 v[82:83], v[20:21], v[10:11] op_sel_hi:[0,1]
	v_pk_fma_f32 v[62:63], s[74:75], v[64:65], v[62:63]
	v_exp_f32_e32 v82, v82
	v_exp_f32_e32 v83, v83
	v_pk_mul_f32 v[84:85], v[20:21], v[12:13] op_sel_hi:[0,1]
	v_exp_f32_e32 v84, v84
	v_exp_f32_e32 v85, v85
	v_pk_mul_f32 v[82:83], v[82:83], v[100:101]
	s_nop 0
	v_pk_fma_f32 v[70:71], v[22:23], s[40:41], v[82:83] op_sel_hi:[0, 1, 1]
	v_pk_mul_f32 v[82:83], v[84:85], v[106:107]
	v_pk_mul_f32 v[84:85], v[20:21], v[8:9] op_sel_hi:[0,1]
	v_pk_fma_f32 v[72:73], v[22:23], s[42:43], v[82:83] op_sel_hi:[0, 1, 1]
	v_pk_mul_f32 v[82:83], v[20:21], v[6:7] op_sel_hi:[0,1]
	v_exp_f32_e32 v82, v82
	v_exp_f32_e32 v83, v83
	v_exp_f32_e32 v84, v84
	v_exp_f32_e32 v85, v85
	v_pk_fma_f32 v[62:63], s[76:77], v[70:71], v[62:63]
	v_pk_mul_f32 v[82:83], v[82:83], v[108:109]
	v_pk_fma_f32 v[62:63], s[78:79], v[72:73], v[62:63]
	v_pk_fma_f32 v[74:75], v[22:23], s[44:45], v[82:83] op_sel_hi:[0, 1, 1]
	v_pk_mul_f32 v[82:83], v[84:85], v[102:103]
	v_pk_mul_f32 v[84:85], v[20:21], v[4:5] op_sel_hi:[0,1]
	v_pk_fma_f32 v[76:77], v[22:23], s[46:47], v[82:83] op_sel_hi:[0, 1, 1]
	v_pk_mul_f32 v[82:83], v[20:21], v[2:3] op_sel_hi:[0,1]
	v_exp_f32_e32 v82, v82
	v_exp_f32_e32 v83, v83
	v_exp_f32_e32 v84, v84
	v_exp_f32_e32 v85, v85
	v_pk_fma_f32 v[62:63], s[80:81], v[74:75], v[62:63]
	v_pk_mul_f32 v[82:83], v[82:83], v[104:105]
	v_pk_fma_f32 v[62:63], s[82:83], v[76:77], v[62:63]
	v_pk_fma_f32 v[78:79], v[22:23], s[48:49], v[82:83] op_sel_hi:[0, 1, 1]
	v_pk_mul_f32 v[18:19], v[84:85], v[18:19]
	v_pk_fma_f32 v[62:63], s[84:85], v[78:79], v[62:63]
	v_pk_fma_f32 v[18:19], v[22:23], s[50:51], v[18:19] op_sel_hi:[0, 1, 1]
	v_pk_fma_f32 v[22:23], s[86:87], v[18:19], v[62:63]
	s_nop 0
	v_add_f32_e32 v20, v22, v23
	v_fma_mix_f32 v20, v1, v21, v20 op_sel_hi:[0,1,0]
	v_fma_mixlo_f16 v20, v20, v25, 0 op_sel_hi:[0,1,0]
	ds_write_b16 v68, v20 offset:35296
	s_waitcnt lgkmcnt(0)
	v_cvt_f32_f16_sdwa v20, v29 dst_sel:DWORD dst_unused:UNUSED_PAD src0_sel:WORD_1
	v_cvt_f32_f16_sdwa v22, v21 dst_sel:DWORD dst_unused:UNUSED_PAD src0_sel:WORD_1
	v_pk_mul_f32 v[14:15], v[20:21], v[14:15] op_sel_hi:[0,1]
	v_exp_f32_e32 v14, v14
	v_exp_f32_e32 v15, v15
	v_pk_mul_f32 v[16:17], v[20:21], v[16:17] op_sel_hi:[0,1]
	v_exp_f32_e32 v16, v16
	v_exp_f32_e32 v17, v17
	v_pk_mul_f32 v[10:11], v[20:21], v[10:11] op_sel_hi:[0,1]
	v_exp_f32_e32 v10, v10
	v_exp_f32_e32 v11, v11
	v_pk_mul_f32 v[12:13], v[20:21], v[12:13] op_sel_hi:[0,1]
	v_exp_f32_e32 v12, v12
	v_exp_f32_e32 v13, v13
	v_pk_mul_f32 v[6:7], v[20:21], v[6:7] op_sel_hi:[0,1]
	v_mul_f32_e32 v22, v20, v22
	v_pk_mul_f32 v[14:15], v[14:15], v[26:27]
	v_exp_f32_e32 v6, v6
	v_exp_f32_e32 v7, v7
	v_pk_mul_f32 v[8:9], v[20:21], v[8:9] op_sel_hi:[0,1]
	v_pk_fma_f32 v[14:15], v[22:23], s[56:57], v[14:15] op_sel_hi:[0, 1, 1]
	v_pk_mul_f32 v[16:17], v[16:17], v[64:65]
	v_exp_f32_e32 v8, v8
	v_exp_f32_e32 v9, v9
	v_pk_mul_f32 v[2:3], v[20:21], v[2:3] op_sel_hi:[0,1]
	v_pk_fma_f32 v[14:15], s[88:89], v[14:15], 0 op_sel_hi:[1, 1, 0]
	v_pk_fma_f32 v[16:17], v[22:23], s[58:59], v[16:17] op_sel_hi:[0, 1, 1]
	v_pk_mul_f32 v[10:11], v[10:11], v[70:71]
	v_exp_f32_e32 v2, v2
	v_exp_f32_e32 v3, v3
	v_pk_mul_f32 v[4:5], v[20:21], v[4:5] op_sel_hi:[0,1]
	v_pk_fma_f32 v[14:15], s[90:91], v[16:17], v[14:15]
	v_pk_fma_f32 v[10:11], v[22:23], s[60:61], v[10:11] op_sel_hi:[0, 1, 1]
	v_pk_mul_f32 v[12:13], v[12:13], v[72:73]
	v_exp_f32_e32 v4, v4
	v_exp_f32_e32 v5, v5
	v_pk_fma_f32 v[10:11], s[92:93], v[10:11], v[14:15]
	v_pk_fma_f32 v[12:13], v[22:23], s[62:63], v[12:13] op_sel_hi:[0, 1, 1]
	v_pk_mul_f32 v[6:7], v[6:7], v[74:75]
	v_pk_fma_f32 v[10:11], s[94:95], v[12:13], v[10:11]
	v_pk_fma_f32 v[6:7], v[22:23], s[64:65], v[6:7] op_sel_hi:[0, 1, 1]
	v_pk_mul_f32 v[8:9], v[8:9], v[76:77]
	v_pk_fma_f32 v[6:7], s[96:97], v[6:7], v[10:11]
	v_pk_fma_f32 v[8:9], v[22:23], s[66:67], v[8:9] op_sel_hi:[0, 1, 1]
	v_pk_mul_f32 v[2:3], v[2:3], v[78:79]
	v_pk_fma_f32 v[6:7], s[98:99], v[8:9], v[6:7]
	v_pk_fma_f32 v[2:3], v[22:23], s[68:69], v[2:3] op_sel_hi:[0, 1, 1]
	v_pk_mul_f32 v[4:5], v[4:5], v[18:19]
	v_pk_fma_f32 v[2:3], s[20:21], v[2:3], v[6:7]
	v_pk_fma_f32 v[4:5], v[22:23], s[70:71], v[4:5] op_sel_hi:[0, 1, 1]
	v_pk_fma_f32 v[2:3], s[22:23], v[4:5], v[2:3]
	s_nop 0
	v_add_f32_e32 v2, v2, v3
	v_fma_mix_f32 v1, v1, v21, v2 op_sel:[0,1,0] op_sel_hi:[0,1,0]
	v_fma_mixlo_f16 v1, v1, v25, 0 op_sel:[0,1,0] op_sel_hi:[0,1,0]
	ds_write_b16 v68, v1 offset:36336
	v_lshlrev_b32_e32 v1, 9, v0
	v_and_b32_e32 v2, 0x38000, v1
	v_mov_b32_e32 v3, v67
	v_and_b32_e32 v1, 63, v0
	s_bfe_u32 s14, s2, 0x40003
	v_lshl_add_u64 v[2:3], s[18:19], 0, v[2:3]
	v_lshlrev_b32_e32 v58, 4, v1
	v_mov_b32_e32 v59, v67
	s_lshl_b32 s13, s14, 6
	v_lshl_add_u64 v[20:21], v[2:3], 0, v[58:59]
	s_lshl_b32 s26, s14, 10
	s_add_i32 s12, s13, 64
	v_lshl_add_u64 v[2:3], v[20:21], 0, s[26:27]
	s_and_b32 s15, s12, 0x3c0
	v_add_co_u32_e32 v4, vcc, s52, v2
	s_lshl_b32 s26, s15, 4
	s_lshl_b32 s12, s12, 4
	v_addc_co_u32_e32 v5, vcc, 0, v3, vcc
	global_load_dwordx4 v[28:31], v[2:3], off
	global_load_dwordx4 v[32:35], v[4:5], off
	v_lshl_add_u64 v[2:3], v[20:21], 0, s[26:27]
	s_or_b32 s26, s12, 0x4000
	s_add_i32 s12, s13, 0x80
	s_and_b32 s15, s12, 0x3c0
	v_lshl_add_u64 v[4:5], v[20:21], 0, s[26:27]
	s_lshl_b32 s26, s15, 4
	s_lshl_b32 s12, s12, 4
	global_load_dwordx4 v[36:39], v[2:3], off
	global_load_dwordx4 v[40:43], v[4:5], off
	v_lshl_add_u64 v[2:3], v[20:21], 0, s[26:27]
	s_or_b32 s26, s12, 0x4000
	s_add_i32 s12, s13, 0xc0
	s_and_b32 s15, s12, 0x3c0
	v_lshl_add_u64 v[4:5], v[20:21], 0, s[26:27]
	s_lshl_b32 s26, s15, 4
	s_lshl_b32 s12, s12, 4
	global_load_dwordx4 v[44:47], v[2:3], off
	global_load_dwordx4 v[48:51], v[4:5], off
	v_lshl_add_u64 v[2:3], v[20:21], 0, s[26:27]
	s_or_b32 s26, s12, 0x4000
	s_add_i32 s12, s13, 0x100
	s_and_b32 s15, s12, 0x3c0
	v_lshl_add_u64 v[4:5], v[20:21], 0, s[26:27]
	s_lshl_b32 s26, s15, 4
	s_lshl_b32 s12, s12, 4
	global_load_dwordx4 v[52:55], v[2:3], off
	global_load_dwordx4 v[60:63], v[4:5], off
	v_lshl_add_u64 v[2:3], v[20:21], 0, s[26:27]
	s_or_b32 s26, s12, 0x4000
	s_add_i32 s12, s13, 0x140
	s_and_b32 s15, s12, 0x3c0
	v_lshl_add_u64 v[4:5], v[20:21], 0, s[26:27]
	s_lshl_b32 s26, s15, 4
	s_lshl_b32 s12, s12, 4
	global_load_dwordx4 v[68:71], v[2:3], off
	global_load_dwordx4 v[72:75], v[4:5], off
	v_lshl_add_u64 v[2:3], v[20:21], 0, s[26:27]
	s_or_b32 s26, s12, 0x4000
	s_add_i32 s12, s13, 0x180
	s_and_b32 s15, s12, 0x3c0
	v_lshl_add_u64 v[4:5], v[20:21], 0, s[26:27]
	s_lshl_b32 s26, s15, 4
	s_lshl_b32 s12, s12, 4
	global_load_dwordx4 v[76:79], v[2:3], off
	global_load_dwordx4 v[82:85], v[4:5], off
	v_lshl_add_u64 v[2:3], v[20:21], 0, s[26:27]
	s_or_b32 s26, s12, 0x4000
	s_add_i32 s12, s13, 0x1c0
	s_and_b32 s15, s12, 0x3c0
	v_lshl_add_u64 v[4:5], v[20:21], 0, s[26:27]
	s_lshl_b32 s26, s15, 4
	s_lshl_b32 s12, s12, 4
	v_lshl_add_u64 v[18:19], v[20:21], 0, s[26:27]
	s_or_b32 s26, s12, 0x4000
	s_xor_b32 s15, s13, 0x200
	v_lshl_add_u64 v[22:23], v[20:21], 0, s[26:27]
	s_lshl_b32 s26, s15, 4
	global_load_dwordx4 v[14:17], v[2:3], off
	global_load_dwordx4 v[10:13], v[4:5], off
	global_load_dwordx4 v[6:9], v[18:19], off
	s_nop 0
	global_load_dwordx4 v[2:5], v[22:23], off
	v_lshl_add_u64 v[18:19], v[20:21], 0, s[26:27]
	v_add_co_u32_e32 v22, vcc, s52, v18
	s_waitcnt lgkmcnt(0)
	s_barrier
	v_addc_co_u32_e32 v23, vcc, 0, v19, vcc
	global_load_dwordx4 v[86:89], v[18:19], off
	global_load_dwordx4 v[90:93], v[22:23], off
	v_lshrrev_b32_e32 v118, 6, v0
	v_lshlrev_b32_e32 v22, 7, v118
	v_mov_b32_e32 v23, v67
	v_and_b32_e32 v81, 15, v0
	v_lshl_add_u64 v[24:25], s[4:5], 0, v[22:23]
	v_and_b32_e32 v18, 48, v0
	v_mov_b32_e32 v19, v67
	s_movk_i32 s12, 0x410
	v_lshl_add_u64 v[56:57], v[24:25], 0, v[18:19]
	v_mad_u32_u24 v19, v81, s12, v18
	v_add_u32_e32 v23, s13, v19
	ds_read_b128 v[94:97], v23 offset:4096
	ds_read_b128 v[98:101], v23 offset:20736
	v_or_b32_e32 v26, s28, v81
	v_mov_b32_e32 v27, v67
	v_lshlrev_b64 v[24:25], 10, v[26:27]
	v_or_b32_e32 v26, 16, v26
	v_lshlrev_b64 v[26:27], 10, v[26:27]
	v_lshrrev_b32_e32 v23, 1, v0
	v_lshl_add_u64 v[24:25], v[56:57], 0, v[24:25]
	v_lshl_add_u64 v[26:27], v[56:57], 0, v[26:27]
	v_and_b32_e32 v80, 24, v23
	s_lshl_b32 s14, s14, 5
	s_setprio 1
	s_waitcnt vmcnt(17) lgkmcnt(1)
	v_mfma_f32_16x16x32_f16 v[102:105], v[28:31], v[94:97], 0
	s_waitcnt lgkmcnt(0)
	v_mfma_f32_16x16x32_f16 v[28:31], v[28:31], v[98:101], 0
	s_waitcnt vmcnt(16)
	v_mfma_f32_16x16x32_f16 v[94:97], v[32:35], v[94:97], 0
	v_mfma_f32_16x16x32_f16 v[32:35], v[32:35], v[98:101], 0
	s_setprio 0
	s_add_i32 s16, s13, 0x240
	s_and_b32 s17, s16, 0x3c0
	s_lshl_b32 s26, s17, 4
	s_lshl_b32 s16, s16, 4
	v_lshl_add_u64 v[56:57], v[20:21], 0, s[26:27]
	s_or_b32 s26, s16, 0x4000
	v_lshl_add_u64 v[64:65], v[20:21], 0, s[26:27]
	global_load_dwordx4 v[98:101], v[56:57], off
	global_load_dwordx4 v[106:109], v[64:65], off
	s_add_i32 s16, s14, 32
	s_and_b32 s16, s16, 0x1e0
	v_lshl_add_u32 v23, s16, 1, v19
	ds_read_b128 v[110:113], v23 offset:4096
	ds_read_b128 v[114:117], v23 offset:20736
	s_setprio 1
	s_waitcnt vmcnt(17) lgkmcnt(1)
	v_mfma_f32_16x16x32_f16 v[102:105], v[36:39], v[110:113], v[102:105]
	s_waitcnt lgkmcnt(0)
	v_mfma_f32_16x16x32_f16 v[28:31], v[36:39], v[114:117], v[28:31]
	s_waitcnt vmcnt(16)
	v_mfma_f32_16x16x32_f16 v[36:39], v[40:43], v[110:113], v[94:97]
	v_mfma_f32_16x16x32_f16 v[32:35], v[40:43], v[114:117], v[32:35]
	s_setprio 0
	s_add_i32 s16, s13, 0x280
	s_and_b32 s17, s16, 0x3c0
	s_lshl_b32 s26, s17, 4
	s_lshl_b32 s16, s16, 4
	v_lshl_add_u64 v[56:57], v[20:21], 0, s[26:27]
	s_or_b32 s26, s16, 0x4000
	v_lshl_add_u64 v[64:65], v[20:21], 0, s[26:27]
	global_load_dwordx4 v[40:43], v[56:57], off
	global_load_dwordx4 v[94:97], v[64:65], off
	s_add_i32 s16, s14, 64
	s_and_b32 s16, s16, 0x1e0
	v_lshl_add_u32 v23, s16, 1, v19
	ds_read_b128 v[110:113], v23 offset:4096
	ds_read_b128 v[114:117], v23 offset:20736
	s_setprio 1
	s_waitcnt vmcnt(17) lgkmcnt(1)
	v_mfma_f32_16x16x32_f16 v[102:105], v[44:47], v[110:113], v[102:105]
	s_waitcnt lgkmcnt(0)
	v_mfma_f32_16x16x32_f16 v[28:31], v[44:47], v[114:117], v[28:31]
	s_waitcnt vmcnt(16)
	v_mfma_f32_16x16x32_f16 v[36:39], v[48:51], v[110:113], v[36:39]
	v_mfma_f32_16x16x32_f16 v[32:35], v[48:51], v[114:117], v[32:35]
	s_setprio 0
	s_add_i32 s16, s13, 0x2c0
	s_and_b32 s17, s16, 0x3c0
	s_lshl_b32 s26, s17, 4
	s_lshl_b32 s16, s16, 4
	v_lshl_add_u64 v[56:57], v[20:21], 0, s[26:27]
	s_or_b32 s26, s16, 0x4000
	v_lshl_add_u64 v[64:65], v[20:21], 0, s[26:27]
	global_load_dwordx4 v[44:47], v[56:57], off
	global_load_dwordx4 v[48:51], v[64:65], off
	s_add_i32 s16, s14, 0x60
	s_and_b32 s16, s16, 0x1e0
	v_lshl_add_u32 v23, s16, 1, v19
	ds_read_b128 v[110:113], v23 offset:4096
	ds_read_b128 v[114:117], v23 offset:20736
	s_setprio 1
	s_waitcnt vmcnt(17) lgkmcnt(1)
	v_mfma_f32_16x16x32_f16 v[102:105], v[52:55], v[110:113], v[102:105]
	s_waitcnt lgkmcnt(0)
	v_mfma_f32_16x16x32_f16 v[28:31], v[52:55], v[114:117], v[28:31]
	s_waitcnt vmcnt(16)
	v_mfma_f32_16x16x32_f16 v[36:39], v[60:63], v[110:113], v[36:39]
	v_mfma_f32_16x16x32_f16 v[32:35], v[60:63], v[114:117], v[32:35]
	s_setprio 0
	s_add_i32 s16, s13, 0x300
	s_and_b32 s17, s16, 0x3c0
	s_lshl_b32 s26, s17, 4
	s_lshl_b32 s16, s16, 4
	v_lshl_add_u64 v[56:57], v[20:21], 0, s[26:27]
	s_or_b32 s26, s16, 0x4000
	v_lshl_add_u64 v[64:65], v[20:21], 0, s[26:27]
	global_load_dwordx4 v[52:55], v[56:57], off
	global_load_dwordx4 v[60:63], v[64:65], off
	s_add_i32 s16, s14, 0x80
	s_and_b32 s16, s16, 0x1e0
	v_lshl_add_u32 v23, s16, 1, v19
	ds_read_b128 v[110:113], v23 offset:4096
	ds_read_b128 v[114:117], v23 offset:20736
	s_setprio 1
	s_waitcnt vmcnt(17) lgkmcnt(1)
	v_mfma_f32_16x16x32_f16 v[102:105], v[68:71], v[110:113], v[102:105]
	s_waitcnt lgkmcnt(0)
	v_mfma_f32_16x16x32_f16 v[28:31], v[68:71], v[114:117], v[28:31]
	s_waitcnt vmcnt(16)
	v_mfma_f32_16x16x32_f16 v[36:39], v[72:75], v[110:113], v[36:39]
	v_mfma_f32_16x16x32_f16 v[32:35], v[72:75], v[114:117], v[32:35]
	s_setprio 0
	s_add_i32 s16, s13, 0x340
	s_and_b32 s17, s16, 0x3c0
	s_lshl_b32 s26, s17, 4
	s_lshl_b32 s16, s16, 4
	v_lshl_add_u64 v[56:57], v[20:21], 0, s[26:27]
	s_or_b32 s26, s16, 0x4000
	v_lshl_add_u64 v[64:65], v[20:21], 0, s[26:27]
	global_load_dwordx4 v[68:71], v[56:57], off
	global_load_dwordx4 v[72:75], v[64:65], off
	s_add_i32 s16, s14, 0xa0
	s_and_b32 s16, s16, 0x1e0
	v_lshl_add_u32 v23, s16, 1, v19
	ds_read_b128 v[110:113], v23 offset:4096
	ds_read_b128 v[114:117], v23 offset:20736
	s_setprio 1
	s_waitcnt vmcnt(17) lgkmcnt(1)
	v_mfma_f32_16x16x32_f16 v[102:105], v[76:79], v[110:113], v[102:105]
	s_waitcnt lgkmcnt(0)
	v_mfma_f32_16x16x32_f16 v[28:31], v[76:79], v[114:117], v[28:31]
	s_waitcnt vmcnt(16)
	v_mfma_f32_16x16x32_f16 v[36:39], v[82:85], v[110:113], v[36:39]
	v_mfma_f32_16x16x32_f16 v[32:35], v[82:85], v[114:117], v[32:35]
	s_setprio 0
	s_add_i32 s16, s13, 0x380
	s_and_b32 s17, s16, 0x3c0
	s_lshl_b32 s26, s17, 4
	s_lshl_b32 s16, s16, 4
	v_lshl_add_u64 v[56:57], v[20:21], 0, s[26:27]
	s_or_b32 s26, s16, 0x4000
	v_lshl_add_u64 v[64:65], v[20:21], 0, s[26:27]
	global_load_dwordx4 v[76:79], v[56:57], off
	global_load_dwordx4 v[82:85], v[64:65], off
	s_add_i32 s16, s14, 0xc0
	s_and_b32 s16, s16, 0x1e0
	v_lshl_add_u32 v23, s16, 1, v19
	ds_read_b128 v[110:113], v23 offset:4096
	ds_read_b128 v[114:117], v23 offset:20736
	s_setprio 1
	s_waitcnt vmcnt(17) lgkmcnt(1)
	v_mfma_f32_16x16x32_f16 v[102:105], v[14:17], v[110:113], v[102:105]
	s_waitcnt lgkmcnt(0)
	v_mfma_f32_16x16x32_f16 v[14:17], v[14:17], v[114:117], v[28:31]
	s_waitcnt vmcnt(16)
	v_mfma_f32_16x16x32_f16 v[28:31], v[10:13], v[110:113], v[36:39]
	v_mfma_f32_16x16x32_f16 v[10:13], v[10:13], v[114:117], v[32:35]
	s_setprio 0
	s_addk_i32 s13, 0x3c0
	s_and_b32 s16, s13, 0x3c0
	s_lshl_b32 s26, s16, 4
	s_lshl_b32 s13, s13, 4
	v_lshl_add_u64 v[56:57], v[20:21], 0, s[26:27]
	s_or_b32 s26, s13, 0x4000
	v_lshl_add_u64 v[20:21], v[20:21], 0, s[26:27]
	global_load_dwordx4 v[32:35], v[56:57], off
	global_load_dwordx4 v[36:39], v[20:21], off
	s_add_i32 s13, s14, 0xe0
	s_and_b32 s13, s13, 0x1e0
	v_lshl_add_u32 v20, s13, 1, v19
	ds_read_b128 v[110:113], v20 offset:4096
	ds_read_b128 v[114:117], v20 offset:20736
	s_setprio 1
	s_waitcnt vmcnt(17) lgkmcnt(1)
	v_mfma_f32_16x16x32_f16 v[102:105], v[6:9], v[110:113], v[102:105]
	s_waitcnt lgkmcnt(0)
	v_mfma_f32_16x16x32_f16 v[6:9], v[6:9], v[114:117], v[14:17]
	s_waitcnt vmcnt(16)
	v_mfma_f32_16x16x32_f16 v[14:17], v[2:5], v[110:113], v[28:31]
	v_mfma_f32_16x16x32_f16 v[2:5], v[2:5], v[114:117], v[10:13]
	s_setprio 0
	v_add_u32_e32 v20, s15, v19
	s_nop 0
	ds_read_b128 v[10:13], v20 offset:4096
	ds_read_b128 v[28:31], v20 offset:20736
	s_setprio 1
	s_waitcnt vmcnt(15) lgkmcnt(1)
	v_mfma_f32_16x16x32_f16 v[102:105], v[86:89], v[10:13], v[102:105]
	s_waitcnt lgkmcnt(0)
	v_mfma_f32_16x16x32_f16 v[6:9], v[86:89], v[28:31], v[6:9]
	s_waitcnt vmcnt(14)
	v_mfma_f32_16x16x32_f16 v[10:13], v[90:93], v[10:13], v[14:17]
	v_mfma_f32_16x16x32_f16 v[2:5], v[90:93], v[28:31], v[2:5]
	s_setprio 0
	s_add_i32 s13, s14, 0x120
	s_and_b32 s13, s13, 0x1e0
	v_lshl_add_u32 v20, s13, 1, v19
	ds_read_b128 v[14:17], v20 offset:4096
	ds_read_b128 v[28:31], v20 offset:20736
	s_setprio 1
	s_waitcnt vmcnt(13) lgkmcnt(1)
	v_mfma_f32_16x16x32_f16 v[86:89], v[98:101], v[14:17], v[102:105]
	s_waitcnt lgkmcnt(0)
	v_mfma_f32_16x16x32_f16 v[6:9], v[98:101], v[28:31], v[6:9]
	s_waitcnt vmcnt(12)
	v_mfma_f32_16x16x32_f16 v[10:13], v[106:109], v[14:17], v[10:13]
	v_mfma_f32_16x16x32_f16 v[2:5], v[106:109], v[28:31], v[2:5]
	s_setprio 0
	s_add_i32 s13, s14, 0x140
	s_and_b32 s13, s13, 0x1e0
	v_lshl_add_u32 v20, s13, 1, v19
	ds_read_b128 v[14:17], v20 offset:4096
	ds_read_b128 v[28:31], v20 offset:20736
	s_setprio 1
	s_waitcnt vmcnt(11) lgkmcnt(1)
	v_mfma_f32_16x16x32_f16 v[86:89], v[40:43], v[14:17], v[86:89]
	s_waitcnt lgkmcnt(0)
	v_mfma_f32_16x16x32_f16 v[6:9], v[40:43], v[28:31], v[6:9]
	s_waitcnt vmcnt(10)
	v_mfma_f32_16x16x32_f16 v[10:13], v[94:97], v[14:17], v[10:13]
	v_mfma_f32_16x16x32_f16 v[2:5], v[94:97], v[28:31], v[2:5]
	s_setprio 0
	s_add_i32 s13, s14, 0x160
	s_and_b32 s13, s13, 0x1e0
	v_lshl_add_u32 v20, s13, 1, v19
	ds_read_b128 v[14:17], v20 offset:4096
	ds_read_b128 v[28:31], v20 offset:20736
	s_setprio 1
	s_waitcnt vmcnt(9) lgkmcnt(1)
	v_mfma_f32_16x16x32_f16 v[40:43], v[44:47], v[14:17], v[86:89]
	s_waitcnt lgkmcnt(0)
	v_mfma_f32_16x16x32_f16 v[6:9], v[44:47], v[28:31], v[6:9]
	s_waitcnt vmcnt(8)
	v_mfma_f32_16x16x32_f16 v[10:13], v[48:51], v[14:17], v[10:13]
	v_mfma_f32_16x16x32_f16 v[2:5], v[48:51], v[28:31], v[2:5]
	s_setprio 0
	s_add_i32 s13, s14, 0x180
	s_and_b32 s13, s13, 0x1e0
	v_lshl_add_u32 v20, s13, 1, v19
	ds_read_b128 v[14:17], v20 offset:4096
	ds_read_b128 v[28:31], v20 offset:20736
	s_setprio 1
	s_waitcnt vmcnt(7) lgkmcnt(1)
	v_mfma_f32_16x16x32_f16 v[40:43], v[52:55], v[14:17], v[40:43]
	s_waitcnt lgkmcnt(0)
	v_mfma_f32_16x16x32_f16 v[6:9], v[52:55], v[28:31], v[6:9]
	s_waitcnt vmcnt(6)
	v_mfma_f32_16x16x32_f16 v[10:13], v[60:63], v[14:17], v[10:13]
	v_mfma_f32_16x16x32_f16 v[2:5], v[60:63], v[28:31], v[2:5]
	s_setprio 0
	s_add_i32 s13, s14, 0x1a0
	s_and_b32 s13, s13, 0x1e0
	v_lshl_add_u32 v20, s13, 1, v19
	ds_read_b128 v[14:17], v20 offset:4096
	ds_read_b128 v[28:31], v20 offset:20736
	s_setprio 1
	s_waitcnt vmcnt(5) lgkmcnt(1)
	v_mfma_f32_16x16x32_f16 v[40:43], v[68:71], v[14:17], v[40:43]
	s_waitcnt lgkmcnt(0)
	v_mfma_f32_16x16x32_f16 v[6:9], v[68:71], v[28:31], v[6:9]
	s_waitcnt vmcnt(4)
	v_mfma_f32_16x16x32_f16 v[10:13], v[72:75], v[14:17], v[10:13]
	v_mfma_f32_16x16x32_f16 v[2:5], v[72:75], v[28:31], v[2:5]
	s_setprio 0
	s_add_i32 s13, s14, 0x1c0
	s_and_b32 s13, s13, 0x1e0
	v_lshl_add_u32 v20, s13, 1, v19
	ds_read_b128 v[14:17], v20 offset:4096
	ds_read_b128 v[28:31], v20 offset:20736
	s_setprio 1
	s_waitcnt vmcnt(3) lgkmcnt(1)
	v_mfma_f32_16x16x32_f16 v[40:43], v[76:79], v[14:17], v[40:43]
	s_waitcnt lgkmcnt(0)
	v_mfma_f32_16x16x32_f16 v[6:9], v[76:79], v[28:31], v[6:9]
	s_waitcnt vmcnt(2)
	v_mfma_f32_16x16x32_f16 v[10:13], v[82:85], v[14:17], v[10:13]
	v_mfma_f32_16x16x32_f16 v[2:5], v[82:85], v[28:31], v[2:5]
	s_setprio 0
	s_addk_i32 s14, 0x1e0
	s_and_b32 s13, s14, 0x1e0
	v_lshl_add_u32 v20, s13, 1, v19
	ds_read_b128 v[14:17], v20 offset:4096
	ds_read_b128 v[28:31], v20 offset:20736
	s_setprio 1
	s_waitcnt vmcnt(1) lgkmcnt(1)
	v_mfma_f32_16x16x32_f16 v[40:43], v[32:35], v[14:17], v[40:43]
	s_waitcnt lgkmcnt(0)
	v_mfma_f32_16x16x32_f16 v[6:9], v[32:35], v[28:31], v[6:9]
	s_waitcnt vmcnt(0)
	v_mfma_f32_16x16x32_f16 v[10:13], v[36:39], v[14:17], v[10:13]
	v_mfma_f32_16x16x32_f16 v[2:5], v[36:39], v[28:31], v[2:5]
	s_setprio 0
	v_add_u32_e32 v19, v19, v22
	v_lshlrev_b32_e32 v20, 15, v118
	v_mov_b32_e32 v21, v67
	s_bfe_u32 s22, s2, 0x30003
	v_lshl_add_u64 v[20:21], s[10:11], 0, v[20:21]
	s_lshl_b32 s26, s22, 10
	v_lshl_add_u64 v[64:65], v[20:21], 0, v[58:59]
	v_lshl_add_u64 v[52:53], v[64:65], 0, s[26:27]
	v_add_co_u32_e32 v76, vcc, s29, v52
	s_lshl_b32 s53, s22, 6
	s_nop 0
	v_addc_co_u32_e32 v77, vcc, 0, v53, vcc
	s_mov_b32 s14, 0x14000
	v_mov_b32_e32 v22, 0x14000
	v_mul_u32_u24_e32 v23, 0x210, v81
	s_add_i32 s38, s53, 64
	v_lshlrev_b32_e32 v83, 2, v118
	s_movk_i32 s16, 0x1040
	s_movk_i32 s18, 0x840
	v_lshl_or_b32 v1, v1, 3, v22
	v_add3_u32 v84, v23, v18, s14
	s_and_b32 s14, s38, 0x1c0
	s_movk_i32 s20, 0x210
	s_mov_b32 s19, s27
	v_mad_u32_u24 v56, v118, s16, v58
	v_or_b32_e32 v22, 1, v83
	v_mad_u32_u24 v98, v118, s18, v1
	s_lshl_b32 s18, s14, 4
	v_mad_u32_u24 v99, v22, s12, v58
	v_mad_u32_u24 v85, v22, s20, v1
	v_lshl_add_u64 v[54:55], v[64:65], 0, s[18:19]
	s_add_i32 s12, s53, 0xc0
	s_and_b32 s2, s3, 0x7ffffff
	s_lshl_b32 s3, s22, 5
	s_and_b32 s39, s12, 0x1c0
	s_lshl_b32 s14, s39, 4
	s_add_i32 s39, s3, 32
	s_and_b32 s39, s39, 0xe0
	v_lshl_add_u32 v82, s39, 1, v84
	s_add_i32 s11, s53, 0x80
	s_lshl_b32 s16, s38, 4
	s_mov_b32 s21, s27
	s_and_b32 s30, s11, 0x1c0
	s_lshl_b32 s11, s11, 4
	s_or_b32 s20, s16, 0x2000
	s_mov_b32 s23, s27
	s_mov_b32 s31, s27
	s_mov_b32 s35, s27
	s_or_b32 s22, s16, 0x6000
	s_lshl_b32 s30, s30, 4
	s_or_b32 s34, s11, 0x2000
	v_lshl_add_u64 v[26:27], v[64:65], 0, s[20:21]
	v_lshl_add_u64 v[28:29], v[64:65], 0, s[22:23]
	v_lshl_add_u64 v[30:31], v[64:65], 0, s[30:31]
	v_lshl_add_u64 v[32:33], v[64:65], 0, s[34:35]
	s_mov_b64 s[40:41], 0x40000
	v_lshl_add_u64 v[60:61], v[64:65], 0, s[40:41]
	s_mov_b32 s37, s27
	s_or_b32 s36, s11, 0x6000
	v_lshl_add_u64 v[74:75], v[64:65], 0, s[36:37]
	s_mov_b32 s15, s27
	s_lshl_b32 s12, s12, 4
	v_lshl_add_u64 v[70:71], v[64:65], 0, s[14:15]
	s_mov_b32 s17, s27
	s_or_b32 s16, s12, 0x2000
	s_mov_b32 s13, s27
	s_or_b32 s12, s12, 0x6000
	v_lshl_add_u64 v[72:73], v[64:65], 0, s[16:17]
	v_lshl_add_u64 v[68:69], v[64:65], 0, s[12:13]
	v_add_u32_e32 v1, s53, v84
	s_xor_b32 s10, s26, 0x1000
	s_mov_b32 s11, s27
	s_mov_b32 s49, s27
	s_mov_b32 s51, s27
	s_mov_b32 s47, s27
	v_pk_add_f32 v[14:15], v[180:181], v[40:41]
	v_pk_add_f32 v[16:17], v[182:183], v[42:43]
	v_pk_add_f32 v[10:11], v[184:185], v[10:11]
	v_pk_add_f32 v[12:13], v[186:187], v[12:13]
	v_pk_add_f32 v[6:7], v[188:189], v[6:7]
	v_pk_add_f32 v[8:9], v[190:191], v[8:9]
	v_pk_add_f32 v[2:3], v[192:193], v[2:3]
	v_pk_add_f32 v[4:5], v[194:195], v[4:5]
	ds_write_b128 v19, v[14:17] offset:37376
	ds_write_b128 v19, v[10:13] offset:37440
	ds_write_b128 v19, v[6:9] offset:54016
	ds_write_b128 v19, v[2:5] offset:54080
	v_mov_b64_e32 v[34:35], v[204:205]
	v_mov_b64_e32 v[36:37], v[206:207]
	v_mov_b64_e32 v[38:39], v[208:209]
	v_mov_b64_e32 v[40:41], v[210:211]
	v_add_co_u32_e32 v2, vcc, s52, v52
	s_waitcnt lgkmcnt(0)
	s_nop 0
	v_addc_co_u32_e32 v3, vcc, 0, v53, vcc
	v_add_co_u32_e32 v4, vcc, s33, v52
	s_barrier
	s_nop 0
	v_addc_co_u32_e32 v5, vcc, 0, v53, vcc
	global_load_dwordx4 v[14:17], v[2:3], off
	global_load_dwordx4 v[18:21], v[4:5], off
	global_load_dwordx4 v[22:25], v[52:53], off
	global_load_dwordx4 v[10:13], v[54:55], off
	ds_read_b128 v[2:5], v56 offset:37376
	ds_read_b128 v[6:9], v99 offset:37376
	v_add_co_u32_e32 v78, vcc, s52, v54
	s_mov_b32 s43, s27
	s_waitcnt lgkmcnt(1)
	v_add_f32_e32 v42, v2, v3
	v_add_f32_e32 v42, v42, v4
	v_add_f32_e32 v42, v42, v5
	v_addc_co_u32_e32 v79, vcc, 0, v55, vcc
	s_nop 0
	v_add_f32_dpp v42, v42, v42 quad_perm:[1,0,3,2] row_mask:0xf bank_mask:0xf bound_ctrl:1
	s_mov_b32 s45, s27
	s_mov_b32 s41, s27
	v_add_f32_dpp v42, v42, v42 quad_perm:[2,3,0,1] row_mask:0xf bank_mask:0xf bound_ctrl:1
	v_lshl_add_u64 v[62:63], v[64:65], 0, s[10:11]
	v_lshl_add_u64 v[58:59], s[4:5], 0, v[58:59]
	v_add_f32_dpp v42, v42, v42 row_half_mirror row_mask:0xf bank_mask:0xf bound_ctrl:1
	v_lshl_add_u64 v[152:153], v[60:61], 0, s[26:27]
	v_lshl_add_u64 v[154:155], v[60:61], 0, s[18:19]
	v_add_f32_dpp v42, v42, v42 row_mirror row_mask:0xf bank_mask:0xf bound_ctrl:1
	v_lshl_add_u64 v[156:157], v[60:61], 0, s[20:21]
	v_readlane_b32 s8, v42, 16
	v_readlane_b32 s9, v42, 48
	v_readlane_b32 s6, v42, 0
	v_readlane_b32 s7, v42, 32
	v_mov_b32_e32 v42, s8
	v_mov_b32_e32 v43, s9
	v_pk_add_f32 v[42:43], s[6:7], v[42:43]
	s_mov_b32 s6, 0x3b800000
	v_add_f32_e32 v42, v42, v43
	v_mul_f32_e32 v42, 0x3b800000, v42
	v_pk_add_f32 v[86:87], v[2:3], v[42:43] op_sel_hi:[1,0] neg_lo:[0,1] neg_hi:[0,1]
	v_pk_add_f32 v[88:89], v[4:5], v[42:43] op_sel_hi:[1,0] neg_lo:[0,1] neg_hi:[0,1]
	v_pk_mul_f32 v[42:43], v[86:87], v[86:87]
	v_pk_mul_f32 v[44:45], v[88:89], v[88:89]
	v_add_f32_e32 v42, v42, v43
	v_add_f32_e32 v42, v44, v42
	s_waitcnt lgkmcnt(0)
	v_add_f32_e32 v44, v6, v7
	v_add_f32_e32 v42, v45, v42
	v_add_f32_e32 v44, v44, v8
	v_add_f32_e32 v44, v44, v9
	v_add_f32_dpp v42, v42, v42 quad_perm:[1,0,3,2] row_mask:0xf bank_mask:0xf bound_ctrl:1
	v_lshl_add_u64 v[158:159], v[60:61], 0, s[22:23]
	v_add_f32_dpp v44, v44, v44 quad_perm:[1,0,3,2] row_mask:0xf bank_mask:0xf bound_ctrl:1
	v_add_f32_dpp v42, v42, v42 quad_perm:[2,3,0,1] row_mask:0xf bank_mask:0xf bound_ctrl:1
	v_lshl_add_u64 v[160:161], v[60:61], 0, s[30:31]
	v_add_f32_dpp v44, v44, v44 quad_perm:[2,3,0,1] row_mask:0xf bank_mask:0xf bound_ctrl:1
	v_add_f32_dpp v42, v42, v42 row_half_mirror row_mask:0xf bank_mask:0xf bound_ctrl:1
	v_lshl_add_u64 v[162:163], v[60:61], 0, s[34:35]
	v_add_f32_dpp v44, v44, v44 row_half_mirror row_mask:0xf bank_mask:0xf bound_ctrl:1
	v_add_f32_dpp v42, v42, v42 row_mirror row_mask:0xf bank_mask:0xf bound_ctrl:1
	v_lshl_add_u64 v[164:165], v[60:61], 0, s[36:37]
	v_readlane_b32 s7, v42, 16
	v_readlane_b32 s39, v42, 48
	v_add_f32_dpp v44, v44, v44 row_mirror row_mask:0xf bank_mask:0xf bound_ctrl:1
	v_readlane_b32 s8, v42, 0
	v_readlane_b32 s9, v42, 32
	v_mov_b32_e32 v42, s7
	v_mov_b32_e32 v43, s39
	v_readlane_b32 s7, v44, 16
	v_readlane_b32 s39, v44, 48
	v_pk_add_f32 v[42:43], s[8:9], v[42:43]
	v_readlane_b32 s8, v44, 0
	v_readlane_b32 s9, v44, 32
	v_mov_b32_e32 v44, s7
	v_mov_b32_e32 v45, s39
	v_pk_add_f32 v[44:45], s[8:9], v[44:45]
	s_nop 0
	v_add_f32_e32 v44, v44, v45
	v_mul_f32_e32 v44, 0x3b800000, v44
	v_pk_add_f32 v[90:91], v[6:7], v[44:45] op_sel_hi:[1,0] neg_lo:[0,1] neg_hi:[0,1]
	v_pk_add_f32 v[92:93], v[8:9], v[44:45] op_sel_hi:[1,0] neg_lo:[0,1] neg_hi:[0,1]
	v_pk_mul_f32 v[46:47], v[90:91], v[90:91]
	v_pk_mul_f32 v[44:45], v[92:93], v[92:93]
	v_add_f32_e32 v46, v46, v47
	v_add_f32_e32 v44, v44, v46
	v_add_f32_e32 v44, v45, v44
	v_mov_b32_e32 v47, v42
	s_nop 0
	v_add_f32_dpp v44, v44, v44 quad_perm:[1,0,3,2] row_mask:0xf bank_mask:0xf bound_ctrl:1
	s_nop 1
	v_add_f32_dpp v44, v44, v44 quad_perm:[2,3,0,1] row_mask:0xf bank_mask:0xf bound_ctrl:1
	s_nop 1
	v_add_f32_dpp v44, v44, v44 row_half_mirror row_mask:0xf bank_mask:0xf bound_ctrl:1
	s_nop 1
	v_add_f32_dpp v44, v44, v44 row_mirror row_mask:0xf bank_mask:0xf bound_ctrl:1
	s_nop 0
	v_readlane_b32 s7, v44, 16
	v_readlane_b32 s39, v44, 48
	v_readlane_b32 s8, v44, 0
	v_readlane_b32 s9, v44, 32
	v_mov_b32_e32 v44, s7
	v_mov_b32_e32 v45, s39
	v_pk_add_f32 v[44:45], s[8:9], v[44:45]
	s_mov_b32 s8, 0x3727c5ac
	v_mov_b32_e32 v46, v44
	v_mov_b32_e32 v42, v45
	v_pk_add_f32 v[42:43], v[46:47], v[42:43]
	v_mov_b64_e32 v[94:95], s[8:9]
	v_pk_fma_f32 v[96:97], v[42:43], s[6:7], v[94:95] op_sel_hi:[1,0,0]
	s_mov_b32 s7, 0x800000
	v_mul_f32_e32 v42, 0x4b800000, v97
	v_cmp_gt_f32_e32 vcc, s7, v97
	s_nop 1
	v_cndmask_b32_e32 v42, v97, v42, vcc
	v_rsq_f32_e32 v97, v42
	global_load_dwordx4 v[54:57], v[26:27], off
	global_load_dwordx4 v[50:53], v[28:29], off
	global_load_dwordx4 v[46:49], v[30:31], off
	global_load_dwordx4 v[42:45], v[32:33], off
	v_mul_f32_e32 v26, 0x45800000, v97
	v_cndmask_b32_e32 v26, v97, v26, vcc
	v_pk_mul_f32 v[28:29], v[86:87], v[26:27] op_sel_hi:[1,0]
	v_cmp_gt_f32_e32 vcc, s7, v96
	s_waitcnt vmcnt(8)
	v_pk_fma_f32 v[28:29], v[34:35], v[28:29], v[38:39]
	v_pk_mul_f32 v[26:27], v[88:89], v[26:27] op_sel_hi:[1,0]
	v_cvt_pk_f16_f32 v28, v28, v29
	v_mul_f32_e32 v29, 0x4b800000, v96
	v_cndmask_b32_e32 v29, v96, v29, vcc
	v_rsq_f32_e32 v32, v29
	v_pk_fma_f32 v[26:27], v[36:37], v[26:27], v[40:41]
	s_nop 0
	v_cvt_pk_f16_f32 v29, v26, v27
	v_mul_f32_e32 v26, 0x45800000, v32
	v_cndmask_b32_e32 v26, v32, v26, vcc
	ds_write_b64 v98, v[28:29]
	v_pk_mul_f32 v[28:29], v[90:91], v[26:27] op_sel_hi:[1,0]
	v_pk_mul_f32 v[26:27], v[92:93], v[26:27] op_sel_hi:[1,0]
	v_pk_fma_f32 v[28:29], v[34:35], v[28:29], v[38:39]
	v_pk_fma_f32 v[26:27], v[36:37], v[26:27], v[40:41]
	v_cvt_pk_f16_f32 v28, v28, v29
	v_cvt_pk_f16_f32 v29, v26, v27
	ds_write_b64 v85, v[28:29]
	ds_read_b128 v[26:29], v99 offset:38416
	v_add_co_u32_e32 v102, vcc, s52, v30
	s_nop 1
	v_addc_co_u32_e32 v103, vcc, 0, v31, vcc
	ds_read_b128 v[30:33], v99 offset:39456
	s_waitcnt lgkmcnt(1)
	v_add_f32_e32 v86, v26, v27
	v_add_f32_e32 v86, v86, v28
	v_add_f32_e32 v86, v86, v29
	s_nop 1
	v_add_f32_dpp v86, v86, v86 quad_perm:[1,0,3,2] row_mask:0xf bank_mask:0xf bound_ctrl:1
	s_nop 1
	v_add_f32_dpp v86, v86, v86 quad_perm:[2,3,0,1] row_mask:0xf bank_mask:0xf bound_ctrl:1
	s_nop 1
	v_add_f32_dpp v86, v86, v86 row_half_mirror row_mask:0xf bank_mask:0xf bound_ctrl:1
	s_nop 1
	v_add_f32_dpp v86, v86, v86 row_mirror row_mask:0xf bank_mask:0xf bound_ctrl:1
	s_nop 0
	v_readlane_b32 s39, v86, 16
	v_readlane_b32 s40, v86, 48
	v_readlane_b32 s8, v86, 0
	v_readlane_b32 s9, v86, 32
	v_mov_b32_e32 v86, s39
	v_mov_b32_e32 v87, s40
	v_pk_add_f32 v[86:87], s[8:9], v[86:87]
	s_nop 0
	v_add_f32_e32 v86, v86, v87
	v_mul_f32_e32 v86, 0x3b800000, v86
	v_pk_add_f32 v[104:105], v[26:27], v[86:87] op_sel_hi:[1,0] neg_lo:[0,1] neg_hi:[0,1]
	v_pk_add_f32 v[106:107], v[28:29], v[86:87] op_sel_hi:[1,0] neg_lo:[0,1] neg_hi:[0,1]
	v_pk_mul_f32 v[88:89], v[104:105], v[104:105]
	v_pk_mul_f32 v[86:87], v[106:107], v[106:107]
	v_add_f32_e32 v88, v88, v89
	v_add_f32_e32 v86, v86, v88
	s_waitcnt lgkmcnt(0)
	v_add_f32_e32 v88, v30, v31
	v_add_f32_e32 v86, v87, v86
	v_add_f32_e32 v88, v88, v32
	v_add_f32_e32 v88, v88, v33
	v_add_f32_dpp v86, v86, v86 quad_perm:[1,0,3,2] row_mask:0xf bank_mask:0xf bound_ctrl:1
	s_nop 0
	v_add_f32_dpp v88, v88, v88 quad_perm:[1,0,3,2] row_mask:0xf bank_mask:0xf bound_ctrl:1
	v_add_f32_dpp v86, v86, v86 quad_perm:[2,3,0,1] row_mask:0xf bank_mask:0xf bound_ctrl:1
	s_nop 0
	v_add_f32_dpp v88, v88, v88 quad_perm:[2,3,0,1] row_mask:0xf bank_mask:0xf bound_ctrl:1
	v_add_f32_dpp v86, v86, v86 row_half_mirror row_mask:0xf bank_mask:0xf bound_ctrl:1
	s_nop 0
	v_add_f32_dpp v88, v88, v88 row_half_mirror row_mask:0xf bank_mask:0xf bound_ctrl:1
	v_add_f32_dpp v86, v86, v86 row_mirror row_mask:0xf bank_mask:0xf bound_ctrl:1
	s_nop 0
	v_readlane_b32 s39, v86, 16
	v_readlane_b32 s40, v86, 48
	v_add_f32_dpp v88, v88, v88 row_mirror row_mask:0xf bank_mask:0xf bound_ctrl:1
	v_readlane_b32 s8, v86, 0
	v_readlane_b32 s9, v86, 32
	v_mov_b32_e32 v86, s39
	v_mov_b32_e32 v87, s40
	v_readlane_b32 s39, v88, 16
	v_readlane_b32 s40, v88, 48
	v_pk_add_f32 v[86:87], s[8:9], v[86:87]
	v_readlane_b32 s8, v88, 0
	v_readlane_b32 s9, v88, 32
	v_mov_b32_e32 v88, s39
	v_mov_b32_e32 v89, s40
	v_pk_add_f32 v[88:89], s[8:9], v[88:89]
	s_nop 0
	v_add_f32_e32 v88, v88, v89
	v_mul_f32_e32 v88, 0x3b800000, v88
	v_pk_add_f32 v[108:109], v[30:31], v[88:89] op_sel_hi:[1,0] neg_lo:[0,1] neg_hi:[0,1]
	v_pk_add_f32 v[110:111], v[32:33], v[88:89] op_sel_hi:[1,0] neg_lo:[0,1] neg_hi:[0,1]
	v_pk_mul_f32 v[90:91], v[108:109], v[108:109]
	v_pk_mul_f32 v[88:89], v[110:111], v[110:111]
	v_add_f32_e32 v90, v90, v91
	v_add_f32_e32 v88, v88, v90
	v_add_f32_e32 v88, v89, v88
	v_mov_b32_e32 v91, v86
	s_nop 0
	v_add_f32_dpp v88, v88, v88 quad_perm:[1,0,3,2] row_mask:0xf bank_mask:0xf bound_ctrl:1
	s_nop 1
	v_add_f32_dpp v88, v88, v88 quad_perm:[2,3,0,1] row_mask:0xf bank_mask:0xf bound_ctrl:1
	s_nop 1
	v_add_f32_dpp v88, v88, v88 row_half_mirror row_mask:0xf bank_mask:0xf bound_ctrl:1
	s_nop 1
	v_add_f32_dpp v88, v88, v88 row_mirror row_mask:0xf bank_mask:0xf bound_ctrl:1
	s_nop 0
	v_readlane_b32 s39, v88, 16
	v_readlane_b32 s40, v88, 48
	v_readlane_b32 s8, v88, 0
	v_readlane_b32 s9, v88, 32
	v_mov_b32_e32 v88, s39
	v_mov_b32_e32 v89, s40
	v_pk_add_f32 v[88:89], s[8:9], v[88:89]
	s_mov_b32 s9, s27
	v_mov_b32_e32 v90, v88
	v_mov_b32_e32 v86, v89
	v_pk_add_f32 v[86:87], v[90:91], v[86:87]
	s_mov_b32 s39, s27
	v_pk_fma_f32 v[112:113], v[86:87], s[6:7], v[94:95] op_sel_hi:[1,0,0]
	s_add_i32 s6, s53, 0x140
	v_mul_f32_e32 v86, 0x4b800000, v113
	v_cmp_gt_f32_e32 vcc, s7, v113
	s_nop 1
	v_cndmask_b32_e32 v86, v113, v86, vcc
	v_rsq_f32_e32 v113, v86
	global_load_dwordx4 v[86:89], v[78:79], off
	global_load_dwordx4 v[90:93], v[102:103], off
	global_load_dwordx4 v[94:97], v[76:77], off
	global_load_dwordx4 v[98:101], v[74:75], off
	v_mul_f32_e32 v74, 0x45800000, v113
	v_cndmask_b32_e32 v74, v113, v74, vcc
	v_pk_mul_f32 v[76:77], v[104:105], v[74:75] op_sel_hi:[1,0]
	v_mul_f32_e32 v75, 0x4b800000, v112
	v_cmp_gt_f32_e32 vcc, s7, v112
	v_pk_fma_f32 v[76:77], v[34:35], v[76:77], v[38:39]
	s_and_b32 s7, s6, 0x1c0
	v_cndmask_b32_e32 v75, v112, v75, vcc
	v_rsq_f32_e32 v78, v75
	v_pk_mul_f32 v[74:75], v[106:107], v[74:75] op_sel_hi:[1,0]
	v_cvt_pk_f16_f32 v76, v76, v77
	v_pk_fma_f32 v[74:75], v[36:37], v[74:75], v[40:41]
	s_lshl_b32 s6, s6, 4
	v_cvt_pk_f16_f32 v77, v74, v75
	v_mul_f32_e32 v74, 0x45800000, v78
	v_cndmask_b32_e32 v74, v78, v74, vcc
	v_pk_mul_f32 v[78:79], v[108:109], v[74:75] op_sel_hi:[1,0]
	s_or_b32 s50, s6, 0x2000
	v_pk_fma_f32 v[34:35], v[34:35], v[78:79], v[38:39]
	v_pk_mul_f32 v[38:39], v[110:111], v[74:75] op_sel_hi:[1,0]
	v_add_co_u32_e32 v78, vcc, s52, v70
	v_pk_fma_f32 v[36:37], v[36:37], v[38:39], v[40:41]
	v_cvt_pk_f16_f32 v34, v34, v35
	v_cvt_pk_f16_f32 v35, v36, v37
	v_addc_co_u32_e32 v79, vcc, 0, v71, vcc
	ds_write2_b64 v85, v[76:77], v[34:35] offset0:66 offset1:132
	s_waitcnt lgkmcnt(0)
	s_barrier
	global_load_dwordx4 v[34:37], v[70:71], off
	global_load_dwordx4 v[38:41], v[72:73], off
	s_nop 0
	global_load_dwordx4 v[70:73], v[78:79], off
	global_load_dwordx4 v[74:77], v[68:69], off
	s_or_b32 s46, s6, 0x6000
	s_sub_i32 s6, s38, s3
	s_and_b32 s6, s6, 0xe0
	v_lshl_add_u32 v172, s6, 1, v84
	s_add_i32 s6, s53, 0x180
	s_lshl_b32 s48, s7, 4
	s_and_b32 s7, s6, 0x1c0
	s_lshl_b32 s6, s6, 4
	s_or_b32 s44, s6, 0x2000
	s_or_b32 s40, s6, 0x6000
	s_add_i32 s6, s3, 0x60
	s_and_b32 s6, s6, 0xe0
	v_lshl_add_u32 v173, s6, 1, v84
	s_add_i32 s6, s53, 0x1c0
	s_xor_b32 s53, s53, 0x100
	v_add_u32_e32 v174, s53, v84
	s_add_i32 s53, s3, 0xa0
	s_lshl_b32 s42, s7, 4
	s_and_b32 s7, s6, 0x1c0
	s_lshl_b32 s6, s6, 4
	s_and_b32 s53, s53, 0xe0
	s_lshl_b32 s8, s7, 4
	s_or_b32 s38, s6, 0x2000
	s_or_b32 s6, s6, 0x6000
	s_mov_b32 s7, s27
	v_lshl_add_u32 v175, s53, 1, v84
	s_add_i32 s53, s3, 0xc0
	s_addk_i32 s3, 0xe0
	v_lshl_add_u64 v[68:69], v[64:65], 0, s[48:49]
	v_lshl_add_u64 v[78:79], v[64:65], 0, s[50:51]
	v_lshl_add_u64 v[138:139], v[64:65], 0, s[46:47]
	v_lshl_add_u64 v[140:141], v[64:65], 0, s[42:43]
	v_lshl_add_u64 v[142:143], v[64:65], 0, s[44:45]
	v_lshl_add_u64 v[144:145], v[64:65], 0, s[40:41]
	v_lshl_add_u64 v[146:147], v[64:65], 0, s[8:9]
	v_lshl_add_u64 v[148:149], v[64:65], 0, s[38:39]
	v_lshl_add_u64 v[150:151], v[64:65], 0, s[6:7]
	s_and_b32 s53, s53, 0xe0
	s_and_b32 s3, s3, 0xe0
	v_add_u32_e32 v64, s28, v83
	v_mov_b32_e32 v65, v67
	v_lshl_add_u32 v176, s53, 1, v84
	v_lshl_add_u32 v177, s3, 1, v84
	v_lshlrev_b64 v[84:85], 10, v[64:65]
	ds_read_b128 v[102:105], v1
	ds_read_b128 v[106:109], v1 offset:8448
	v_lshl_add_u64 v[166:167], v[58:59], 0, v[84:85]
	v_or_b32_e32 v84, 1, v64
	v_mov_b32_e32 v85, v67
	v_lshlrev_b64 v[84:85], 10, v[84:85]
	v_lshl_add_u64 v[168:169], v[58:59], 0, v[84:85]
	v_or_b32_e32 v84, 2, v64
	v_mov_b32_e32 v85, v67
	v_or_b32_e32 v64, 3, v64
	v_lshlrev_b64 v[84:85], 10, v[84:85]
	v_lshlrev_b64 v[64:65], 10, v[64:65]
	v_lshl_add_u64 v[170:171], v[58:59], 0, v[84:85]
	v_lshl_add_u64 v[58:59], v[58:59], 0, v[64:65]
	s_setprio 1
	s_waitcnt vmcnt(13) lgkmcnt(1)
	v_mfma_f32_16x16x32_f16 v[110:113], v[102:105], v[22:25], 0
	s_waitcnt lgkmcnt(0)
	v_mfma_f32_16x16x32_f16 v[22:25], v[106:109], v[22:25], 0
	s_waitcnt vmcnt(5)
	v_mfma_f32_16x16x32_f16 v[114:117], v[102:105], v[94:97], 0
	v_mfma_f32_16x16x32_f16 v[94:97], v[106:109], v[94:97], 0
	v_mfma_f32_16x16x32_f16 v[118:121], v[102:105], v[14:17], 0
	v_mfma_f32_16x16x32_f16 v[14:17], v[106:109], v[14:17], 0
	v_mfma_f32_16x16x32_f16 v[102:105], v[102:105], v[18:21], 0
	v_mfma_f32_16x16x32_f16 v[18:21], v[106:109], v[18:21], 0
	s_setprio 0
	v_add_co_u32_e32 v64, vcc, s29, v62
	global_load_dwordx4 v[106:109], v[62:63], off
	s_nop 0
	v_addc_co_u32_e32 v65, vcc, 0, v63, vcc
	v_add_co_u32_e32 v84, vcc, s52, v62
	s_nop 1
	v_addc_co_u32_e32 v85, vcc, 0, v63, vcc
	v_add_co_u32_e32 v62, vcc, s33, v62
	global_load_dwordx4 v[122:125], v[64:65], off
	global_load_dwordx4 v[126:129], v[84:85], off
	v_addc_co_u32_e32 v63, vcc, 0, v63, vcc
	global_load_dwordx4 v[62:65], v[62:63], off
	ds_read_b128 v[130:133], v82
	ds_read_b128 v[134:137], v82 offset:8448
	s_setprio 1
	s_waitcnt lgkmcnt(1)
	v_mfma_f32_16x16x32_f16 v[110:113], v[130:133], v[10:13], v[110:113]
	s_waitcnt lgkmcnt(0)
	v_mfma_f32_16x16x32_f16 v[10:13], v[134:137], v[10:13], v[22:25]
	v_mfma_f32_16x16x32_f16 v[22:25], v[130:133], v[54:57], v[114:117]
	v_mfma_f32_16x16x32_f16 v[54:57], v[134:137], v[54:57], v[94:97]
	v_mfma_f32_16x16x32_f16 v[94:97], v[130:133], v[86:89], v[118:121]
	v_mfma_f32_16x16x32_f16 v[14:17], v[134:137], v[86:89], v[14:17]
	v_mfma_f32_16x16x32_f16 v[84:87], v[130:133], v[50:53], v[102:105]
	v_mfma_f32_16x16x32_f16 v[18:21], v[134:137], v[50:53], v[18:21]
	s_setprio 0
	global_load_dwordx4 v[50:53], v[68:69], off
	global_load_dwordx4 v[102:105], v[78:79], off
	v_add_co_u32_e32 v68, vcc, s52, v68
	s_nop 1
	v_addc_co_u32_e32 v69, vcc, 0, v69, vcc
	global_load_dwordx4 v[114:117], v[68:69], off
	global_load_dwordx4 v[118:121], v[138:139], off
	ds_read_b128 v[130:133], v172
	ds_read_b128 v[134:137], v172 offset:8448
	s_setprio 1
	s_waitcnt lgkmcnt(1)
	v_mfma_f32_16x16x32_f16 v[110:113], v[130:133], v[46:49], v[110:113]
	s_waitcnt lgkmcnt(0)
	v_mfma_f32_16x16x32_f16 v[10:13], v[134:137], v[46:49], v[10:13]
	v_mfma_f32_16x16x32_f16 v[22:25], v[130:133], v[42:45], v[22:25]
	v_mfma_f32_16x16x32_f16 v[42:45], v[134:137], v[42:45], v[54:57]
	v_mfma_f32_16x16x32_f16 v[46:49], v[130:133], v[90:93], v[94:97]
	v_mfma_f32_16x16x32_f16 v[14:17], v[134:137], v[90:93], v[14:17]
	s_waitcnt vmcnt(12)
	v_mfma_f32_16x16x32_f16 v[54:57], v[130:133], v[98:101], v[84:87]
	v_mfma_f32_16x16x32_f16 v[18:21], v[134:137], v[98:101], v[18:21]
	s_setprio 0
	v_add_co_u32_e32 v68, vcc, s52, v140
	global_load_dwordx4 v[84:87], v[140:141], off
	global_load_dwordx4 v[88:91], v[142:143], off
	v_addc_co_u32_e32 v69, vcc, 0, v141, vcc
	global_load_dwordx4 v[92:95], v[68:69], off
	global_load_dwordx4 v[96:99], v[144:145], off
	ds_read_b128 v[130:133], v173
	ds_read_b128 v[134:137], v173 offset:8448
	s_setprio 1
	s_waitcnt vmcnt(15) lgkmcnt(1)
	v_mfma_f32_16x16x32_f16 v[110:113], v[130:133], v[34:37], v[110:113]
	s_waitcnt lgkmcnt(0)
	v_mfma_f32_16x16x32_f16 v[10:13], v[134:137], v[34:37], v[10:13]
	s_waitcnt vmcnt(14)
	v_mfma_f32_16x16x32_f16 v[22:25], v[130:133], v[38:41], v[22:25]
	v_mfma_f32_16x16x32_f16 v[34:37], v[134:137], v[38:41], v[42:45]
	s_waitcnt vmcnt(13)
	v_mfma_f32_16x16x32_f16 v[38:41], v[130:133], v[70:73], v[46:49]
	v_mfma_f32_16x16x32_f16 v[14:17], v[134:137], v[70:73], v[14:17]
	s_waitcnt vmcnt(12)
	v_mfma_f32_16x16x32_f16 v[42:45], v[130:133], v[74:77], v[54:57]
	v_mfma_f32_16x16x32_f16 v[18:21], v[134:137], v[74:77], v[18:21]
	s_setprio 0
	v_add_co_u32_e32 v68, vcc, s52, v146
	global_load_dwordx4 v[46:49], v[146:147], off
	global_load_dwordx4 v[54:57], v[148:149], off
	v_addc_co_u32_e32 v69, vcc, 0, v147, vcc
	global_load_dwordx4 v[68:71], v[68:69], off
	s_nop 0
	global_load_dwordx4 v[72:75], v[150:151], off
	ds_read_b128 v[76:79], v174
	ds_read_b128 v[130:133], v174 offset:8448
	s_setprio 1
	s_waitcnt vmcnt(15) lgkmcnt(1)
	v_mfma_f32_16x16x32_f16 v[110:113], v[76:79], v[106:109], v[110:113]
	s_waitcnt lgkmcnt(0)
	v_mfma_f32_16x16x32_f16 v[10:13], v[130:133], v[106:109], v[10:13]
	s_waitcnt vmcnt(14)
	v_mfma_f32_16x16x32_f16 v[22:25], v[76:79], v[122:125], v[22:25]
	v_mfma_f32_16x16x32_f16 v[34:37], v[130:133], v[122:125], v[34:37]
	s_waitcnt vmcnt(13)
	v_mfma_f32_16x16x32_f16 v[38:41], v[76:79], v[126:129], v[38:41]
	v_mfma_f32_16x16x32_f16 v[14:17], v[130:133], v[126:129], v[14:17]
	s_waitcnt vmcnt(12)
	v_mfma_f32_16x16x32_f16 v[42:45], v[76:79], v[62:65], v[42:45]
	v_mfma_f32_16x16x32_f16 v[18:21], v[130:133], v[62:65], v[18:21]
	s_setprio 0
	ds_read_b128 v[62:65], v175
	ds_read_b128 v[76:79], v175 offset:8448
	s_setprio 1
	s_waitcnt vmcnt(11) lgkmcnt(1)
	v_mfma_f32_16x16x32_f16 v[106:109], v[62:65], v[50:53], v[110:113]
	s_waitcnt lgkmcnt(0)
	v_mfma_f32_16x16x32_f16 v[10:13], v[76:79], v[50:53], v[10:13]
	s_waitcnt vmcnt(10)
	v_mfma_f32_16x16x32_f16 v[22:25], v[62:65], v[102:105], v[22:25]
	v_mfma_f32_16x16x32_f16 v[34:37], v[76:79], v[102:105], v[34:37]
	s_waitcnt vmcnt(9)
	v_mfma_f32_16x16x32_f16 v[38:41], v[62:65], v[114:117], v[38:41]
	v_mfma_f32_16x16x32_f16 v[14:17], v[76:79], v[114:117], v[14:17]
	s_waitcnt vmcnt(8)
	v_mfma_f32_16x16x32_f16 v[42:45], v[62:65], v[118:121], v[42:45]
	v_mfma_f32_16x16x32_f16 v[18:21], v[76:79], v[118:121], v[18:21]
	s_setprio 0
	ds_read_b128 v[50:53], v176
	ds_read_b128 v[62:65], v176 offset:8448
	s_setprio 1
	s_waitcnt vmcnt(7) lgkmcnt(1)
	v_mfma_f32_16x16x32_f16 v[76:79], v[50:53], v[84:87], v[106:109]
	s_waitcnt lgkmcnt(0)
	v_mfma_f32_16x16x32_f16 v[10:13], v[62:65], v[84:87], v[10:13]
	s_waitcnt vmcnt(6)
	v_mfma_f32_16x16x32_f16 v[22:25], v[50:53], v[88:91], v[22:25]
	v_mfma_f32_16x16x32_f16 v[34:37], v[62:65], v[88:91], v[34:37]
	s_waitcnt vmcnt(5)
	v_mfma_f32_16x16x32_f16 v[38:41], v[50:53], v[92:95], v[38:41]
	v_mfma_f32_16x16x32_f16 v[14:17], v[62:65], v[92:95], v[14:17]
	s_waitcnt vmcnt(4)
	v_mfma_f32_16x16x32_f16 v[42:45], v[50:53], v[96:99], v[42:45]
	v_mfma_f32_16x16x32_f16 v[18:21], v[62:65], v[96:99], v[18:21]
	s_setprio 0
	ds_read_b128 v[50:53], v177
	ds_read_b128 v[62:65], v177 offset:8448
	s_setprio 1
	s_waitcnt vmcnt(3) lgkmcnt(1)
	v_mfma_f32_16x16x32_f16 v[76:79], v[50:53], v[46:49], v[76:79]
	s_waitcnt lgkmcnt(0)
	v_mfma_f32_16x16x32_f16 v[10:13], v[62:65], v[46:49], v[10:13]
	s_waitcnt vmcnt(2)
	v_mfma_f32_16x16x32_f16 v[22:25], v[50:53], v[54:57], v[22:25]
	v_mfma_f32_16x16x32_f16 v[34:37], v[62:65], v[54:57], v[34:37]
	s_waitcnt vmcnt(1)
	v_mfma_f32_16x16x32_f16 v[38:41], v[50:53], v[68:71], v[38:41]
	v_mfma_f32_16x16x32_f16 v[14:17], v[62:65], v[68:71], v[14:17]
	s_waitcnt vmcnt(0)
	v_mfma_f32_16x16x32_f16 v[42:45], v[50:53], v[72:75], v[42:45]
	v_mfma_f32_16x16x32_f16 v[18:21], v[62:65], v[72:75], v[18:21]
	s_setprio 0
	v_add_co_u32_e32 v108, vcc, s29, v152
	v_and_b32_e32 v67, 0x1c0, v0
	s_nop 0
	v_addc_co_u32_e32 v109, vcc, 0, v153, vcc
	v_add_co_u32_e32 v46, vcc, s52, v152
	s_movk_i32 s4, 0x50
	s_nop 0
	v_addc_co_u32_e32 v47, vcc, 0, v153, vcc
	v_add_co_u32_e32 v68, vcc, s33, v152
	v_or_b32_e32 v116, 16, v67
	s_nop 0
	v_addc_co_u32_e32 v69, vcc, 0, v153, vcc
	v_add_co_u32_e32 v110, vcc, s52, v154
	global_load_dwordx4 v[46:49], v[46:47], off
	s_nop 0
	global_load_dwordx4 v[50:53], v[68:69], off
	global_load_dwordx4 v[54:57], v[152:153], off
	global_load_dwordx4 v[62:65], v[154:155], off
	v_addc_co_u32_e32 v111, vcc, 0, v155, vcc
	v_add_co_u32_e32 v112, vcc, s52, v160
	global_load_dwordx4 v[68:71], v[156:157], off
	global_load_dwordx4 v[72:75], v[158:159], off
	global_load_dwordx4 v[84:87], v[160:161], off
	global_load_dwordx4 v[88:91], v[162:163], off
	v_addc_co_u32_e32 v113, vcc, 0, v161, vcc
	global_load_dwordx4 v[92:95], v[110:111], off
	global_load_dwordx4 v[96:99], v[112:113], off
	global_load_dwordx4 v[100:103], v[108:109], off
	global_load_dwordx4 v[104:107], v[164:165], off
	s_nop 0
	global_store_dwordx4 v[166:167], v[2:5], off sc0 sc1
	global_store_dwordx4 v[168:169], v[6:9], off sc0 sc1
	global_store_dwordx4 v[170:171], v[26:29], off sc0 sc1
	global_store_dwordx4 v[58:59], v[30:33], off sc0 sc1
	v_and_b32_e32 v4, 0x1cf, v0
	v_cvt_pk_f16_f32 v3, v78, v79
	v_cvt_pk_f16_f32 v2, v76, v77
	v_mad_u32_u24 v4, v4, s4, v80
	v_or_b32_e32 v5, v116, v81
	v_or_b32_e32 v117, 32, v67
	ds_write_b64 v4, v[2:3]
	v_cvt_pk_f16_f32 v3, v24, v25
	v_cvt_pk_f16_f32 v2, v22, v23
	v_mad_u32_u24 v5, v5, s4, v80
	v_or_b32_e32 v6, v117, v81
	v_or_b32_e32 v118, 48, v67
	ds_write_b64 v5, v[2:3]
	v_cvt_pk_f16_f32 v3, v40, v41
	v_cvt_pk_f16_f32 v2, v38, v39
	v_mad_u32_u24 v6, v6, s4, v80
	v_or_b32_e32 v7, v118, v81
	ds_write_b64 v6, v[2:3]
	v_cvt_pk_f16_f32 v3, v44, v45
	v_cvt_pk_f16_f32 v2, v42, v43
	v_mad_u32_u24 v7, v7, s4, v80
	ds_write_b64 v7, v[2:3]
	v_cvt_pk_f16_f32 v3, v12, v13
	v_cvt_pk_f16_f32 v2, v10, v11
	ds_write_b64 v4, v[2:3] offset:32
	v_cvt_pk_f16_f32 v3, v36, v37
	v_cvt_pk_f16_f32 v2, v34, v35
	ds_write_b64 v5, v[2:3] offset:32
	v_cvt_pk_f16_f32 v3, v16, v17
	v_cvt_pk_f16_f32 v2, v14, v15
	v_lshl_add_u64 v[10:11], v[60:61], 0, s[14:15]
	ds_write_b64 v6, v[2:3] offset:32
	v_cvt_pk_f16_f32 v2, v18, v19
	v_add_co_u32_e32 v18, vcc, s52, v10
	v_cvt_pk_f16_f32 v3, v20, v21
	v_lshl_add_u64 v[12:13], v[60:61], 0, s[16:17]
	v_addc_co_u32_e32 v19, vcc, 0, v11, vcc
	ds_write_b64 v7, v[2:3] offset:32
	s_waitcnt lgkmcnt(0)
	s_barrier
	global_load_dwordx4 v[2:5], v[10:11], off
	global_load_dwordx4 v[6:9], v[12:13], off
	v_lshl_add_u64 v[20:21], v[60:61], 0, s[12:13]
	global_load_dwordx4 v[10:13], v[18:19], off
	global_load_dwordx4 v[14:17], v[20:21], off
	ds_read_b128 v[18:21], v1
	ds_read_b128 v[22:25], v1 offset:8448
	s_mov_b32 s3, s27
	s_setprio 1
	s_waitcnt vmcnt(17) lgkmcnt(1)
	v_mfma_f32_16x16x32_f16 v[26:29], v[18:21], v[54:57], 0
	s_waitcnt lgkmcnt(0)
	v_mfma_f32_16x16x32_f16 v[30:33], v[22:25], v[54:57], 0
	s_waitcnt vmcnt(9)
	v_mfma_f32_16x16x32_f16 v[34:37], v[18:21], v[100:103], 0
	v_mfma_f32_16x16x32_f16 v[38:41], v[22:25], v[100:103], 0
	v_mfma_f32_16x16x32_f16 v[42:45], v[18:21], v[46:49], 0
	v_mfma_f32_16x16x32_f16 v[46:49], v[22:25], v[46:49], 0
	v_mfma_f32_16x16x32_f16 v[18:21], v[18:21], v[50:53], 0
	v_mfma_f32_16x16x32_f16 v[22:25], v[22:25], v[50:53], 0
	s_setprio 0
	v_lshl_add_u64 v[58:59], v[60:61], 0, s[10:11]
	v_add_co_u32_e32 v76, vcc, s29, v58
	s_nop 1
	v_addc_co_u32_e32 v77, vcc, 0, v59, vcc
	v_add_co_u32_e32 v108, vcc, s52, v58
	global_load_dwordx4 v[50:53], v[58:59], off
	global_load_dwordx4 v[54:57], v[76:77], off
	v_addc_co_u32_e32 v109, vcc, 0, v59, vcc
	v_add_co_u32_e32 v58, vcc, s33, v58
	s_nop 1
	v_addc_co_u32_e32 v59, vcc, 0, v59, vcc
	global_load_dwordx4 v[76:79], v[108:109], off
	global_load_dwordx4 v[100:103], v[58:59], off
	ds_read_b128 v[108:111], v82
	ds_read_b128 v[112:115], v82 offset:8448
	s_setprio 1
	s_waitcnt lgkmcnt(1)
	v_mfma_f32_16x16x32_f16 v[26:29], v[108:111], v[62:65], v[26:29]
	s_waitcnt lgkmcnt(0)
	v_mfma_f32_16x16x32_f16 v[30:33], v[112:115], v[62:65], v[30:33]
	v_mfma_f32_16x16x32_f16 v[34:37], v[108:111], v[68:71], v[34:37]
	v_mfma_f32_16x16x32_f16 v[38:41], v[112:115], v[68:71], v[38:41]
	v_mfma_f32_16x16x32_f16 v[42:45], v[108:111], v[92:95], v[42:45]
	v_mfma_f32_16x16x32_f16 v[46:49], v[112:115], v[92:95], v[46:49]
	v_mfma_f32_16x16x32_f16 v[18:21], v[108:111], v[72:75], v[18:21]
	v_mfma_f32_16x16x32_f16 v[22:25], v[112:115], v[72:75], v[22:25]
	s_setprio 0
	v_lshl_add_u64 v[58:59], v[60:61], 0, s[48:49]
	v_lshl_add_u64 v[72:73], v[60:61], 0, s[50:51]
	global_load_dwordx4 v[62:65], v[58:59], off
	global_load_dwordx4 v[68:71], v[72:73], off
	v_add_co_u32_e32 v58, vcc, s52, v58
	v_lshl_add_u64 v[82:83], v[60:61], 0, s[46:47]
	s_nop 0
	v_addc_co_u32_e32 v59, vcc, 0, v59, vcc
	global_load_dwordx4 v[72:75], v[58:59], off
	global_load_dwordx4 v[92:95], v[82:83], off
	ds_read_b128 v[108:111], v172
	ds_read_b128 v[112:115], v172 offset:8448
	s_setprio 1
	s_waitcnt lgkmcnt(1)
	v_mfma_f32_16x16x32_f16 v[26:29], v[108:111], v[84:87], v[26:29]
	s_waitcnt lgkmcnt(0)
	v_mfma_f32_16x16x32_f16 v[30:33], v[112:115], v[84:87], v[30:33]
	v_mfma_f32_16x16x32_f16 v[34:37], v[108:111], v[88:91], v[34:37]
	v_mfma_f32_16x16x32_f16 v[38:41], v[112:115], v[88:91], v[38:41]
	v_mfma_f32_16x16x32_f16 v[42:45], v[108:111], v[96:99], v[42:45]
	v_mfma_f32_16x16x32_f16 v[46:49], v[112:115], v[96:99], v[46:49]
	s_waitcnt vmcnt(16)
	v_mfma_f32_16x16x32_f16 v[18:21], v[108:111], v[104:107], v[18:21]
	v_mfma_f32_16x16x32_f16 v[22:25], v[112:115], v[104:107], v[22:25]
	s_setprio 0
	v_lshl_add_u64 v[58:59], v[60:61], 0, s[42:43]
	v_lshl_add_u64 v[90:91], v[60:61], 0, s[44:45]
	global_load_dwordx4 v[82:85], v[58:59], off
	global_load_dwordx4 v[86:89], v[90:91], off
	v_add_co_u32_e32 v58, vcc, s52, v58
	v_lshl_add_u64 v[90:91], v[60:61], 0, s[40:41]
	s_nop 0
	v_addc_co_u32_e32 v59, vcc, 0, v59, vcc
	global_load_dwordx4 v[96:99], v[58:59], off
	global_load_dwordx4 v[104:107], v[90:91], off
	ds_read_b128 v[108:111], v173
	ds_read_b128 v[112:115], v173 offset:8448
	s_setprio 1
	s_waitcnt vmcnt(15) lgkmcnt(1)
	v_mfma_f32_16x16x32_f16 v[26:29], v[108:111], v[2:5], v[26:29]
	s_waitcnt lgkmcnt(0)
	v_mfma_f32_16x16x32_f16 v[2:5], v[112:115], v[2:5], v[30:33]
	s_waitcnt vmcnt(14)
	v_mfma_f32_16x16x32_f16 v[30:33], v[108:111], v[6:9], v[34:37]
	v_mfma_f32_16x16x32_f16 v[6:9], v[112:115], v[6:9], v[38:41]
	s_waitcnt vmcnt(13)
	v_mfma_f32_16x16x32_f16 v[34:37], v[108:111], v[10:13], v[42:45]
	v_mfma_f32_16x16x32_f16 v[10:13], v[112:115], v[10:13], v[46:49]
	s_waitcnt vmcnt(12)
	v_mfma_f32_16x16x32_f16 v[18:21], v[108:111], v[14:17], v[18:21]
	v_mfma_f32_16x16x32_f16 v[14:17], v[112:115], v[14:17], v[22:25]
	s_setprio 0
	v_lshl_add_u64 v[42:43], v[60:61], 0, s[8:9]
	v_add_co_u32_e32 v58, vcc, s52, v42
	v_lshl_add_u64 v[44:45], v[60:61], 0, s[38:39]
	s_nop 0
	v_addc_co_u32_e32 v59, vcc, 0, v43, vcc
	global_load_dwordx4 v[22:25], v[42:43], off
	global_load_dwordx4 v[38:41], v[44:45], off
	v_lshl_add_u64 v[60:61], v[60:61], 0, s[6:7]
	global_load_dwordx4 v[42:45], v[58:59], off
	global_load_dwordx4 v[46:49], v[60:61], off
	ds_read_b128 v[58:61], v174
	ds_read_b128 v[108:111], v174 offset:8448
	s_setprio 1
	s_waitcnt vmcnt(15) lgkmcnt(1)
	v_mfma_f32_16x16x32_f16 v[26:29], v[58:61], v[50:53], v[26:29]
	s_waitcnt lgkmcnt(0)
	v_mfma_f32_16x16x32_f16 v[2:5], v[108:111], v[50:53], v[2:5]
	s_waitcnt vmcnt(14)
	v_mfma_f32_16x16x32_f16 v[30:33], v[58:61], v[54:57], v[30:33]
	v_mfma_f32_16x16x32_f16 v[6:9], v[108:111], v[54:57], v[6:9]
	s_waitcnt vmcnt(13)
	v_mfma_f32_16x16x32_f16 v[34:37], v[58:61], v[76:79], v[34:37]
	v_mfma_f32_16x16x32_f16 v[10:13], v[108:111], v[76:79], v[10:13]
	s_waitcnt vmcnt(12)
	v_mfma_f32_16x16x32_f16 v[18:21], v[58:61], v[100:103], v[18:21]
	v_mfma_f32_16x16x32_f16 v[14:17], v[108:111], v[100:103], v[14:17]
	s_setprio 0
	ds_read_b128 v[50:53], v175
	ds_read_b128 v[54:57], v175 offset:8448
	s_setprio 1
	s_waitcnt vmcnt(11) lgkmcnt(1)
	v_mfma_f32_16x16x32_f16 v[26:29], v[50:53], v[62:65], v[26:29]
	s_waitcnt lgkmcnt(0)
	v_mfma_f32_16x16x32_f16 v[2:5], v[54:57], v[62:65], v[2:5]
	s_waitcnt vmcnt(10)
	v_mfma_f32_16x16x32_f16 v[30:33], v[50:53], v[68:71], v[30:33]
	v_mfma_f32_16x16x32_f16 v[6:9], v[54:57], v[68:71], v[6:9]
	s_waitcnt vmcnt(9)
	v_mfma_f32_16x16x32_f16 v[34:37], v[50:53], v[72:75], v[34:37]
	v_mfma_f32_16x16x32_f16 v[10:13], v[54:57], v[72:75], v[10:13]
	s_waitcnt vmcnt(8)
	v_mfma_f32_16x16x32_f16 v[18:21], v[50:53], v[92:95], v[18:21]
	v_mfma_f32_16x16x32_f16 v[14:17], v[54:57], v[92:95], v[14:17]
	s_setprio 0
	ds_read_b128 v[50:53], v176
	ds_read_b128 v[54:57], v176 offset:8448
	s_setprio 1
	s_waitcnt vmcnt(7) lgkmcnt(1)
	v_mfma_f32_16x16x32_f16 v[26:29], v[50:53], v[82:85], v[26:29]
	s_waitcnt lgkmcnt(0)
	v_mfma_f32_16x16x32_f16 v[2:5], v[54:57], v[82:85], v[2:5]
	s_waitcnt vmcnt(6)
	v_mfma_f32_16x16x32_f16 v[30:33], v[50:53], v[86:89], v[30:33]
	v_mfma_f32_16x16x32_f16 v[6:9], v[54:57], v[86:89], v[6:9]
	s_waitcnt vmcnt(5)
	v_mfma_f32_16x16x32_f16 v[34:37], v[50:53], v[96:99], v[34:37]
	v_mfma_f32_16x16x32_f16 v[58:61], v[54:57], v[96:99], v[10:13]
	s_waitcnt vmcnt(4)
	v_mfma_f32_16x16x32_f16 v[18:21], v[50:53], v[104:107], v[18:21]
	v_mfma_f32_16x16x32_f16 v[50:53], v[54:57], v[104:107], v[14:17]
	s_setprio 0
	ds_read_b128 v[54:57], v177
	ds_read_b128 v[62:65], v177 offset:8448
	s_setprio 1
	s_waitcnt vmcnt(3) lgkmcnt(1)
	v_mfma_f32_16x16x32_f16 v[26:29], v[54:57], v[22:25], v[26:29]
	s_waitcnt lgkmcnt(0)
	v_mfma_f32_16x16x32_f16 v[14:17], v[62:65], v[22:25], v[2:5]
	s_waitcnt vmcnt(2)
	v_mfma_f32_16x16x32_f16 v[22:25], v[54:57], v[38:41], v[30:33]
	v_mfma_f32_16x16x32_f16 v[10:13], v[62:65], v[38:41], v[6:9]
	s_waitcnt vmcnt(1)
	v_mfma_f32_16x16x32_f16 v[30:33], v[54:57], v[42:45], v[34:37]
	v_mfma_f32_16x16x32_f16 v[6:9], v[62:65], v[42:45], v[58:61]
	s_waitcnt vmcnt(0)
	v_mfma_f32_16x16x32_f16 v[34:37], v[54:57], v[46:49], v[18:21]
	v_mfma_f32_16x16x32_f16 v[2:5], v[62:65], v[46:49], v[50:53]
	s_setprio 0
	s_nop 1
	v_mul_u32_u24_e32 v52, 0x50, v0
	ds_read_b128 v[18:21], v52
	s_lshl_b64 s[2:3], s[2:3], 15
	v_or_b32_e32 v0, s2, v66
	v_mov_b32_e32 v1, s3
	v_lshl_add_u64 v[50:51], s[24:25], 0, v[0:1]
	ds_read_b128 v[38:41], v52 offset:16
	ds_read_b128 v[42:45], v52 offset:32
	ds_read_b128 v[46:49], v52 offset:48
	s_waitcnt lgkmcnt(3)
	global_store_dwordx4 v[50:51], v[18:21], off sc0 sc1
	s_nop 1
	v_add_co_u32_e32 v18, vcc, s29, v50
	s_nop 1
	v_addc_co_u32_e32 v19, vcc, 0, v51, vcc
	s_waitcnt lgkmcnt(2)
	global_store_dwordx4 v[18:19], v[38:41], off sc0 sc1
	v_or_b32_e32 v18, 0x4000, v0
	v_mov_b32_e32 v19, s3
	v_lshl_add_u64 v[20:21], s[24:25], 0, v[18:19]
	s_waitcnt lgkmcnt(1)
	global_store_dwordx4 v[20:21], v[42:45], off sc0 sc1
	v_mul_f32_e32 v20, 0xbfb8aa3b, v26
	v_exp_f32_e32 v38, v20
	v_add_co_u32_e32 v20, vcc, s33, v50
	v_or_b32_e32 v39, 0x200, v81
	s_nop 0
	v_addc_co_u32_e32 v21, vcc, 0, v51, vcc
	s_waitcnt lgkmcnt(0)
	global_store_dwordx4 v[20:21], v[46:49], off sc0 sc1
	v_add_f32_e32 v20, 1.0, v38
	v_rcp_f32_e32 v20, v20
	v_mul_f32_e32 v21, 0xbfb8aa3b, v27
	v_mul_f32_e32 v38, 0xbfb8aa3b, v28
	v_exp_f32_e32 v21, v21
	v_exp_f32_e32 v38, v38
	v_fma_mixlo_f16 v40, v26, v20, 0
	v_mul_f32_e32 v26, 0xbfb8aa3b, v29
	v_add_f32_e32 v20, 1.0, v21
	v_add_f32_e32 v21, 1.0, v38
	v_exp_f32_e32 v38, v26
	v_rcp_f32_e32 v20, v20
	v_rcp_f32_e32 v21, v21
	v_mov_b32_e32 v26, v27
	v_mov_b32_e32 v27, v28
	v_add_f32_e32 v28, 1.0, v38
	v_rcp_f32_e32 v28, v28
	v_pk_mul_f32 v[20:21], v[26:27], v[20:21]
	v_or_b32_e32 v27, v39, v67
	v_cvt_pk_f16_f32 v21, v20, v21
	v_fma_mixlo_f16 v26, v29, v28, 0
	v_pack_b32_f16 v20, v40, v21
	v_alignbit_b32 v21, v26, v21, 16
	v_mul_f32_e32 v26, 0xbfb8aa3b, v22
	v_exp_f32_e32 v26, v26
	v_mad_u32_u24 v27, v27, s4, v80
	ds_write_b64 v27, v[20:21]
	v_mul_f32_e32 v21, 0xbfb8aa3b, v23
	v_add_f32_e32 v20, 1.0, v26
	v_rcp_f32_e32 v20, v20
	v_mul_f32_e32 v26, 0xbfb8aa3b, v24
	v_exp_f32_e32 v21, v21
	v_exp_f32_e32 v26, v26
	v_fma_mixlo_f16 v28, v22, v20, 0
	v_mul_f32_e32 v22, 0xbfb8aa3b, v25
	v_add_f32_e32 v20, 1.0, v21
	v_add_f32_e32 v21, 1.0, v26
	v_exp_f32_e32 v26, v22
	v_rcp_f32_e32 v20, v20
	v_rcp_f32_e32 v21, v21
	v_mov_b32_e32 v22, v23
	v_mov_b32_e32 v23, v24
	v_add_f32_e32 v24, 1.0, v26
	v_rcp_f32_e32 v24, v24
	v_pk_mul_f32 v[20:21], v[22:23], v[20:21]
	v_or_b32_e32 v23, v116, v39
	v_cvt_pk_f16_f32 v21, v20, v21
	v_fma_mixlo_f16 v22, v25, v24, 0
	v_pack_b32_f16 v20, v28, v21
	v_alignbit_b32 v21, v22, v21, 16
	v_mul_f32_e32 v22, 0xbfb8aa3b, v30
	v_exp_f32_e32 v22, v22
	v_mad_u32_u24 v24, v23, s4, v80
	ds_write_b64 v24, v[20:21]
	v_mul_f32_e32 v21, 0xbfb8aa3b, v31
	v_add_f32_e32 v20, 1.0, v22
	v_mul_f32_e32 v22, 0xbfb8aa3b, v32
	v_rcp_f32_e32 v20, v20
	v_exp_f32_e32 v21, v21
	v_exp_f32_e32 v22, v22
	v_mov_b32_e32 v23, v32
	v_fma_mixlo_f16 v25, v30, v20, 0
	v_add_f32_e32 v20, 1.0, v21
	v_add_f32_e32 v21, 1.0, v22
	v_mul_f32_e32 v22, 0xbfb8aa3b, v33
	v_exp_f32_e32 v26, v22
	v_rcp_f32_e32 v20, v20
	v_rcp_f32_e32 v21, v21
	v_mov_b32_e32 v22, v31
	v_add_f32_e32 v26, 1.0, v26
	v_rcp_f32_e32 v26, v26
	v_pk_mul_f32 v[20:21], v[22:23], v[20:21]
	v_or_b32_e32 v23, v117, v39
	v_cvt_pk_f16_f32 v21, v20, v21
	v_fma_mixlo_f16 v22, v33, v26, 0
	v_pack_b32_f16 v20, v25, v21
	v_alignbit_b32 v21, v22, v21, 16
	v_mul_f32_e32 v22, 0xbfb8aa3b, v34
	v_exp_f32_e32 v22, v22
	v_mad_u32_u24 v25, v23, s4, v80
	ds_write_b64 v25, v[20:21]
	v_mul_f32_e32 v21, 0xbfb8aa3b, v35
	v_add_f32_e32 v20, 1.0, v22
	v_mul_f32_e32 v22, 0xbfb8aa3b, v36
	v_rcp_f32_e32 v20, v20
	v_exp_f32_e32 v21, v21
	v_exp_f32_e32 v22, v22
	v_mov_b32_e32 v23, v36
	v_fma_mixlo_f16 v26, v34, v20, 0
	v_add_f32_e32 v20, 1.0, v21
	v_add_f32_e32 v21, 1.0, v22
	v_mul_f32_e32 v22, 0xbfb8aa3b, v37
	v_exp_f32_e32 v28, v22
	v_rcp_f32_e32 v20, v20
	v_rcp_f32_e32 v21, v21
	v_mov_b32_e32 v22, v35
	v_add_f32_e32 v28, 1.0, v28
	v_rcp_f32_e32 v28, v28
	v_pk_mul_f32 v[20:21], v[22:23], v[20:21]
	v_or_b32_e32 v23, v118, v39
	v_cvt_pk_f16_f32 v21, v20, v21
	v_fma_mixlo_f16 v22, v37, v28, 0
	v_pack_b32_f16 v20, v26, v21
	v_alignbit_b32 v21, v22, v21, 16
	v_mul_f32_e32 v22, 0xbfb8aa3b, v14
	v_exp_f32_e32 v22, v22
	v_mad_u32_u24 v23, v23, s4, v80
	ds_write_b64 v23, v[20:21]
	v_mul_f32_e32 v21, 0xbfb8aa3b, v15
	v_add_f32_e32 v20, 1.0, v22
	v_rcp_f32_e32 v20, v20
	v_exp_f32_e32 v21, v21
	v_mul_f32_e32 v22, 0xbfb8aa3b, v16
	v_exp_f32_e32 v22, v22
	v_fma_mixlo_f16 v26, v14, v20, 0
	v_add_f32_e32 v14, 1.0, v21
	v_rcp_f32_e32 v20, v14
	v_add_f32_e32 v14, 1.0, v22
	v_rcp_f32_e32 v21, v14
	v_mov_b32_e32 v14, v15
	v_mul_f32_e32 v15, 0xbfb8aa3b, v17
	v_exp_f32_e32 v22, v15
	v_mov_b32_e32 v15, v16
	v_pk_mul_f32 v[14:15], v[14:15], v[20:21]
	v_mul_f32_e32 v20, 0xbfb8aa3b, v10
	v_cvt_pk_f16_f32 v15, v14, v15
	v_add_f32_e32 v14, 1.0, v22
	v_rcp_f32_e32 v16, v14
	v_exp_f32_e32 v20, v20
	v_pack_b32_f16 v14, v26, v15
	v_lshl_add_u64 v[0:1], s[0:1], 0, v[0:1]
	v_fma_mixlo_f16 v16, v17, v16, 0
	v_alignbit_b32 v15, v16, v15, 16
	ds_write_b64 v27, v[14:15] offset:32
	v_add_f32_e32 v14, 1.0, v20
	v_mul_f32_e32 v15, 0xbfb8aa3b, v11
	v_rcp_f32_e32 v14, v14
	v_exp_f32_e32 v15, v15
	v_mul_f32_e32 v16, 0xbfb8aa3b, v12
	v_exp_f32_e32 v16, v16
	v_fma_mixlo_f16 v17, v10, v14, 0
	v_add_f32_e32 v10, 1.0, v15
	v_rcp_f32_e32 v14, v10
	v_add_f32_e32 v10, 1.0, v16
	v_rcp_f32_e32 v15, v10
	v_mov_b32_e32 v10, v11
	v_mul_f32_e32 v11, 0xbfb8aa3b, v13
	v_exp_f32_e32 v16, v11
	v_mov_b32_e32 v11, v12
	v_pk_mul_f32 v[10:11], v[10:11], v[14:15]
	v_mul_f32_e32 v14, 0xbfb8aa3b, v6
	v_cvt_pk_f16_f32 v11, v10, v11
	v_add_f32_e32 v10, 1.0, v16
	v_rcp_f32_e32 v12, v10
	v_exp_f32_e32 v14, v14
	v_pack_b32_f16 v10, v17, v11
	v_fma_mixlo_f16 v12, v13, v12, 0
	v_alignbit_b32 v11, v12, v11, 16
	ds_write_b64 v24, v[10:11] offset:32
	v_add_f32_e32 v10, 1.0, v14
	v_mul_f32_e32 v11, 0xbfb8aa3b, v7
	v_rcp_f32_e32 v10, v10
	v_exp_f32_e32 v11, v11
	v_mul_f32_e32 v12, 0xbfb8aa3b, v8
	v_exp_f32_e32 v12, v12
	v_fma_mixlo_f16 v13, v6, v10, 0
	v_add_f32_e32 v6, 1.0, v11
	v_rcp_f32_e32 v10, v6
	v_add_f32_e32 v6, 1.0, v12
	v_rcp_f32_e32 v11, v6
	v_mov_b32_e32 v6, v7
	v_mul_f32_e32 v7, 0xbfb8aa3b, v9
	v_exp_f32_e32 v12, v7
	v_mov_b32_e32 v7, v8
	v_pk_mul_f32 v[6:7], v[6:7], v[10:11]
	v_mul_f32_e32 v10, 0xbfb8aa3b, v2
	v_cvt_pk_f16_f32 v7, v6, v7
	v_add_f32_e32 v6, 1.0, v12
	v_rcp_f32_e32 v8, v6
	v_exp_f32_e32 v10, v10
	v_pack_b32_f16 v6, v13, v7
	v_fma_mixlo_f16 v8, v9, v8, 0
	v_alignbit_b32 v7, v8, v7, 16
	ds_write_b64 v25, v[6:7] offset:32
	v_add_f32_e32 v6, 1.0, v10
	v_mul_f32_e32 v7, 0xbfb8aa3b, v3
	v_rcp_f32_e32 v6, v6
	v_exp_f32_e32 v7, v7
	v_mul_f32_e32 v8, 0xbfb8aa3b, v4
	v_exp_f32_e32 v8, v8
	v_fma_mixlo_f16 v9, v2, v6, 0
	v_add_f32_e32 v2, 1.0, v7
	v_mul_f32_e32 v7, 0xbfb8aa3b, v5
	v_rcp_f32_e32 v6, v2
	v_add_f32_e32 v2, 1.0, v8
	v_exp_f32_e32 v8, v7
	v_rcp_f32_e32 v7, v2
	v_mov_b32_e32 v2, v3
	v_mov_b32_e32 v3, v4
	v_add_f32_e32 v4, 1.0, v8
	v_rcp_f32_e32 v4, v4
	v_pk_mul_f32 v[2:3], v[2:3], v[6:7]
	v_fma_mixlo_f16 v4, v5, v4, 0
	v_cvt_pk_f16_f32 v3, v2, v3
	v_pack_b32_f16 v2, v9, v3
	v_alignbit_b32 v3, v4, v3, 16
	ds_write_b64 v23, v[2:3] offset:32
	s_waitcnt lgkmcnt(0)
	s_barrier
	ds_read_b128 v[2:5], v52 offset:40960
	ds_read_b128 v[6:9], v52 offset:40976
	ds_read_b128 v[10:13], v52 offset:40992
	ds_read_b128 v[14:17], v52 offset:41008
	s_waitcnt lgkmcnt(3)
	global_store_dwordx4 v[0:1], v[2:5], off sc0 sc1
	s_nop 1
	v_add_co_u32_e32 v2, vcc, 0x2000, v0
	s_nop 1
	v_addc_co_u32_e32 v3, vcc, 0, v1, vcc
	v_add_co_u32_e32 v0, vcc, 0x6000, v0
	s_waitcnt lgkmcnt(2)
	global_store_dwordx4 v[2:3], v[6:9], off sc0 sc1
	v_lshl_add_u64 v[2:3], s[0:1], 0, v[18:19]
	v_addc_co_u32_e32 v1, vcc, 0, v1, vcc
	s_waitcnt lgkmcnt(1)
	global_store_dwordx4 v[2:3], v[10:13], off sc0 sc1
	s_waitcnt lgkmcnt(0)
	global_store_dwordx4 v[0:1], v[14:17], off sc0 sc1
	s_endpgm
	.p2align	8
